# v27 + removed the full lgkmcnt(0) after the barrier in all GEMM MMA phases (per-fragment waits remain)
# baseline (speedup 1.0000x reference)
.LBB0_351:
	s_add_i32 s10, s38, 0xfffc0080
	s_cmp_eq_u32 s40, 12
	s_cselect_b32 s43, s6, s10
	s_cselect_b32 s41, s7, s39
	s_add_i32 s10, 0, 0x10000
	v_add_u32_e32 v135, s10, v131
	v_add_u32_e32 v218, s10, v132
	ds_read_b128 v[136:139], v135
	ds_read_b128 v[144:147], v135 offset:2048
	ds_read_b128 v[140:143], v218
	ds_read_b128 v[148:151], v218 offset:2048
	s_or_b32 s42, s43, 0x80
	s_mov_b32 m0, s27
	ds_read_b128 v[152:155], v133
	ds_read_b128 v[168:171], v133 offset:2048
	ds_read_b128 v[156:159], v134
	ds_read_b128 v[172:175], v134 offset:2048
	ds_read_b128 v[176:179], v133 offset:4096
	ds_read_b128 v[184:187], v133 offset:6144
	ds_read_b128 v[180:183], v134 offset:4096
	ds_read_b128 v[188:191], v134 offset:6144
	buffer_load_dwordx4 v96, s[72:75], s38 offen lds
	s_mov_b32 m0, s28
	s_nop 0
	buffer_load_dwordx4 v130, s[72:75], s38 offen lds
	s_waitcnt lgkmcnt(8)
	s_barrier
	s_setprio 1
	s_waitcnt lgkmcnt(5)
	v_mfma_scale_f32_16x16x128_f8f6f4 v[126:129], v[136:143], v[152:159], v[126:129], v212, v212 op_sel_hi:[0,0,0]
	v_mfma_scale_f32_16x16x128_f8f6f4 v[122:125], v[144:151], v[152:159], v[122:125], v212, v212 op_sel_hi:[0,0,0]
	s_waitcnt lgkmcnt(4)
	v_mfma_scale_f32_16x16x128_f8f6f4 v[118:121], v[136:143], v[168:175], v[118:121], v212, v212 op_sel_hi:[0,0,0]
	v_mfma_scale_f32_16x16x128_f8f6f4 v[114:117], v[144:151], v[168:175], v[114:117], v212, v212 op_sel_hi:[0,0,0]
	s_waitcnt lgkmcnt(1)
	v_mfma_scale_f32_16x16x128_f8f6f4 v[160:163], v[136:143], v[176:183], v[102:105], v212, v212 op_sel_hi:[0,0,0]
	v_mfma_scale_f32_16x16x128_f8f6f4 v[192:195], v[144:151], v[176:183], v[98:101], v212, v212 op_sel_hi:[0,0,0]
	s_waitcnt lgkmcnt(0)
	v_mfma_scale_f32_16x16x128_f8f6f4 v[196:199], v[136:143], v[184:191], v[84:87], v212, v212 op_sel_hi:[0,0,0]
	v_mfma_scale_f32_16x16x128_f8f6f4 v[200:203], v[144:151], v[184:191], v[80:83], v212, v212 op_sel_hi:[0,0,0]
	s_setprio 0
	s_barrier
	s_mov_b32 s10, s74
	s_mov_b32 s11, s75
	s_mov_b32 m0, s13
	s_nop 1
	ds_read_b128 v[80:83], v135 offset:16384
	ds_read_b128 v[98:101], v135 offset:18432
	ds_read_b128 v[84:87], v218 offset:16384
	ds_read_b128 v[102:105], v218 offset:18432
	buffer_load_dwordx4 v96, s[8:11], s41 offen lds
	s_mov_b32 m0, s14
	s_nop 0
	buffer_load_dwordx4 v130, s[8:11], s41 offen lds
	s_barrier
	s_setprio 1
	s_waitcnt lgkmcnt(1)
	v_mfma_scale_f32_16x16x128_f8f6f4 v[204:207], v[80:87], v[152:159], v[110:113], v212, v212 op_sel_hi:[0,0,0]
	s_waitcnt lgkmcnt(0)
	v_mfma_scale_f32_16x16x128_f8f6f4 v[152:155], v[98:105], v[152:159], v[106:109], v212, v212 op_sel_hi:[0,0,0]
	v_mfma_scale_f32_16x16x128_f8f6f4 v[156:159], v[80:87], v[168:175], v[92:95], v212, v212 op_sel_hi:[0,0,0]
	v_mfma_scale_f32_16x16x128_f8f6f4 v[168:171], v[98:105], v[168:175], v[88:91], v212, v212 op_sel_hi:[0,0,0]
	v_mfma_scale_f32_16x16x128_f8f6f4 v[172:175], v[80:87], v[176:183], v[76:79], v212, v212 op_sel_hi:[0,0,0]
	v_mfma_scale_f32_16x16x128_f8f6f4 v[176:179], v[98:105], v[176:183], v[72:75], v212, v212 op_sel_hi:[0,0,0]
	v_mfma_scale_f32_16x16x128_f8f6f4 v[180:183], v[80:87], v[184:191], v[68:71], v212, v212 op_sel_hi:[0,0,0]
	v_mfma_scale_f32_16x16x128_f8f6f4 v[184:187], v[98:105], v[184:191], v[16:19], v212, v212 op_sel_hi:[0,0,0]
	s_setprio 0
	s_mov_b32 m0, s12
	s_barrier
	ds_read_b128 v[64:67], v133 offset:16384
	s_nop 0
	ds_read_b128 v[72:75], v133 offset:18432
	ds_read_b128 v[68:71], v134 offset:16384
	ds_read_b128 v[76:79], v134 offset:18432
	ds_read_b128 v[88:91], v133 offset:20480
	ds_read_b128 v[106:109], v133 offset:22528
	ds_read_b128 v[92:95], v134 offset:20480
	ds_read_b128 v[110:113], v134 offset:22528
	buffer_load_dwordx4 v96, s[72:75], s43 offen lds
	s_mov_b32 m0, s15
	s_nop 0
	buffer_load_dwordx4 v130, s[72:75], s43 offen lds
	s_barrier
	s_setprio 1
	s_waitcnt lgkmcnt(5)
	v_mfma_scale_f32_16x16x128_f8f6f4 v[60:63], v[136:143], v[64:71], v[60:63], v212, v212 op_sel_hi:[0,0,0]
	v_mfma_scale_f32_16x16x128_f8f6f4 v[56:59], v[144:151], v[64:71], v[56:59], v212, v212 op_sel_hi:[0,0,0]
	s_waitcnt lgkmcnt(4)
	v_mfma_scale_f32_16x16x128_f8f6f4 v[52:55], v[136:143], v[72:79], v[52:55], v212, v212 op_sel_hi:[0,0,0]
	v_mfma_scale_f32_16x16x128_f8f6f4 v[228:231], v[144:151], v[72:79], v[44:47], v212, v212 op_sel_hi:[0,0,0]
	s_waitcnt lgkmcnt(1)
	v_mfma_scale_f32_16x16x128_f8f6f4 v[232:235], v[136:143], v[88:95], v[36:39], v212, v212 op_sel_hi:[0,0,0]
	v_mfma_scale_f32_16x16x128_f8f6f4 v[236:239], v[144:151], v[88:95], v[28:31], v212, v212 op_sel_hi:[0,0,0]
	s_waitcnt lgkmcnt(0)
	v_mfma_scale_f32_16x16x128_f8f6f4 v[240:243], v[136:143], v[106:113], v[20:23], v212, v212 op_sel_hi:[0,0,0]
	v_mfma_scale_f32_16x16x128_f8f6f4 v[244:247], v[144:151], v[106:113], v[12:15], v212, v212 op_sel_hi:[0,0,0]
	s_setprio 0
	s_barrier
	s_add_i32 s44, s41, 0x40000
	s_mov_b32 m0, s16
	s_nop 0
	buffer_load_dwordx4 v96, s[8:11], s44 offen lds
	s_mov_b32 m0, s17
	s_nop 0
	buffer_load_dwordx4 v130, s[8:11], s44 offen lds
	s_waitcnt vmcnt(6)
	s_barrier
	s_setprio 1
	v_mfma_scale_f32_16x16x128_f8f6f4 v[48:51], v[80:87], v[64:71], v[48:51], v212, v212 op_sel_hi:[0,0,0]
	v_mfma_scale_f32_16x16x128_f8f6f4 v[208:211], v[80:87], v[88:95], v[208:211], v212, v212 op_sel_hi:[0,0,0]
	v_mfma_scale_f32_16x16x128_f8f6f4 v[248:251], v[98:105], v[64:71], v[40:43], v212, v212 op_sel_hi:[0,0,0]
	v_mfma_scale_f32_16x16x128_f8f6f4 v[164:167], v[80:87], v[72:79], v[32:35], v212, v212 op_sel_hi:[0,0,0]
	v_mfma_scale_f32_16x16x128_f8f6f4 v[224:227], v[98:105], v[72:79], v[24:27], v212, v212 op_sel_hi:[0,0,0]
	v_mfma_scale_f32_16x16x128_f8f6f4 v[214:217], v[98:105], v[88:95], v[8:11], v212, v212 op_sel_hi:[0,0,0]
	v_mfma_scale_f32_16x16x128_f8f6f4 v[220:223], v[80:87], v[106:113], v[4:7], v212, v212 op_sel_hi:[0,0,0]
	v_mfma_scale_f32_16x16x128_f8f6f4 v[64:67], v[98:105], v[106:113], v[0:3], v212, v212 op_sel_hi:[0,0,0]
	s_setprio 0
	s_barrier
	s_nop 4
	ds_read_b128 v[0:3], v135 offset:32768
	ds_read_b128 v[8:11], v135 offset:34816
	ds_read_b128 v[4:7], v218 offset:32768
	ds_read_b128 v[12:15], v218 offset:34816
	s_add_i32 s43, s43, 0x40000
	s_mov_b32 m0, s18
	ds_read_b128 v[16:19], v133 offset:32768
	ds_read_b128 v[24:27], v133 offset:34816
	ds_read_b128 v[20:23], v134 offset:32768
	ds_read_b128 v[28:31], v134 offset:34816
	ds_read_b128 v[32:35], v133 offset:36864
	ds_read_b128 v[40:43], v133 offset:38912
	ds_read_b128 v[36:39], v134 offset:36864
	ds_read_b128 v[44:47], v134 offset:38912
	buffer_load_dwordx4 v96, s[72:75], s43 offen lds
	s_mov_b32 m0, s19
	s_nop 0
	buffer_load_dwordx4 v130, s[72:75], s43 offen lds
	s_waitcnt lgkmcnt(8)
	s_barrier
	s_setprio 1
	s_waitcnt lgkmcnt(5)
	v_mfma_scale_f32_16x16x128_f8f6f4 v[126:129], v[0:7], v[16:23], v[126:129], v212, v212 op_sel_hi:[0,0,0]
	v_mfma_scale_f32_16x16x128_f8f6f4 v[122:125], v[8:15], v[16:23], v[122:125], v212, v212 op_sel_hi:[0,0,0]
	s_waitcnt lgkmcnt(4)
	v_mfma_scale_f32_16x16x128_f8f6f4 v[118:121], v[0:7], v[24:31], v[118:121], v212, v212 op_sel_hi:[0,0,0]
	v_mfma_scale_f32_16x16x128_f8f6f4 v[114:117], v[8:15], v[24:31], v[114:117], v212, v212 op_sel_hi:[0,0,0]
	s_waitcnt lgkmcnt(1)
	v_mfma_scale_f32_16x16x128_f8f6f4 v[102:105], v[0:7], v[32:39], v[160:163], v212, v212 op_sel_hi:[0,0,0]
	v_mfma_scale_f32_16x16x128_f8f6f4 v[98:101], v[8:15], v[32:39], v[192:195], v212, v212 op_sel_hi:[0,0,0]
	s_waitcnt lgkmcnt(0)
	v_mfma_scale_f32_16x16x128_f8f6f4 v[84:87], v[0:7], v[40:47], v[196:199], v212, v212 op_sel_hi:[0,0,0]
	v_mfma_scale_f32_16x16x128_f8f6f4 v[80:83], v[8:15], v[40:47], v[200:203], v212, v212 op_sel_hi:[0,0,0]
	s_setprio 0
	s_barrier
	s_or_b32 s43, s41, 0x80
	s_mov_b32 m0, s22
	ds_read_b128 v[136:139], v135 offset:49152
	ds_read_b128 v[144:147], v135 offset:51200
	ds_read_b128 v[140:143], v218 offset:49152
	ds_read_b128 v[148:151], v218 offset:51200
	buffer_load_dwordx4 v96, s[8:11], s43 offen lds
	s_mov_b32 m0, s2
	s_nop 0
	buffer_load_dwordx4 v130, s[8:11], s43 offen lds
	s_barrier
	s_setprio 1
	s_waitcnt lgkmcnt(1)
	v_mfma_scale_f32_16x16x128_f8f6f4 v[110:113], v[136:143], v[16:23], v[204:207], v212, v212 op_sel_hi:[0,0,0]
	s_waitcnt lgkmcnt(0)
	v_mfma_scale_f32_16x16x128_f8f6f4 v[106:109], v[144:151], v[16:23], v[152:155], v212, v212 op_sel_hi:[0,0,0]
	v_mfma_scale_f32_16x16x128_f8f6f4 v[92:95], v[136:143], v[24:31], v[156:159], v212, v212 op_sel_hi:[0,0,0]
	v_mfma_scale_f32_16x16x128_f8f6f4 v[88:91], v[144:151], v[24:31], v[168:171], v212, v212 op_sel_hi:[0,0,0]
	v_mfma_scale_f32_16x16x128_f8f6f4 v[76:79], v[136:143], v[32:39], v[172:175], v212, v212 op_sel_hi:[0,0,0]
	v_mfma_scale_f32_16x16x128_f8f6f4 v[72:75], v[144:151], v[32:39], v[176:179], v212, v212 op_sel_hi:[0,0,0]
	v_mfma_scale_f32_16x16x128_f8f6f4 v[68:71], v[136:143], v[40:47], v[180:183], v212, v212 op_sel_hi:[0,0,0]
	v_mfma_scale_f32_16x16x128_f8f6f4 v[16:19], v[144:151], v[40:47], v[184:187], v212, v212 op_sel_hi:[0,0,0]
	s_setprio 0
	s_mov_b32 m0, s23
	s_barrier
	ds_read_b128 v[152:155], v133 offset:49152
	ds_read_b128 v[168:171], v133 offset:51200
	ds_read_b128 v[156:159], v134 offset:49152
	ds_read_b128 v[172:175], v134 offset:51200
	ds_read_b128 v[176:179], v133 offset:53248
	ds_read_b128 v[184:187], v133 offset:55296
	ds_read_b128 v[180:183], v134 offset:53248
	ds_read_b128 v[188:191], v134 offset:55296
	buffer_load_dwordx4 v96, s[72:75], s42 offen lds
	s_mov_b32 m0, s24
	s_nop 0
	buffer_load_dwordx4 v130, s[72:75], s42 offen lds
	s_barrier
	s_setprio 1
	s_waitcnt lgkmcnt(5)
	v_mfma_scale_f32_16x16x128_f8f6f4 v[60:63], v[0:7], v[152:159], v[60:63], v212, v212 op_sel_hi:[0,0,0]
	v_mfma_scale_f32_16x16x128_f8f6f4 v[56:59], v[8:15], v[152:159], v[56:59], v212, v212 op_sel_hi:[0,0,0]
	s_waitcnt lgkmcnt(4)
	v_mfma_scale_f32_16x16x128_f8f6f4 v[52:55], v[0:7], v[168:175], v[52:55], v212, v212 op_sel_hi:[0,0,0]
	v_mfma_scale_f32_16x16x128_f8f6f4 v[44:47], v[8:15], v[168:175], v[228:231], v212, v212 op_sel_hi:[0,0,0]
	s_waitcnt lgkmcnt(1)
	v_mfma_scale_f32_16x16x128_f8f6f4 v[36:39], v[0:7], v[176:183], v[232:235], v212, v212 op_sel_hi:[0,0,0]
	v_mfma_scale_f32_16x16x128_f8f6f4 v[28:31], v[8:15], v[176:183], v[236:239], v212, v212 op_sel_hi:[0,0,0]
	s_waitcnt lgkmcnt(0)
	v_mfma_scale_f32_16x16x128_f8f6f4 v[20:23], v[0:7], v[184:191], v[240:243], v212, v212 op_sel_hi:[0,0,0]
	v_mfma_scale_f32_16x16x128_f8f6f4 v[12:15], v[8:15], v[184:191], v[244:247], v212, v212 op_sel_hi:[0,0,0]
	s_setprio 0
	s_barrier
	s_add_i32 s41, s41, 0x40080
	s_mov_b32 m0, s25
	s_nop 0
	buffer_load_dwordx4 v96, s[8:11], s41 offen lds
	s_mov_b32 m0, s26
	s_nop 0
	buffer_load_dwordx4 v130, s[8:11], s41 offen lds
	s_waitcnt vmcnt(6)
	s_barrier
	s_setprio 1
	v_mfma_scale_f32_16x16x128_f8f6f4 v[48:51], v[136:143], v[152:159], v[48:51], v212, v212 op_sel_hi:[0,0,0]
	v_mfma_scale_f32_16x16x128_f8f6f4 v[40:43], v[144:151], v[152:159], v[248:251], v212, v212 op_sel_hi:[0,0,0]
	v_mfma_scale_f32_16x16x128_f8f6f4 v[32:35], v[136:143], v[168:175], v[164:167], v212, v212 op_sel_hi:[0,0,0]
	v_mfma_scale_f32_16x16x128_f8f6f4 v[24:27], v[144:151], v[168:175], v[224:227], v212, v212 op_sel_hi:[0,0,0]
	v_mfma_scale_f32_16x16x128_f8f6f4 v[208:211], v[136:143], v[176:183], v[208:211], v212, v212 op_sel_hi:[0,0,0]
	v_mfma_scale_f32_16x16x128_f8f6f4 v[8:11], v[144:151], v[176:183], v[214:217], v212, v212 op_sel_hi:[0,0,0]
	v_mfma_scale_f32_16x16x128_f8f6f4 v[4:7], v[136:143], v[184:191], v[220:223], v212, v212 op_sel_hi:[0,0,0]
	v_mfma_scale_f32_16x16x128_f8f6f4 v[0:3], v[144:151], v[184:191], v[64:67], v212, v212 op_sel_hi:[0,0,0]
	s_setprio 0
	s_add_i32 s40, s40, 2
	s_addk_i32 s38, 0x100
	s_addk_i32 s39, 0x100
	s_cmp_gt_u32 s40, 13
	s_barrier
	s_cbranch_scc0 .LBB0_351
	s_getreg_b32 s6, hwreg(HW_REG_HW_ID, 0, 6)
	s_and_b32 s6, s6, 63
	s_lshl_b32 s6, s6, 2
	s_add_i32 s6, s6, 0
	s_add_i32 s6, s6, 0x20010
	v_mov_b32_e32 v64, s6
	ds_read_b32 v64, v64
	s_lshl_b32 s6, s37, 8
	s_mul_i32 s7, s37, 0x300000
	v_mbcnt_lo_u32_b32 v65, -1, 0
	v_mbcnt_hi_u32_b32 v65, -1, v65
	s_mul_hi_i32 s6, s6, 0x3000
	s_waitcnt lgkmcnt(0)
	v_readfirstlane_b32 s10, v64
	v_and_b32_e32 v66, 15, v65
	v_pk_mul_f32 v[18:19], v[18:19], s[78:79] op_sel_hi:[1,0]
	v_lshl_or_b32 v135, s10, 6, v65
	s_add_u32 s10, s20, s7
	s_addc_u32 s11, s21, s6
	s_lshl_b32 s6, s36, 8
	s_ashr_i32 s7, s6, 31
	s_lshl_b64 s[6:7], s[6:7], 1
	s_add_u32 s6, s10, s6
	v_lshrrev_b32_e32 v64, 2, v135
	s_mov_b32 s10, 0xfffc0
	v_and_or_b32 v136, v64, s10, v66
	v_pk_mul_f32 v[64:65], v[128:129], s[78:79] op_sel_hi:[1,0]
	v_pk_mul_f32 v[66:67], v[126:127], s[78:79] op_sel_hi:[1,0]
	v_pk_mul_f32 v[126:127], v[124:125], s[78:79] op_sel_hi:[1,0]
	v_pk_mul_f32 v[124:125], v[122:123], s[78:79] op_sel_hi:[1,0]
	v_cvt_pk_bf16_f32 v123, v64, v65
	v_mul_u32_u24_e32 v64, 0x3000, v136
	s_movk_i32 s10, 0xf0
	v_cvt_pk_bf16_f32 v122, v66, v67
	v_cvt_pk_bf16_f32 v124, v124, v125
	v_cvt_pk_bf16_f32 v125, v126, v127
	v_and_or_b32 v126, v135, s10, v64
	v_pk_mul_f32 v[64:65], v[112:113], s[78:79] op_sel_hi:[1,0]
	v_pk_mul_f32 v[66:67], v[110:111], s[78:79] op_sel_hi:[1,0]
	v_pk_mul_f32 v[110:111], v[108:109], s[78:79] op_sel_hi:[1,0]
	v_pk_mul_f32 v[108:109], v[106:107], s[78:79] op_sel_hi:[1,0]
	s_addc_u32 s7, s11, s7
	v_cvt_pk_bf16_f32 v106, v66, v67
	v_cvt_pk_bf16_f32 v107, v64, v65
	v_cvt_pk_bf16_f32 v108, v108, v109
	v_cvt_pk_bf16_f32 v109, v110, v111
	global_store_dwordx4 v126, v[106:109], s[6:7] offset:256
	v_pk_mul_f32 v[64:65], v[120:121], s[78:79] op_sel_hi:[1,0]
	v_pk_mul_f32 v[66:67], v[118:119], s[78:79] op_sel_hi:[1,0]
	v_pk_mul_f32 v[110:111], v[116:117], s[78:79] op_sel_hi:[1,0]
	v_pk_mul_f32 v[108:109], v[114:115], s[78:79] op_sel_hi:[1,0]
	v_cvt_pk_bf16_f32 v106, v66, v67
	v_cvt_pk_bf16_f32 v107, v64, v65
	v_cvt_pk_bf16_f32 v108, v108, v109
	v_cvt_pk_bf16_f32 v109, v110, v111
	v_add_u32_e32 v64, 0x30000, v126
	global_store_dwordx4 v64, v[106:109], s[6:7]
	v_pk_mul_f32 v[64:65], v[94:95], s[78:79] op_sel_hi:[1,0]
	v_pk_mul_f32 v[66:67], v[92:93], s[78:79] op_sel_hi:[1,0]
	v_pk_mul_f32 v[92:93], v[90:91], s[78:79] op_sel_hi:[1,0]
	v_pk_mul_f32 v[90:91], v[88:89], s[78:79] op_sel_hi:[1,0]
	v_cvt_pk_bf16_f32 v88, v66, v67
	v_cvt_pk_bf16_f32 v89, v64, v65
	v_cvt_pk_bf16_f32 v90, v90, v91
	v_cvt_pk_bf16_f32 v91, v92, v93
	v_add_u32_e32 v64, 0x30100, v126
	global_store_dwordx4 v126, v[122:125], s[6:7]
	global_store_dwordx4 v64, v[88:91], s[6:7]
	v_pk_mul_f32 v[64:65], v[104:105], s[78:79] op_sel_hi:[1,0]
	v_pk_mul_f32 v[66:67], v[102:103], s[78:79] op_sel_hi:[1,0]
	v_pk_mul_f32 v[92:93], v[100:101], s[78:79] op_sel_hi:[1,0]
	v_pk_mul_f32 v[90:91], v[98:99], s[78:79] op_sel_hi:[1,0]
	v_cvt_pk_bf16_f32 v88, v66, v67
	v_cvt_pk_bf16_f32 v89, v64, v65
	v_cvt_pk_bf16_f32 v90, v90, v91
	v_cvt_pk_bf16_f32 v91, v92, v93
	v_add_u32_e32 v64, 0x60000, v126
	global_store_dwordx4 v64, v[88:91], s[6:7]
	v_pk_mul_f32 v[64:65], v[78:79], s[78:79] op_sel_hi:[1,0]
	v_pk_mul_f32 v[66:67], v[76:77], s[78:79] op_sel_hi:[1,0]
	v_pk_mul_f32 v[76:77], v[74:75], s[78:79] op_sel_hi:[1,0]
	v_pk_mul_f32 v[74:75], v[72:73], s[78:79] op_sel_hi:[1,0]
	v_cvt_pk_bf16_f32 v72, v66, v67
	v_cvt_pk_bf16_f32 v73, v64, v65
	v_cvt_pk_bf16_f32 v74, v74, v75
	v_cvt_pk_bf16_f32 v75, v76, v77
	v_add_u32_e32 v64, 0x60100, v126
	global_store_dwordx4 v64, v[72:75], s[6:7]
	v_pk_mul_f32 v[64:65], v[86:87], s[78:79] op_sel_hi:[1,0]
	v_pk_mul_f32 v[66:67], v[84:85], s[78:79] op_sel_hi:[1,0]
	v_cvt_pk_bf16_f32 v73, v64, v65
	v_cvt_pk_bf16_f32 v72, v66, v67
	v_pk_mul_f32 v[66:67], v[70:71], s[78:79] op_sel_hi:[1,0]
	v_pk_mul_f32 v[64:65], v[68:69], s[78:79] op_sel_hi:[1,0]
	v_pk_mul_f32 v[16:17], v[16:17], s[78:79] op_sel_hi:[1,0]
	v_pk_mul_f32 v[76:77], v[82:83], s[78:79] op_sel_hi:[1,0]
	v_pk_mul_f32 v[74:75], v[80:81], s[78:79] op_sel_hi:[1,0]
	v_cvt_pk_bf16_f32 v64, v64, v65
	v_cvt_pk_bf16_f32 v65, v66, v67
	v_cvt_pk_bf16_f32 v66, v16, v17
	v_cvt_pk_bf16_f32 v67, v18, v19
	v_pk_mul_f32 v[16:17], v[62:63], s[78:79] op_sel_hi:[1,0]
	v_pk_mul_f32 v[18:19], v[60:61], s[78:79] op_sel_hi:[1,0]
	v_pk_mul_f32 v[60:61], v[58:59], s[78:79] op_sel_hi:[1,0]
	v_pk_mul_f32 v[58:59], v[56:57], s[78:79] op_sel_hi:[1,0]
	v_cvt_pk_bf16_f32 v74, v74, v75
	v_cvt_pk_bf16_f32 v75, v76, v77
	v_add_u32_e32 v76, 0x90000, v126
	v_cvt_pk_bf16_f32 v56, v18, v19
	v_cvt_pk_bf16_f32 v57, v16, v17
	v_cvt_pk_bf16_f32 v58, v58, v59
	v_cvt_pk_bf16_f32 v59, v60, v61
	v_add_u32_e32 v16, 0x180000, v126
	global_store_dwordx4 v76, v[72:75], s[6:7]
	global_store_dwordx4 v76, v[64:67], s[6:7] offset:256
	global_store_dwordx4 v16, v[56:59], s[6:7]
	v_pk_mul_f32 v[16:17], v[50:51], s[78:79] op_sel_hi:[1,0]
	v_pk_mul_f32 v[18:19], v[48:49], s[78:79] op_sel_hi:[1,0]
	v_pk_mul_f32 v[48:49], v[42:43], s[78:79] op_sel_hi:[1,0]
	v_pk_mul_f32 v[42:43], v[40:41], s[78:79] op_sel_hi:[1,0]
	v_cvt_pk_bf16_f32 v40, v18, v19
	v_cvt_pk_bf16_f32 v41, v16, v17
	v_cvt_pk_bf16_f32 v42, v42, v43
	v_cvt_pk_bf16_f32 v43, v48, v49
	v_add_u32_e32 v16, 0x180100, v126
	global_store_dwordx4 v16, v[40:43], s[6:7]
	v_pk_mul_f32 v[16:17], v[54:55], s[78:79] op_sel_hi:[1,0]
	v_pk_mul_f32 v[18:19], v[52:53], s[78:79] op_sel_hi:[1,0]
	v_cvt_pk_bf16_f32 v41, v16, v17
	v_cvt_pk_bf16_f32 v40, v18, v19
	v_pk_mul_f32 v[16:17], v[34:35], s[78:79] op_sel_hi:[1,0]
	v_pk_mul_f32 v[18:19], v[32:33], s[78:79] op_sel_hi:[1,0]
	v_pk_mul_f32 v[32:33], v[26:27], s[78:79] op_sel_hi:[1,0]
	v_pk_mul_f32 v[26:27], v[24:25], s[78:79] op_sel_hi:[1,0]
	v_pk_mul_f32 v[42:43], v[44:45], s[78:79] op_sel_hi:[1,0]
	v_add_u32_e32 v44, 0x1b0000, v126
	v_cvt_pk_bf16_f32 v24, v18, v19
	v_cvt_pk_bf16_f32 v25, v16, v17
	v_cvt_pk_bf16_f32 v26, v26, v27
	v_cvt_pk_bf16_f32 v27, v32, v33
	v_pk_mul_f32 v[46:47], v[46:47], s[78:79] op_sel_hi:[1,0]
	global_store_dwordx4 v44, v[24:27], s[6:7] offset:256
	v_pk_mul_f32 v[16:17], v[38:39], s[78:79] op_sel_hi:[1,0]
	v_pk_mul_f32 v[18:19], v[36:37], s[78:79] op_sel_hi:[1,0]
	v_pk_mul_f32 v[30:31], v[30:31], s[78:79] op_sel_hi:[1,0]
	v_pk_mul_f32 v[26:27], v[28:29], s[78:79] op_sel_hi:[1,0]
	v_cvt_pk_bf16_f32 v42, v42, v43
	v_cvt_pk_bf16_f32 v43, v46, v47
	v_cvt_pk_bf16_f32 v24, v18, v19
	v_cvt_pk_bf16_f32 v25, v16, v17
	v_cvt_pk_bf16_f32 v26, v26, v27
	v_cvt_pk_bf16_f32 v27, v30, v31
	v_add_u32_e32 v28, 0x1e0000, v126
	global_store_dwordx4 v44, v[40:43], s[6:7]
	global_store_dwordx4 v28, v[24:27], s[6:7]
	v_pk_mul_f32 v[16:17], v[210:211], s[78:79] op_sel_hi:[1,0]
	v_pk_mul_f32 v[18:19], v[208:209], s[78:79] op_sel_hi:[1,0]
	v_pk_mul_f32 v[24:25], v[10:11], s[78:79] op_sel_hi:[1,0]
	v_pk_mul_f32 v[10:11], v[8:9], s[78:79] op_sel_hi:[1,0]
	v_cvt_pk_bf16_f32 v8, v18, v19
	v_cvt_pk_bf16_f32 v9, v16, v17
	v_cvt_pk_bf16_f32 v10, v10, v11
	v_cvt_pk_bf16_f32 v11, v24, v25
	global_store_dwordx4 v28, v[8:11], s[6:7] offset:256
	v_pk_mul_f32 v[14:15], v[14:15], s[78:79] op_sel_hi:[1,0]
	v_pk_mul_f32 v[12:13], v[12:13], s[78:79] op_sel_hi:[1,0]
	v_pk_mul_f32 v[10:11], v[22:23], s[78:79] op_sel_hi:[1,0]
	v_pk_mul_f32 v[8:9], v[20:21], s[78:79] op_sel_hi:[1,0]
	v_pk_mul_f32 v[6:7], v[6:7], s[78:79] op_sel_hi:[1,0]
	v_cvt_pk_bf16_f32 v8, v8, v9
	v_cvt_pk_bf16_f32 v9, v10, v11
	v_cvt_pk_bf16_f32 v10, v12, v13
	v_cvt_pk_bf16_f32 v11, v14, v15
	v_add_u32_e32 v12, 0x210000, v126
	global_store_dwordx4 v12, v[8:11], s[6:7]
	v_pk_mul_f32 v[4:5], v[4:5], s[78:79] op_sel_hi:[1,0]
	s_and_b64 vcc, exec, s[4:5]
	v_pk_mul_f32 v[8:9], v[2:3], s[78:79] op_sel_hi:[1,0]
	v_pk_mul_f32 v[2:3], v[0:1], s[78:79] op_sel_hi:[1,0]
	v_cvt_pk_bf16_f32 v0, v4, v5
	v_cvt_pk_bf16_f32 v1, v6, v7
	v_cvt_pk_bf16_f32 v2, v2, v3
	v_cvt_pk_bf16_f32 v3, v8, v9
	s_mov_b32 s36, s30
	s_mov_b32 s37, s31
	s_mov_b32 s39, s35
	s_mov_b32 s10, s34
	v_mov_b32_e32 v242, v252
	v_mov_b32_e32 v252, v213
	v_mov_b32_e32 v213, 0x358637bd
	global_store_dwordx4 v12, v[0:3], s[6:7] offset:256
	s_cbranch_vccz .LBB0_344
	s_waitcnt vmcnt(0)
	s_cmpk_gt_u32 s0, 0xff
	s_cbranch_scc1 .LBB0_355
	s_barrier

.LBB0_484:
	ds_read_b128 v[136:139], v133
	ds_read_b128 v[140:143], v133 offset:1024
	ds_read_b128 v[144:147], v133 offset:2048
	ds_read_b128 v[148:151], v133 offset:3072
	s_add_i32 s10, s42, 0xffe80080
	s_cmp_eq_u32 s44, 4
	s_cselect_b32 s47, s6, s10
	s_cselect_b32 s45, s7, s43
	s_or_b32 s46, s47, 0x80
	s_mov_b32 m0, s31
	ds_read_b128 v[152:155], v134
	ds_read_b128 v[156:159], v134 offset:1024
	ds_read_b128 v[160:163], v134 offset:2048
	ds_read_b128 v[164:167], v134 offset:3072
	ds_read_b128 v[168:171], v134 offset:4096
	ds_read_b128 v[172:175], v134 offset:5120
	ds_read_b128 v[176:179], v134 offset:6144
	ds_read_b128 v[180:183], v134 offset:7168
	buffer_load_dwordx4 v96, s[72:75], s42 offen lds
	s_mov_b32 m0, s34
	s_nop 0
	buffer_load_dwordx4 v131, s[72:75], s42 offen lds
	s_waitcnt lgkmcnt(8)
	s_barrier
	s_setprio 1
	s_waitcnt lgkmcnt(7)
	v_mfma_f32_16x16x32_bf16 v[126:129], v[136:139], v[152:155], v[126:129]
	v_mfma_f32_16x16x32_bf16 v[122:125], v[144:147], v[152:155], v[122:125]
	s_waitcnt lgkmcnt(5)
	v_mfma_f32_16x16x32_bf16 v[118:121], v[136:139], v[160:163], v[118:121]
	v_mfma_f32_16x16x32_bf16 v[114:117], v[144:147], v[160:163], v[114:117]
	s_waitcnt lgkmcnt(3)
	v_mfma_f32_16x16x32_bf16 v[102:105], v[136:139], v[168:171], v[102:105]
	v_mfma_f32_16x16x32_bf16 v[98:101], v[144:147], v[168:171], v[98:101]
	s_waitcnt lgkmcnt(1)
	v_mfma_f32_16x16x32_bf16 v[84:87], v[136:139], v[176:179], v[84:87]
	v_mfma_f32_16x16x32_bf16 v[80:83], v[144:147], v[176:179], v[80:83]
	v_mfma_f32_16x16x32_bf16 v[126:129], v[140:143], v[156:159], v[126:129]
	v_mfma_f32_16x16x32_bf16 v[122:125], v[148:151], v[156:159], v[122:125]
	v_mfma_f32_16x16x32_bf16 v[118:121], v[140:143], v[164:167], v[118:121]
	v_mfma_f32_16x16x32_bf16 v[114:117], v[148:151], v[164:167], v[114:117]
	v_mfma_f32_16x16x32_bf16 v[102:105], v[140:143], v[172:175], v[102:105]
	v_mfma_f32_16x16x32_bf16 v[98:101], v[148:151], v[172:175], v[98:101]
	s_waitcnt lgkmcnt(0)
	v_mfma_f32_16x16x32_bf16 v[84:87], v[140:143], v[180:183], v[84:87]
	v_mfma_f32_16x16x32_bf16 v[80:83], v[148:151], v[180:183], v[80:83]
	s_setprio 0
	s_barrier
	s_mov_b32 s10, s74
	s_mov_b32 s11, s75
	s_mov_b32 m0, s16
	ds_read_b128 v[184:187], v133 offset:16384
	ds_read_b128 v[188:191], v133 offset:17408
	ds_read_b128 v[192:195], v133 offset:18432
	ds_read_b128 v[196:199], v133 offset:19456
	buffer_load_dwordx4 v130, s[8:11], s45 offen lds
	s_mov_b32 m0, s17
	s_nop 0
	buffer_load_dwordx4 v132, s[8:11], s45 offen lds
	s_barrier
	s_setprio 1
	s_waitcnt lgkmcnt(3)
	v_mfma_f32_16x16x32_bf16 v[110:113], v[184:187], v[152:155], v[110:113]
	s_waitcnt lgkmcnt(1)
	v_mfma_f32_16x16x32_bf16 v[106:109], v[192:195], v[152:155], v[106:109]
	v_mfma_f32_16x16x32_bf16 v[92:95], v[184:187], v[160:163], v[92:95]
	v_mfma_f32_16x16x32_bf16 v[88:91], v[192:195], v[160:163], v[88:91]
	v_mfma_f32_16x16x32_bf16 v[76:79], v[184:187], v[168:171], v[76:79]
	v_mfma_f32_16x16x32_bf16 v[72:75], v[192:195], v[168:171], v[72:75]
	v_mfma_f32_16x16x32_bf16 v[68:71], v[184:187], v[176:179], v[68:71]
	v_mfma_f32_16x16x32_bf16 v[64:67], v[192:195], v[176:179], v[64:67]
	v_mfma_f32_16x16x32_bf16 v[110:113], v[188:191], v[156:159], v[110:113]
	s_waitcnt lgkmcnt(0)
	v_mfma_f32_16x16x32_bf16 v[106:109], v[196:199], v[156:159], v[106:109]
	v_mfma_f32_16x16x32_bf16 v[92:95], v[188:191], v[164:167], v[92:95]
	v_mfma_f32_16x16x32_bf16 v[88:91], v[196:199], v[164:167], v[88:91]
	v_mfma_f32_16x16x32_bf16 v[76:79], v[188:191], v[172:175], v[76:79]
	v_mfma_f32_16x16x32_bf16 v[72:75], v[196:199], v[172:175], v[72:75]
	v_mfma_f32_16x16x32_bf16 v[68:71], v[188:191], v[180:183], v[68:71]
	v_mfma_f32_16x16x32_bf16 v[64:67], v[196:199], v[180:183], v[64:67]
	s_setprio 0
	s_mov_b32 m0, s15
	s_barrier
	ds_read_b128 v[152:155], v134 offset:16384
	ds_read_b128 v[156:159], v134 offset:17408
	ds_read_b128 v[160:163], v134 offset:18432
	ds_read_b128 v[164:167], v134 offset:19456
	ds_read_b128 v[168:171], v134 offset:20480
	ds_read_b128 v[172:175], v134 offset:21504
	ds_read_b128 v[176:179], v134 offset:22528
	ds_read_b128 v[180:183], v134 offset:23552
	buffer_load_dwordx4 v96, s[72:75], s47 offen lds
	s_mov_b32 m0, s18
	s_nop 0
	buffer_load_dwordx4 v131, s[72:75], s47 offen lds
	s_barrier
	s_setprio 1
	s_waitcnt lgkmcnt(7)
	v_mfma_f32_16x16x32_bf16 v[60:63], v[136:139], v[152:155], v[60:63]
	v_mfma_f32_16x16x32_bf16 v[56:59], v[144:147], v[152:155], v[56:59]
	s_waitcnt lgkmcnt(5)
	v_mfma_f32_16x16x32_bf16 v[52:55], v[136:139], v[160:163], v[52:55]
	v_mfma_f32_16x16x32_bf16 v[48:51], v[144:147], v[160:163], v[48:51]
	s_waitcnt lgkmcnt(3)
	v_mfma_f32_16x16x32_bf16 v[36:39], v[136:139], v[168:171], v[36:39]
	v_mfma_f32_16x16x32_bf16 v[32:35], v[144:147], v[168:171], v[32:35]
	s_waitcnt lgkmcnt(1)
	v_mfma_f32_16x16x32_bf16 v[20:23], v[136:139], v[176:179], v[20:23]
	v_mfma_f32_16x16x32_bf16 v[16:19], v[144:147], v[176:179], v[16:19]
	v_mfma_f32_16x16x32_bf16 v[60:63], v[140:143], v[156:159], v[60:63]
	v_mfma_f32_16x16x32_bf16 v[56:59], v[148:151], v[156:159], v[56:59]
	v_mfma_f32_16x16x32_bf16 v[52:55], v[140:143], v[164:167], v[52:55]
	v_mfma_f32_16x16x32_bf16 v[48:51], v[148:151], v[164:167], v[48:51]
	v_mfma_f32_16x16x32_bf16 v[36:39], v[140:143], v[172:175], v[36:39]
	v_mfma_f32_16x16x32_bf16 v[32:35], v[148:151], v[172:175], v[32:35]
	s_waitcnt lgkmcnt(0)
	v_mfma_f32_16x16x32_bf16 v[20:23], v[140:143], v[180:183], v[20:23]
	v_mfma_f32_16x16x32_bf16 v[16:19], v[148:151], v[180:183], v[16:19]
	s_setprio 0
	s_barrier
	s_add_i32 s48, s45, 0x20000
	s_mov_b32 m0, s19
	s_nop 0
	buffer_load_dwordx4 v130, s[8:11], s48 offen lds
	s_mov_b32 m0, s20
	s_nop 0
	buffer_load_dwordx4 v132, s[8:11], s48 offen lds
	s_waitcnt vmcnt(6)
	s_barrier
	s_setprio 1
	v_mfma_f32_16x16x32_bf16 v[44:47], v[184:187], v[152:155], v[44:47]
	v_mfma_f32_16x16x32_bf16 v[40:43], v[192:195], v[152:155], v[40:43]
	v_mfma_f32_16x16x32_bf16 v[28:31], v[184:187], v[160:163], v[28:31]
	v_mfma_f32_16x16x32_bf16 v[24:27], v[192:195], v[160:163], v[24:27]
	v_mfma_f32_16x16x32_bf16 v[12:15], v[184:187], v[168:171], v[12:15]
	v_mfma_f32_16x16x32_bf16 v[8:11], v[192:195], v[168:171], v[8:11]
	v_mfma_f32_16x16x32_bf16 v[4:7], v[184:187], v[176:179], v[4:7]
	v_mfma_f32_16x16x32_bf16 v[0:3], v[192:195], v[176:179], v[0:3]
	v_mfma_f32_16x16x32_bf16 v[44:47], v[188:191], v[156:159], v[44:47]
	v_mfma_f32_16x16x32_bf16 v[40:43], v[196:199], v[156:159], v[40:43]
	v_mfma_f32_16x16x32_bf16 v[28:31], v[188:191], v[164:167], v[28:31]
	v_mfma_f32_16x16x32_bf16 v[24:27], v[196:199], v[164:167], v[24:27]
	v_mfma_f32_16x16x32_bf16 v[12:15], v[188:191], v[172:175], v[12:15]
	v_mfma_f32_16x16x32_bf16 v[8:11], v[196:199], v[172:175], v[8:11]
	v_mfma_f32_16x16x32_bf16 v[4:7], v[188:191], v[180:183], v[4:7]
	v_mfma_f32_16x16x32_bf16 v[0:3], v[196:199], v[180:183], v[0:3]
	s_setprio 0
	s_barrier
	ds_read_b128 v[136:139], v133 offset:32768
	ds_read_b128 v[140:143], v133 offset:33792
	ds_read_b128 v[144:147], v133 offset:34816
	ds_read_b128 v[148:151], v133 offset:35840
	s_add_i32 s47, s47, 0x180000
	s_mov_b32 m0, s21
	ds_read_b128 v[152:155], v134 offset:32768
	ds_read_b128 v[156:159], v134 offset:33792
	ds_read_b128 v[160:163], v134 offset:34816
	ds_read_b128 v[164:167], v134 offset:35840
	ds_read_b128 v[168:171], v134 offset:36864
	ds_read_b128 v[172:175], v134 offset:37888
	ds_read_b128 v[176:179], v134 offset:38912
	ds_read_b128 v[180:183], v134 offset:39936
	buffer_load_dwordx4 v96, s[72:75], s47 offen lds
	s_mov_b32 m0, s22
	s_nop 0
	buffer_load_dwordx4 v131, s[72:75], s47 offen lds
	s_waitcnt lgkmcnt(8)
	s_barrier
	s_setprio 1
	s_waitcnt lgkmcnt(7)
	v_mfma_f32_16x16x32_bf16 v[126:129], v[136:139], v[152:155], v[126:129]
	v_mfma_f32_16x16x32_bf16 v[122:125], v[144:147], v[152:155], v[122:125]
	s_waitcnt lgkmcnt(5)
	v_mfma_f32_16x16x32_bf16 v[118:121], v[136:139], v[160:163], v[118:121]
	v_mfma_f32_16x16x32_bf16 v[114:117], v[144:147], v[160:163], v[114:117]
	s_waitcnt lgkmcnt(3)
	v_mfma_f32_16x16x32_bf16 v[102:105], v[136:139], v[168:171], v[102:105]
	v_mfma_f32_16x16x32_bf16 v[98:101], v[144:147], v[168:171], v[98:101]
	s_waitcnt lgkmcnt(1)
	v_mfma_f32_16x16x32_bf16 v[84:87], v[136:139], v[176:179], v[84:87]
	v_mfma_f32_16x16x32_bf16 v[80:83], v[144:147], v[176:179], v[80:83]
	v_mfma_f32_16x16x32_bf16 v[126:129], v[140:143], v[156:159], v[126:129]
	v_mfma_f32_16x16x32_bf16 v[122:125], v[148:151], v[156:159], v[122:125]
	v_mfma_f32_16x16x32_bf16 v[118:121], v[140:143], v[164:167], v[118:121]
	v_mfma_f32_16x16x32_bf16 v[114:117], v[148:151], v[164:167], v[114:117]
	v_mfma_f32_16x16x32_bf16 v[102:105], v[140:143], v[172:175], v[102:105]
	v_mfma_f32_16x16x32_bf16 v[98:101], v[148:151], v[172:175], v[98:101]
	s_waitcnt lgkmcnt(0)
	v_mfma_f32_16x16x32_bf16 v[84:87], v[140:143], v[180:183], v[84:87]
	v_mfma_f32_16x16x32_bf16 v[80:83], v[148:151], v[180:183], v[80:83]
	s_setprio 0
	s_barrier
	s_or_b32 s47, s45, 0x80
	s_mov_b32 m0, s25
	ds_read_b128 v[184:187], v133 offset:49152
	ds_read_b128 v[188:191], v133 offset:50176
	ds_read_b128 v[192:195], v133 offset:51200
	ds_read_b128 v[196:199], v133 offset:52224
	buffer_load_dwordx4 v130, s[8:11], s47 offen lds
	s_mov_b32 m0, s26
	s_nop 0
	buffer_load_dwordx4 v132, s[8:11], s47 offen lds
	s_barrier
	s_setprio 1
	s_waitcnt lgkmcnt(3)
	v_mfma_f32_16x16x32_bf16 v[110:113], v[184:187], v[152:155], v[110:113]
	s_waitcnt lgkmcnt(1)
	v_mfma_f32_16x16x32_bf16 v[106:109], v[192:195], v[152:155], v[106:109]
	v_mfma_f32_16x16x32_bf16 v[92:95], v[184:187], v[160:163], v[92:95]
	v_mfma_f32_16x16x32_bf16 v[88:91], v[192:195], v[160:163], v[88:91]
	v_mfma_f32_16x16x32_bf16 v[76:79], v[184:187], v[168:171], v[76:79]
	v_mfma_f32_16x16x32_bf16 v[72:75], v[192:195], v[168:171], v[72:75]
	v_mfma_f32_16x16x32_bf16 v[68:71], v[184:187], v[176:179], v[68:71]
	v_mfma_f32_16x16x32_bf16 v[64:67], v[192:195], v[176:179], v[64:67]
	v_mfma_f32_16x16x32_bf16 v[110:113], v[188:191], v[156:159], v[110:113]
	s_waitcnt lgkmcnt(0)
	v_mfma_f32_16x16x32_bf16 v[106:109], v[196:199], v[156:159], v[106:109]
	v_mfma_f32_16x16x32_bf16 v[92:95], v[188:191], v[164:167], v[92:95]
	v_mfma_f32_16x16x32_bf16 v[88:91], v[196:199], v[164:167], v[88:91]
	v_mfma_f32_16x16x32_bf16 v[76:79], v[188:191], v[172:175], v[76:79]
	v_mfma_f32_16x16x32_bf16 v[72:75], v[196:199], v[172:175], v[72:75]
	v_mfma_f32_16x16x32_bf16 v[68:71], v[188:191], v[180:183], v[68:71]
	v_mfma_f32_16x16x32_bf16 v[64:67], v[196:199], v[180:183], v[64:67]
	s_setprio 0
	s_mov_b32 m0, s27
	s_barrier
	ds_read_b128 v[152:155], v134 offset:49152
	ds_read_b128 v[156:159], v134 offset:50176
	ds_read_b128 v[160:163], v134 offset:51200
	ds_read_b128 v[164:167], v134 offset:52224
	ds_read_b128 v[168:171], v134 offset:53248
	ds_read_b128 v[172:175], v134 offset:54272
	ds_read_b128 v[176:179], v134 offset:55296
	ds_read_b128 v[180:183], v134 offset:56320
	buffer_load_dwordx4 v96, s[72:75], s46 offen lds
	s_mov_b32 m0, s28
	s_nop 0
	buffer_load_dwordx4 v131, s[72:75], s46 offen lds
	s_barrier
	s_setprio 1
	s_waitcnt lgkmcnt(7)
	v_mfma_f32_16x16x32_bf16 v[60:63], v[136:139], v[152:155], v[60:63]
	v_mfma_f32_16x16x32_bf16 v[56:59], v[144:147], v[152:155], v[56:59]
	s_waitcnt lgkmcnt(5)
	v_mfma_f32_16x16x32_bf16 v[52:55], v[136:139], v[160:163], v[52:55]
	v_mfma_f32_16x16x32_bf16 v[48:51], v[144:147], v[160:163], v[48:51]
	s_waitcnt lgkmcnt(3)
	v_mfma_f32_16x16x32_bf16 v[36:39], v[136:139], v[168:171], v[36:39]
	v_mfma_f32_16x16x32_bf16 v[32:35], v[144:147], v[168:171], v[32:35]
	s_waitcnt lgkmcnt(1)
	v_mfma_f32_16x16x32_bf16 v[20:23], v[136:139], v[176:179], v[20:23]
	v_mfma_f32_16x16x32_bf16 v[16:19], v[144:147], v[176:179], v[16:19]
	v_mfma_f32_16x16x32_bf16 v[60:63], v[140:143], v[156:159], v[60:63]
	v_mfma_f32_16x16x32_bf16 v[56:59], v[148:151], v[156:159], v[56:59]
	v_mfma_f32_16x16x32_bf16 v[52:55], v[140:143], v[164:167], v[52:55]
	v_mfma_f32_16x16x32_bf16 v[48:51], v[148:151], v[164:167], v[48:51]
	v_mfma_f32_16x16x32_bf16 v[36:39], v[140:143], v[172:175], v[36:39]
	v_mfma_f32_16x16x32_bf16 v[32:35], v[148:151], v[172:175], v[32:35]
	s_waitcnt lgkmcnt(0)
	v_mfma_f32_16x16x32_bf16 v[20:23], v[140:143], v[180:183], v[20:23]
	v_mfma_f32_16x16x32_bf16 v[16:19], v[148:151], v[180:183], v[16:19]
	s_setprio 0
	s_barrier
	s_add_i32 s45, s45, 0x20080
	s_mov_b32 m0, s29
	s_nop 0
	buffer_load_dwordx4 v130, s[8:11], s45 offen lds
	s_mov_b32 m0, s30
	s_nop 0
	buffer_load_dwordx4 v132, s[8:11], s45 offen lds
	s_waitcnt vmcnt(6)
	s_barrier
	s_setprio 1
	v_mfma_f32_16x16x32_bf16 v[44:47], v[184:187], v[152:155], v[44:47]
	v_mfma_f32_16x16x32_bf16 v[40:43], v[192:195], v[152:155], v[40:43]
	v_mfma_f32_16x16x32_bf16 v[28:31], v[184:187], v[160:163], v[28:31]
	v_mfma_f32_16x16x32_bf16 v[24:27], v[192:195], v[160:163], v[24:27]
	v_mfma_f32_16x16x32_bf16 v[12:15], v[184:187], v[168:171], v[12:15]
	v_mfma_f32_16x16x32_bf16 v[8:11], v[192:195], v[168:171], v[8:11]
	v_mfma_f32_16x16x32_bf16 v[4:7], v[184:187], v[176:179], v[4:7]
	v_mfma_f32_16x16x32_bf16 v[0:3], v[192:195], v[176:179], v[0:3]
	v_mfma_f32_16x16x32_bf16 v[44:47], v[188:191], v[156:159], v[44:47]
	v_mfma_f32_16x16x32_bf16 v[40:43], v[196:199], v[156:159], v[40:43]
	v_mfma_f32_16x16x32_bf16 v[28:31], v[188:191], v[164:167], v[28:31]
	v_mfma_f32_16x16x32_bf16 v[24:27], v[196:199], v[164:167], v[24:27]
	v_mfma_f32_16x16x32_bf16 v[12:15], v[188:191], v[172:175], v[12:15]
	v_mfma_f32_16x16x32_bf16 v[8:11], v[196:199], v[172:175], v[8:11]
	v_mfma_f32_16x16x32_bf16 v[4:7], v[188:191], v[180:183], v[4:7]
	v_mfma_f32_16x16x32_bf16 v[0:3], v[196:199], v[180:183], v[0:3]
	s_setprio 0
	s_add_i32 s44, s44, 2
	s_addk_i32 s42, 0x100
	s_addk_i32 s43, 0x100
	s_cmp_gt_u32 s44, 5
	s_barrier
	s_cbranch_scc0 .LBB0_484
	s_getreg_b32 s6, hwreg(HW_REG_HW_ID, 0, 6)
	s_and_b32 s6, s6, 63
	s_lshl_b32 s6, s6, 2
	s_add_i32 s6, s6, 0
	s_add_i32 s6, s6, 0x20010
	v_mov_b32_e32 v135, s6
	ds_read_b32 v135, v135
	s_lshl_b32 s6, s41, 8
	s_mul_i32 s7, s41, 0x60000
	v_mbcnt_lo_u32_b32 v136, -1, 0
	v_mbcnt_hi_u32_b32 v136, -1, v136
	s_mul_hi_i32 s6, s6, 0x600
	s_waitcnt lgkmcnt(0)
	v_readfirstlane_b32 s10, v135
	v_and_b32_e32 v137, 15, v136
	v_cvt_pk_bf16_f32 v126, v126, v127
	v_lshl_or_b32 v135, s10, 6, v136
	s_add_u32 s10, s23, s7
	s_addc_u32 s11, s24, s6
	s_lshl_b32 s6, s40, 8
	s_ashr_i32 s7, s6, 31
	s_lshl_b64 s[6:7], s[6:7], 1
	s_add_u32 s6, s10, s6
	v_lshrrev_b32_e32 v136, 2, v135
	s_mov_b32 s10, 0x7fffc0
	v_and_or_b32 v136, v136, s10, v137
	v_cvt_pk_bf16_f32 v127, v128, v129
	v_cvt_pk_bf16_f32 v128, v122, v123
	v_mul_u32_u24_e32 v122, 0x600, v136
	s_movk_i32 s10, 0xf0
	s_addc_u32 s7, s11, s7
	v_and_or_b32 v122, v135, s10, v122
	v_cvt_pk_bf16_f32 v110, v110, v111
	v_cvt_pk_bf16_f32 v111, v112, v113
	v_cvt_pk_bf16_f32 v112, v106, v107
	v_cvt_pk_bf16_f32 v113, v108, v109
	v_cvt_pk_bf16_f32 v129, v124, v125
	global_store_dwordx4 v122, v[110:113], s[6:7] offset:256
	v_cvt_pk_bf16_f32 v106, v118, v119
	v_cvt_pk_bf16_f32 v107, v120, v121
	v_cvt_pk_bf16_f32 v108, v114, v115
	v_cvt_pk_bf16_f32 v109, v116, v117
	v_add_u32_e32 v110, 0x6000, v122
	v_cvt_pk_bf16_f32 v92, v92, v93
	v_cvt_pk_bf16_f32 v93, v94, v95
	v_cvt_pk_bf16_f32 v94, v88, v89
	v_cvt_pk_bf16_f32 v95, v90, v91
	v_add_u32_e32 v88, 0x6100, v122
	global_store_dwordx4 v122, v[126:129], s[6:7]
	global_store_dwordx4 v110, v[106:109], s[6:7]
	global_store_dwordx4 v88, v[92:95], s[6:7]
	v_cvt_pk_bf16_f32 v88, v102, v103
	v_cvt_pk_bf16_f32 v89, v104, v105
	v_cvt_pk_bf16_f32 v90, v98, v99
	v_cvt_pk_bf16_f32 v91, v100, v101
	v_add_u32_e32 v92, 0xc000, v122
	v_cvt_pk_bf16_f32 v76, v76, v77
	v_cvt_pk_bf16_f32 v77, v78, v79
	v_cvt_pk_bf16_f32 v78, v72, v73
	v_cvt_pk_bf16_f32 v79, v74, v75
	v_add_u32_e32 v72, 0xc100, v122
	global_store_dwordx4 v92, v[88:91], s[6:7]
	global_store_dwordx4 v72, v[76:79], s[6:7]
	v_cvt_pk_bf16_f32 v72, v84, v85
	v_cvt_pk_bf16_f32 v73, v86, v87
	v_cvt_pk_bf16_f32 v74, v80, v81
	v_cvt_pk_bf16_f32 v75, v82, v83
	v_add_u32_e32 v76, 0x12000, v122
	v_cvt_pk_bf16_f32 v68, v68, v69
	v_cvt_pk_bf16_f32 v69, v70, v71
	v_cvt_pk_bf16_f32 v70, v64, v65
	v_cvt_pk_bf16_f32 v71, v66, v67
	v_cvt_pk_bf16_f32 v60, v60, v61
	v_cvt_pk_bf16_f32 v61, v62, v63
	v_cvt_pk_bf16_f32 v62, v56, v57
	v_cvt_pk_bf16_f32 v63, v58, v59
	v_add_u32_e32 v56, 0x30000, v122
	v_cvt_pk_bf16_f32 v44, v44, v45
	v_cvt_pk_bf16_f32 v45, v46, v47
	v_cvt_pk_bf16_f32 v46, v40, v41
	v_cvt_pk_bf16_f32 v47, v42, v43
	v_add_u32_e32 v40, 0x30100, v122
	global_store_dwordx4 v76, v[72:75], s[6:7]
	global_store_dwordx4 v76, v[68:71], s[6:7] offset:256
	global_store_dwordx4 v56, v[60:63], s[6:7]
	global_store_dwordx4 v40, v[44:47], s[6:7]
	v_cvt_pk_bf16_f32 v28, v28, v29
	v_cvt_pk_bf16_f32 v29, v30, v31
	v_add_u32_e32 v44, 0x36000, v122
	v_cvt_pk_bf16_f32 v30, v24, v25
	v_cvt_pk_bf16_f32 v31, v26, v27
	v_cvt_pk_bf16_f32 v40, v52, v53
	v_cvt_pk_bf16_f32 v41, v54, v55
	v_cvt_pk_bf16_f32 v42, v48, v49
	v_cvt_pk_bf16_f32 v43, v50, v51
	global_store_dwordx4 v44, v[28:31], s[6:7] offset:256
	v_cvt_pk_bf16_f32 v12, v12, v13
	v_cvt_pk_bf16_f32 v13, v14, v15
	v_add_u32_e32 v28, 0x3c000, v122
	v_cvt_pk_bf16_f32 v14, v8, v9
	v_cvt_pk_bf16_f32 v15, v10, v11
	global_store_dwordx4 v44, v[40:43], s[6:7]
	v_cvt_pk_bf16_f32 v24, v36, v37
	v_cvt_pk_bf16_f32 v25, v38, v39
	v_cvt_pk_bf16_f32 v26, v32, v33
	v_cvt_pk_bf16_f32 v27, v34, v35
	global_store_dwordx4 v28, v[12:15], s[6:7] offset:256
	v_cvt_pk_bf16_f32 v8, v20, v21
	v_cvt_pk_bf16_f32 v9, v22, v23
	v_cvt_pk_bf16_f32 v10, v16, v17
	v_cvt_pk_bf16_f32 v11, v18, v19
	v_add_u32_e32 v12, 0x42000, v122
	v_cvt_pk_bf16_f32 v4, v4, v5
	v_cvt_pk_bf16_f32 v5, v6, v7
	v_cvt_pk_bf16_f32 v6, v0, v1
	v_cvt_pk_bf16_f32 v7, v2, v3
	s_and_b64 vcc, exec, s[4:5]
	s_mov_b32 s40, s36
	s_mov_b32 s41, s37
	s_mov_b32 s10, s39
	s_mov_b32 s11, s38
	global_store_dwordx4 v28, v[24:27], s[6:7]
	global_store_dwordx4 v12, v[8:11], s[6:7]
	global_store_dwordx4 v12, v[4:7], s[6:7] offset:256
	s_cbranch_vccz .LBB0_481
	s_waitcnt vmcnt(0)
	s_cmpk_gt_u32 s14, 0xff
	s_cbranch_scc1 .LBB0_488
	s_barrier

.LBB0_493:
	ds_read_b128 v[6:9], v4
	ds_read_b128 v[10:13], v4 offset:1024
	ds_read_b128 v[14:17], v4 offset:2048
	ds_read_b128 v[18:21], v4 offset:3072
	s_mul_i32 s37, s36, 0x300000
	s_and_b64 s[10:11], s[6:7], exec
	s_cselect_b32 s41, s37, s42
	s_lshl_b32 s38, s35, 17
	s_and_b64 s[6:7], s[6:7], exec
	s_cselect_b32 s6, s38, s43
	s_add_i32 s10, s42, 0x180080
	s_or_b32 s44, s42, 0x100
	s_or_b32 s45, s43, 0x100
	s_or_b32 s7, s42, 0x180
	s_mov_b32 m0, s31
	ds_read_b128 v[22:25], v5
	ds_read_b128 v[26:29], v5 offset:1024
	ds_read_b128 v[30:33], v5 offset:2048
	ds_read_b128 v[34:37], v5 offset:3072
	ds_read_b128 v[38:41], v5 offset:4096
	ds_read_b128 v[42:45], v5 offset:5120
	ds_read_b128 v[46:49], v5 offset:6144
	ds_read_b128 v[50:53], v5 offset:7168
	buffer_load_dwordx4 v0, s[72:75], s10 offen lds
	s_mov_b32 m0, s34
	s_nop 0
	buffer_load_dwordx4 v2, s[72:75], s10 offen lds
	s_waitcnt lgkmcnt(8)
	s_barrier
	s_setprio 1
	s_waitcnt lgkmcnt(7)
	v_mfma_f32_16x16x32_bf16 v[54:57], v[6:9], v[22:25], 0
	v_mfma_f32_16x16x32_bf16 v[58:61], v[14:17], v[22:25], 0
	s_waitcnt lgkmcnt(5)
	v_mfma_f32_16x16x32_bf16 v[62:65], v[6:9], v[30:33], 0
	v_mfma_f32_16x16x32_bf16 v[66:69], v[14:17], v[30:33], 0
	s_waitcnt lgkmcnt(3)
	v_mfma_f32_16x16x32_bf16 v[70:73], v[6:9], v[38:41], 0
	v_mfma_f32_16x16x32_bf16 v[74:77], v[14:17], v[38:41], 0
	s_waitcnt lgkmcnt(1)
	v_mfma_f32_16x16x32_bf16 v[78:81], v[6:9], v[46:49], 0
	v_mfma_f32_16x16x32_bf16 v[82:85], v[14:17], v[46:49], 0
	v_mfma_f32_16x16x32_bf16 v[54:57], v[10:13], v[26:29], v[54:57]
	v_mfma_f32_16x16x32_bf16 v[58:61], v[18:21], v[26:29], v[58:61]
	v_mfma_f32_16x16x32_bf16 v[62:65], v[10:13], v[34:37], v[62:65]
	v_mfma_f32_16x16x32_bf16 v[66:69], v[18:21], v[34:37], v[66:69]
	v_mfma_f32_16x16x32_bf16 v[70:73], v[10:13], v[42:45], v[70:73]
	v_mfma_f32_16x16x32_bf16 v[74:77], v[18:21], v[42:45], v[74:77]
	s_waitcnt lgkmcnt(0)
	v_mfma_f32_16x16x32_bf16 v[78:81], v[10:13], v[50:53], v[78:81]
	v_mfma_f32_16x16x32_bf16 v[82:85], v[18:21], v[50:53], v[82:85]
	s_setprio 0
	s_barrier
	s_mov_b32 s10, s74
	s_mov_b32 s11, s75
	s_mov_b32 m0, s2
	ds_read_b128 v[86:89], v4 offset:16384
	ds_read_b128 v[90:93], v4 offset:17408
	ds_read_b128 v[98:101], v4 offset:18432
	ds_read_b128 v[102:105], v4 offset:19456
	buffer_load_dwordx4 v1, s[8:11], s45 offen lds
	s_mov_b32 m0, s17
	s_nop 0
	buffer_load_dwordx4 v3, s[8:11], s45 offen lds
	s_barrier
	s_setprio 1
	s_waitcnt lgkmcnt(3)
	v_mfma_f32_16x16x32_bf16 v[106:109], v[86:89], v[22:25], 0
	s_waitcnt lgkmcnt(1)
	v_mfma_f32_16x16x32_bf16 v[22:25], v[98:101], v[22:25], 0
	v_mfma_f32_16x16x32_bf16 v[106:109], v[90:93], v[26:29], v[106:109]
	s_waitcnt lgkmcnt(0)
	v_mfma_f32_16x16x32_bf16 v[22:25], v[102:105], v[26:29], v[22:25]
	v_mfma_f32_16x16x32_bf16 v[26:29], v[86:89], v[30:33], 0
	v_mfma_f32_16x16x32_bf16 v[30:33], v[98:101], v[30:33], 0
	v_mfma_f32_16x16x32_bf16 v[26:29], v[90:93], v[34:37], v[26:29]
	v_mfma_f32_16x16x32_bf16 v[30:33], v[102:105], v[34:37], v[30:33]
	v_mfma_f32_16x16x32_bf16 v[34:37], v[86:89], v[38:41], 0
	v_mfma_f32_16x16x32_bf16 v[38:41], v[98:101], v[38:41], 0
	v_mfma_f32_16x16x32_bf16 v[34:37], v[90:93], v[42:45], v[34:37]
	v_mfma_f32_16x16x32_bf16 v[38:41], v[102:105], v[42:45], v[38:41]
	v_mfma_f32_16x16x32_bf16 v[42:45], v[86:89], v[46:49], 0
	v_mfma_f32_16x16x32_bf16 v[46:49], v[98:101], v[46:49], 0
	v_mfma_f32_16x16x32_bf16 v[42:45], v[90:93], v[50:53], v[42:45]
	v_mfma_f32_16x16x32_bf16 v[46:49], v[102:105], v[50:53], v[46:49]
	s_setprio 0
	s_mov_b32 m0, s0
	s_barrier
	ds_read_b128 v[50:53], v5 offset:16384
	ds_read_b128 v[110:113], v5 offset:17408
	ds_read_b128 v[114:117], v5 offset:18432
	ds_read_b128 v[118:121], v5 offset:19456
	ds_read_b128 v[122:125], v5 offset:20480
	ds_read_b128 v[126:129], v5 offset:21504
	ds_read_b128 v[130:133], v5 offset:22528
	ds_read_b128 v[134:137], v5 offset:23552
	buffer_load_dwordx4 v0, s[72:75], s44 offen lds
	s_mov_b32 m0, s18
	s_nop 0
	buffer_load_dwordx4 v2, s[72:75], s44 offen lds
	s_barrier
	s_setprio 1
	s_waitcnt lgkmcnt(7)
	v_mfma_f32_16x16x32_bf16 v[138:141], v[6:9], v[50:53], 0
	s_waitcnt lgkmcnt(5)
	v_mfma_f32_16x16x32_bf16 v[146:149], v[6:9], v[114:117], 0
	s_waitcnt lgkmcnt(3)
	v_mfma_f32_16x16x32_bf16 v[154:157], v[6:9], v[122:125], 0
	s_waitcnt lgkmcnt(1)
	v_mfma_f32_16x16x32_bf16 v[6:9], v[6:9], v[130:133], 0
	v_mfma_f32_16x16x32_bf16 v[138:141], v[10:13], v[110:113], v[138:141]
	v_mfma_f32_16x16x32_bf16 v[142:145], v[14:17], v[50:53], 0
	v_mfma_f32_16x16x32_bf16 v[146:149], v[10:13], v[118:121], v[146:149]
	v_mfma_f32_16x16x32_bf16 v[150:153], v[14:17], v[114:117], 0
	v_mfma_f32_16x16x32_bf16 v[154:157], v[10:13], v[126:129], v[154:157]
	v_mfma_f32_16x16x32_bf16 v[158:161], v[14:17], v[122:125], 0
	s_waitcnt lgkmcnt(0)
	v_mfma_f32_16x16x32_bf16 v[6:9], v[10:13], v[134:137], v[6:9]
	v_mfma_f32_16x16x32_bf16 v[10:13], v[14:17], v[130:133], 0
	v_mfma_f32_16x16x32_bf16 v[142:145], v[18:21], v[110:113], v[142:145]
	v_mfma_f32_16x16x32_bf16 v[150:153], v[18:21], v[118:121], v[150:153]
	v_mfma_f32_16x16x32_bf16 v[158:161], v[18:21], v[126:129], v[158:161]
	v_mfma_f32_16x16x32_bf16 v[10:13], v[18:21], v[134:137], v[10:13]
	s_setprio 0
	s_barrier
	s_or_b32 s44, s43, 0x10100
	s_mov_b32 m0, s19
	s_nop 0
	buffer_load_dwordx4 v1, s[8:11], s44 offen lds
	s_mov_b32 m0, s20
	s_nop 0
	buffer_load_dwordx4 v3, s[8:11], s44 offen lds
	s_waitcnt vmcnt(6)
	s_barrier
	s_setprio 1
	v_mfma_f32_16x16x32_bf16 v[14:17], v[86:89], v[50:53], 0
	v_mfma_f32_16x16x32_bf16 v[18:21], v[98:101], v[50:53], 0
	v_mfma_f32_16x16x32_bf16 v[14:17], v[90:93], v[110:113], v[14:17]
	v_mfma_f32_16x16x32_bf16 v[18:21], v[102:105], v[110:113], v[18:21]
	v_mfma_f32_16x16x32_bf16 v[50:53], v[86:89], v[114:117], 0
	v_mfma_f32_16x16x32_bf16 v[110:113], v[98:101], v[114:117], 0
	v_mfma_f32_16x16x32_bf16 v[114:117], v[86:89], v[122:125], 0
	v_mfma_f32_16x16x32_bf16 v[86:89], v[86:89], v[130:133], 0
	v_mfma_f32_16x16x32_bf16 v[50:53], v[90:93], v[118:121], v[50:53]
	v_mfma_f32_16x16x32_bf16 v[110:113], v[102:105], v[118:121], v[110:113]
	v_mfma_f32_16x16x32_bf16 v[114:117], v[90:93], v[126:129], v[114:117]
	v_mfma_f32_16x16x32_bf16 v[118:121], v[98:101], v[122:125], 0
	v_mfma_f32_16x16x32_bf16 v[86:89], v[90:93], v[134:137], v[86:89]
	v_mfma_f32_16x16x32_bf16 v[90:93], v[98:101], v[130:133], 0
	v_mfma_f32_16x16x32_bf16 v[118:121], v[102:105], v[126:129], v[118:121]
	v_mfma_f32_16x16x32_bf16 v[90:93], v[102:105], v[134:137], v[90:93]
	s_setprio 0
	s_barrier
	ds_read_b128 v[98:101], v4 offset:32768
	ds_read_b128 v[102:105], v4 offset:33792
	ds_read_b128 v[122:125], v4 offset:34816
	ds_read_b128 v[126:129], v4 offset:35840
	s_add_i32 s44, s42, 0x180100
	s_mov_b32 m0, s21
	ds_read_b128 v[130:133], v5 offset:32768
	ds_read_b128 v[134:137], v5 offset:33792
	ds_read_b128 v[162:165], v5 offset:34816
	ds_read_b128 v[166:169], v5 offset:35840
	ds_read_b128 v[170:173], v5 offset:36864
	ds_read_b128 v[174:177], v5 offset:37888
	ds_read_b128 v[178:181], v5 offset:38912
	ds_read_b128 v[182:185], v5 offset:39936
	buffer_load_dwordx4 v0, s[72:75], s44 offen lds
	s_mov_b32 m0, s22
	s_nop 0
	buffer_load_dwordx4 v2, s[72:75], s44 offen lds
	s_waitcnt lgkmcnt(8)
	s_barrier
	s_setprio 1
	s_waitcnt lgkmcnt(7)
	v_mfma_f32_16x16x32_bf16 v[54:57], v[98:101], v[130:133], v[54:57]
	v_mfma_f32_16x16x32_bf16 v[58:61], v[122:125], v[130:133], v[58:61]
	s_waitcnt lgkmcnt(5)
	v_mfma_f32_16x16x32_bf16 v[62:65], v[98:101], v[162:165], v[62:65]
	v_mfma_f32_16x16x32_bf16 v[66:69], v[122:125], v[162:165], v[66:69]
	s_waitcnt lgkmcnt(3)
	v_mfma_f32_16x16x32_bf16 v[70:73], v[98:101], v[170:173], v[70:73]
	v_mfma_f32_16x16x32_bf16 v[74:77], v[122:125], v[170:173], v[74:77]
	s_waitcnt lgkmcnt(1)
	v_mfma_f32_16x16x32_bf16 v[78:81], v[98:101], v[178:181], v[78:81]
	v_mfma_f32_16x16x32_bf16 v[82:85], v[122:125], v[178:181], v[82:85]
	v_mfma_f32_16x16x32_bf16 v[54:57], v[102:105], v[134:137], v[54:57]
	v_mfma_f32_16x16x32_bf16 v[58:61], v[126:129], v[134:137], v[58:61]
	v_mfma_f32_16x16x32_bf16 v[62:65], v[102:105], v[166:169], v[62:65]
	v_mfma_f32_16x16x32_bf16 v[66:69], v[126:129], v[166:169], v[66:69]
	v_mfma_f32_16x16x32_bf16 v[70:73], v[102:105], v[174:177], v[70:73]
	v_mfma_f32_16x16x32_bf16 v[74:77], v[126:129], v[174:177], v[74:77]
	s_waitcnt lgkmcnt(0)
	v_mfma_f32_16x16x32_bf16 v[78:81], v[102:105], v[182:185], v[78:81]
	v_mfma_f32_16x16x32_bf16 v[82:85], v[126:129], v[182:185], v[82:85]
	s_setprio 0
	s_barrier
	s_or_b32 s44, s43, 0x180
	s_mov_b32 m0, s25
	ds_read_b128 v[186:189], v4 offset:49152
	ds_read_b128 v[190:193], v4 offset:50176
	ds_read_b128 v[194:197], v4 offset:51200
	ds_read_b128 v[198:201], v4 offset:52224
	buffer_load_dwordx4 v1, s[8:11], s44 offen lds
	s_mov_b32 m0, s26
	s_nop 0
	buffer_load_dwordx4 v3, s[8:11], s44 offen lds
	s_barrier
	s_setprio 1
	s_waitcnt lgkmcnt(3)
	v_mfma_f32_16x16x32_bf16 v[106:109], v[186:189], v[130:133], v[106:109]
	s_waitcnt lgkmcnt(1)
	v_mfma_f32_16x16x32_bf16 v[22:25], v[194:197], v[130:133], v[22:25]
	v_mfma_f32_16x16x32_bf16 v[26:29], v[186:189], v[162:165], v[26:29]
	v_mfma_f32_16x16x32_bf16 v[30:33], v[194:197], v[162:165], v[30:33]
	v_mfma_f32_16x16x32_bf16 v[34:37], v[186:189], v[170:173], v[34:37]
	v_mfma_f32_16x16x32_bf16 v[38:41], v[194:197], v[170:173], v[38:41]
	v_mfma_f32_16x16x32_bf16 v[42:45], v[186:189], v[178:181], v[42:45]
	v_mfma_f32_16x16x32_bf16 v[46:49], v[194:197], v[178:181], v[46:49]
	v_mfma_f32_16x16x32_bf16 v[106:109], v[190:193], v[134:137], v[106:109]
	s_waitcnt lgkmcnt(0)
	v_mfma_f32_16x16x32_bf16 v[22:25], v[198:201], v[134:137], v[22:25]
	v_mfma_f32_16x16x32_bf16 v[26:29], v[190:193], v[166:169], v[26:29]
	v_mfma_f32_16x16x32_bf16 v[30:33], v[198:201], v[166:169], v[30:33]
	v_mfma_f32_16x16x32_bf16 v[34:37], v[190:193], v[174:177], v[34:37]
	v_mfma_f32_16x16x32_bf16 v[38:41], v[198:201], v[174:177], v[38:41]
	v_mfma_f32_16x16x32_bf16 v[42:45], v[190:193], v[182:185], v[42:45]
	v_mfma_f32_16x16x32_bf16 v[46:49], v[198:201], v[182:185], v[46:49]
	s_setprio 0
	s_mov_b32 m0, s27
	s_barrier
	ds_read_b128 v[130:133], v5 offset:49152
	ds_read_b128 v[134:137], v5 offset:50176
	ds_read_b128 v[162:165], v5 offset:51200
	ds_read_b128 v[166:169], v5 offset:52224
	ds_read_b128 v[170:173], v5 offset:53248
	ds_read_b128 v[174:177], v5 offset:54272
	ds_read_b128 v[178:181], v5 offset:55296
	ds_read_b128 v[182:185], v5 offset:56320
	buffer_load_dwordx4 v0, s[72:75], s7 offen lds
	s_mov_b32 m0, s28
	s_nop 0
	buffer_load_dwordx4 v2, s[72:75], s7 offen lds
	s_barrier
	s_setprio 1
	s_waitcnt lgkmcnt(7)
	v_mfma_f32_16x16x32_bf16 v[138:141], v[98:101], v[130:133], v[138:141]
	v_mfma_f32_16x16x32_bf16 v[142:145], v[122:125], v[130:133], v[142:145]
	s_waitcnt lgkmcnt(5)
	v_mfma_f32_16x16x32_bf16 v[146:149], v[98:101], v[162:165], v[146:149]
	v_mfma_f32_16x16x32_bf16 v[150:153], v[122:125], v[162:165], v[150:153]
	s_waitcnt lgkmcnt(3)
	v_mfma_f32_16x16x32_bf16 v[154:157], v[98:101], v[170:173], v[154:157]
	v_mfma_f32_16x16x32_bf16 v[158:161], v[122:125], v[170:173], v[158:161]
	s_waitcnt lgkmcnt(1)
	v_mfma_f32_16x16x32_bf16 v[6:9], v[98:101], v[178:181], v[6:9]
	v_mfma_f32_16x16x32_bf16 v[10:13], v[122:125], v[178:181], v[10:13]
	v_mfma_f32_16x16x32_bf16 v[138:141], v[102:105], v[134:137], v[138:141]
	v_mfma_f32_16x16x32_bf16 v[142:145], v[126:129], v[134:137], v[142:145]
	v_mfma_f32_16x16x32_bf16 v[146:149], v[102:105], v[166:169], v[146:149]
	v_mfma_f32_16x16x32_bf16 v[150:153], v[126:129], v[166:169], v[150:153]
	v_mfma_f32_16x16x32_bf16 v[154:157], v[102:105], v[174:177], v[154:157]
	v_mfma_f32_16x16x32_bf16 v[158:161], v[126:129], v[174:177], v[158:161]
	s_waitcnt lgkmcnt(0)
	v_mfma_f32_16x16x32_bf16 v[6:9], v[102:105], v[182:185], v[6:9]
	v_mfma_f32_16x16x32_bf16 v[10:13], v[126:129], v[182:185], v[10:13]
	s_setprio 0
	s_barrier
	s_or_b32 s7, s43, 0x10180
	s_mov_b32 m0, s29
	s_nop 0
	buffer_load_dwordx4 v1, s[8:11], s7 offen lds
	s_mov_b32 m0, s30
	s_nop 0
	buffer_load_dwordx4 v3, s[8:11], s7 offen lds
	s_waitcnt vmcnt(6)
	s_barrier
	s_setprio 1
	v_mfma_f32_16x16x32_bf16 v[14:17], v[186:189], v[130:133], v[14:17]
	v_mfma_f32_16x16x32_bf16 v[18:21], v[194:197], v[130:133], v[18:21]
	v_mfma_f32_16x16x32_bf16 v[50:53], v[186:189], v[162:165], v[50:53]
	v_mfma_f32_16x16x32_bf16 v[98:101], v[194:197], v[162:165], v[110:113]
	v_mfma_f32_16x16x32_bf16 v[102:105], v[186:189], v[170:173], v[114:117]
	v_mfma_f32_16x16x32_bf16 v[110:113], v[194:197], v[170:173], v[118:121]
	v_mfma_f32_16x16x32_bf16 v[86:89], v[186:189], v[178:181], v[86:89]
	v_mfma_f32_16x16x32_bf16 v[90:93], v[194:197], v[178:181], v[90:93]
	v_mfma_f32_16x16x32_bf16 v[14:17], v[190:193], v[134:137], v[14:17]
	v_mfma_f32_16x16x32_bf16 v[18:21], v[198:201], v[134:137], v[18:21]
	v_mfma_f32_16x16x32_bf16 v[50:53], v[190:193], v[166:169], v[50:53]
	v_mfma_f32_16x16x32_bf16 v[98:101], v[198:201], v[166:169], v[98:101]
	v_mfma_f32_16x16x32_bf16 v[102:105], v[190:193], v[174:177], v[102:105]
	v_mfma_f32_16x16x32_bf16 v[110:113], v[198:201], v[174:177], v[110:113]
	v_mfma_f32_16x16x32_bf16 v[86:89], v[190:193], v[182:185], v[86:89]
	v_mfma_f32_16x16x32_bf16 v[90:93], v[198:201], v[182:185], v[90:93]
	s_setprio 0
	s_barrier
	ds_read_b128 v[114:117], v4
	ds_read_b128 v[118:121], v4 offset:1024
	ds_read_b128 v[122:125], v4 offset:2048
	ds_read_b128 v[126:129], v4 offset:3072
	s_or_b32 s7, s41, 0x80
	s_add_i32 s42, s42, 0x180180
	s_mov_b32 m0, s31
	ds_read_b128 v[130:133], v5
	ds_read_b128 v[134:137], v5 offset:1024
	ds_read_b128 v[162:165], v5 offset:2048
	ds_read_b128 v[166:169], v5 offset:3072
	ds_read_b128 v[170:173], v5 offset:4096
	ds_read_b128 v[174:177], v5 offset:5120
	ds_read_b128 v[178:181], v5 offset:6144
	ds_read_b128 v[182:185], v5 offset:7168
	buffer_load_dwordx4 v0, s[72:75], s42 offen lds
	s_mov_b32 m0, s34
	s_nop 0
	buffer_load_dwordx4 v2, s[72:75], s42 offen lds
	s_waitcnt lgkmcnt(8)
	s_barrier
	s_setprio 1
	s_waitcnt lgkmcnt(7)
	v_mfma_f32_16x16x32_bf16 v[54:57], v[114:117], v[130:133], v[54:57]
	v_mfma_f32_16x16x32_bf16 v[58:61], v[122:125], v[130:133], v[58:61]
	s_waitcnt lgkmcnt(5)
	v_mfma_f32_16x16x32_bf16 v[62:65], v[114:117], v[162:165], v[62:65]
	v_mfma_f32_16x16x32_bf16 v[66:69], v[122:125], v[162:165], v[66:69]
	s_waitcnt lgkmcnt(3)
	v_mfma_f32_16x16x32_bf16 v[70:73], v[114:117], v[170:173], v[70:73]
	v_mfma_f32_16x16x32_bf16 v[74:77], v[122:125], v[170:173], v[74:77]
	s_waitcnt lgkmcnt(1)
	v_mfma_f32_16x16x32_bf16 v[78:81], v[114:117], v[178:181], v[78:81]
	v_mfma_f32_16x16x32_bf16 v[82:85], v[122:125], v[178:181], v[82:85]
	v_mfma_f32_16x16x32_bf16 v[54:57], v[118:121], v[134:137], v[54:57]
	v_mfma_f32_16x16x32_bf16 v[58:61], v[126:129], v[134:137], v[58:61]
	v_mfma_f32_16x16x32_bf16 v[62:65], v[118:121], v[166:169], v[62:65]
	v_mfma_f32_16x16x32_bf16 v[66:69], v[126:129], v[166:169], v[66:69]
	v_mfma_f32_16x16x32_bf16 v[70:73], v[118:121], v[174:177], v[70:73]
	v_mfma_f32_16x16x32_bf16 v[74:77], v[126:129], v[174:177], v[74:77]
	s_waitcnt lgkmcnt(0)
	v_mfma_f32_16x16x32_bf16 v[78:81], v[118:121], v[182:185], v[78:81]
	v_mfma_f32_16x16x32_bf16 v[82:85], v[126:129], v[182:185], v[82:85]
	s_setprio 0
	s_barrier
	s_mov_b32 m0, s2
	ds_read_b128 v[186:189], v4 offset:16384
	ds_read_b128 v[190:193], v4 offset:17408
	ds_read_b128 v[194:197], v4 offset:18432
	ds_read_b128 v[198:201], v4 offset:19456
	buffer_load_dwordx4 v1, s[8:11], s6 offen lds
	s_mov_b32 m0, s17
	s_nop 0
	buffer_load_dwordx4 v3, s[8:11], s6 offen lds
	s_barrier
	s_setprio 1
	s_waitcnt lgkmcnt(3)
	v_mfma_f32_16x16x32_bf16 v[106:109], v[186:189], v[130:133], v[106:109]
	s_waitcnt lgkmcnt(1)
	v_mfma_f32_16x16x32_bf16 v[22:25], v[194:197], v[130:133], v[22:25]
	v_mfma_f32_16x16x32_bf16 v[26:29], v[186:189], v[162:165], v[26:29]
	v_mfma_f32_16x16x32_bf16 v[30:33], v[194:197], v[162:165], v[30:33]
	v_mfma_f32_16x16x32_bf16 v[34:37], v[186:189], v[170:173], v[34:37]
	v_mfma_f32_16x16x32_bf16 v[38:41], v[194:197], v[170:173], v[38:41]
	v_mfma_f32_16x16x32_bf16 v[42:45], v[186:189], v[178:181], v[42:45]
	v_mfma_f32_16x16x32_bf16 v[46:49], v[194:197], v[178:181], v[46:49]
	v_mfma_f32_16x16x32_bf16 v[106:109], v[190:193], v[134:137], v[106:109]
	s_waitcnt lgkmcnt(0)
	v_mfma_f32_16x16x32_bf16 v[22:25], v[198:201], v[134:137], v[22:25]
	v_mfma_f32_16x16x32_bf16 v[26:29], v[190:193], v[166:169], v[26:29]
	v_mfma_f32_16x16x32_bf16 v[30:33], v[198:201], v[166:169], v[30:33]
	v_mfma_f32_16x16x32_bf16 v[34:37], v[190:193], v[174:177], v[34:37]
	v_mfma_f32_16x16x32_bf16 v[38:41], v[198:201], v[174:177], v[38:41]
	v_mfma_f32_16x16x32_bf16 v[42:45], v[190:193], v[182:185], v[42:45]
	v_mfma_f32_16x16x32_bf16 v[46:49], v[198:201], v[182:185], v[46:49]
	s_setprio 0
	s_mov_b32 m0, s0
	s_barrier
	ds_read_b128 v[130:133], v5 offset:16384
	ds_read_b128 v[134:137], v5 offset:17408
	ds_read_b128 v[162:165], v5 offset:18432
	ds_read_b128 v[166:169], v5 offset:19456
	ds_read_b128 v[170:173], v5 offset:20480
	ds_read_b128 v[174:177], v5 offset:21504
	ds_read_b128 v[178:181], v5 offset:22528
	ds_read_b128 v[182:185], v5 offset:23552
	buffer_load_dwordx4 v0, s[72:75], s41 offen lds
	s_mov_b32 m0, s18
	s_nop 0
	buffer_load_dwordx4 v2, s[72:75], s41 offen lds
	s_barrier
	s_setprio 1
	s_waitcnt lgkmcnt(7)
	v_mfma_f32_16x16x32_bf16 v[138:141], v[114:117], v[130:133], v[138:141]
	v_mfma_f32_16x16x32_bf16 v[142:145], v[122:125], v[130:133], v[142:145]
	s_waitcnt lgkmcnt(5)
	v_mfma_f32_16x16x32_bf16 v[146:149], v[114:117], v[162:165], v[146:149]
	v_mfma_f32_16x16x32_bf16 v[150:153], v[122:125], v[162:165], v[150:153]
	s_waitcnt lgkmcnt(3)
	v_mfma_f32_16x16x32_bf16 v[154:157], v[114:117], v[170:173], v[154:157]
	v_mfma_f32_16x16x32_bf16 v[158:161], v[122:125], v[170:173], v[158:161]
	s_waitcnt lgkmcnt(1)
	v_mfma_f32_16x16x32_bf16 v[6:9], v[114:117], v[178:181], v[6:9]
	v_mfma_f32_16x16x32_bf16 v[10:13], v[122:125], v[178:181], v[10:13]
	v_mfma_f32_16x16x32_bf16 v[138:141], v[118:121], v[134:137], v[138:141]
	v_mfma_f32_16x16x32_bf16 v[142:145], v[126:129], v[134:137], v[142:145]
	v_mfma_f32_16x16x32_bf16 v[146:149], v[118:121], v[166:169], v[146:149]
	v_mfma_f32_16x16x32_bf16 v[150:153], v[126:129], v[166:169], v[150:153]
	v_mfma_f32_16x16x32_bf16 v[154:157], v[118:121], v[174:177], v[154:157]
	v_mfma_f32_16x16x32_bf16 v[158:161], v[126:129], v[174:177], v[158:161]
	s_waitcnt lgkmcnt(0)
	v_mfma_f32_16x16x32_bf16 v[6:9], v[118:121], v[182:185], v[6:9]
	v_mfma_f32_16x16x32_bf16 v[10:13], v[126:129], v[182:185], v[10:13]
	s_setprio 0
	s_barrier
	s_or_b32 s42, s6, 0x10000
	s_mov_b32 m0, s19
	s_nop 0
	buffer_load_dwordx4 v1, s[8:11], s42 offen lds
	s_mov_b32 m0, s20
	s_nop 0
	buffer_load_dwordx4 v3, s[8:11], s42 offen lds
	s_waitcnt vmcnt(6)
	s_barrier
	s_setprio 1
	v_mfma_f32_16x16x32_bf16 v[14:17], v[186:189], v[130:133], v[14:17]
	v_mfma_f32_16x16x32_bf16 v[18:21], v[194:197], v[130:133], v[18:21]
	v_mfma_f32_16x16x32_bf16 v[50:53], v[186:189], v[162:165], v[50:53]
	v_mfma_f32_16x16x32_bf16 v[98:101], v[194:197], v[162:165], v[98:101]
	v_mfma_f32_16x16x32_bf16 v[102:105], v[186:189], v[170:173], v[102:105]
	v_mfma_f32_16x16x32_bf16 v[110:113], v[194:197], v[170:173], v[110:113]
	v_mfma_f32_16x16x32_bf16 v[86:89], v[186:189], v[178:181], v[86:89]
	v_mfma_f32_16x16x32_bf16 v[90:93], v[194:197], v[178:181], v[90:93]
	v_mfma_f32_16x16x32_bf16 v[14:17], v[190:193], v[134:137], v[14:17]
	v_mfma_f32_16x16x32_bf16 v[18:21], v[198:201], v[134:137], v[18:21]
	v_mfma_f32_16x16x32_bf16 v[50:53], v[190:193], v[166:169], v[50:53]
	v_mfma_f32_16x16x32_bf16 v[98:101], v[198:201], v[166:169], v[98:101]
	v_mfma_f32_16x16x32_bf16 v[102:105], v[190:193], v[174:177], v[102:105]
	v_mfma_f32_16x16x32_bf16 v[110:113], v[198:201], v[174:177], v[110:113]
	v_mfma_f32_16x16x32_bf16 v[86:89], v[190:193], v[182:185], v[86:89]
	v_mfma_f32_16x16x32_bf16 v[90:93], v[198:201], v[182:185], v[90:93]
	s_setprio 0
	s_barrier
	ds_read_b128 v[114:117], v4 offset:32768
	ds_read_b128 v[118:121], v4 offset:33792
	ds_read_b128 v[122:125], v4 offset:34816
	ds_read_b128 v[126:129], v4 offset:35840
	s_add_i32 s41, s41, 0x180000
	s_mov_b32 m0, s21
	ds_read_b128 v[130:133], v5 offset:32768
	ds_read_b128 v[134:137], v5 offset:33792
	ds_read_b128 v[162:165], v5 offset:34816
	ds_read_b128 v[166:169], v5 offset:35840
	ds_read_b128 v[170:173], v5 offset:36864
	ds_read_b128 v[174:177], v5 offset:37888
	ds_read_b128 v[178:181], v5 offset:38912
	ds_read_b128 v[182:185], v5 offset:39936
	buffer_load_dwordx4 v0, s[72:75], s41 offen lds
	s_mov_b32 m0, s22
	s_nop 0
	buffer_load_dwordx4 v2, s[72:75], s41 offen lds
	s_waitcnt lgkmcnt(8)
	s_barrier
	s_setprio 1
	s_waitcnt lgkmcnt(7)
	v_mfma_f32_16x16x32_bf16 v[54:57], v[114:117], v[130:133], v[54:57]
	v_mfma_f32_16x16x32_bf16 v[58:61], v[122:125], v[130:133], v[58:61]
	s_waitcnt lgkmcnt(5)
	v_mfma_f32_16x16x32_bf16 v[62:65], v[114:117], v[162:165], v[62:65]
	v_mfma_f32_16x16x32_bf16 v[66:69], v[122:125], v[162:165], v[66:69]
	s_waitcnt lgkmcnt(3)
	v_mfma_f32_16x16x32_bf16 v[70:73], v[114:117], v[170:173], v[70:73]
	v_mfma_f32_16x16x32_bf16 v[74:77], v[122:125], v[170:173], v[74:77]
	s_waitcnt lgkmcnt(1)
	v_mfma_f32_16x16x32_bf16 v[78:81], v[114:117], v[178:181], v[78:81]
	v_mfma_f32_16x16x32_bf16 v[82:85], v[122:125], v[178:181], v[82:85]
	v_mfma_f32_16x16x32_bf16 v[54:57], v[118:121], v[134:137], v[54:57]
	v_mfma_f32_16x16x32_bf16 v[58:61], v[126:129], v[134:137], v[58:61]
	v_mfma_f32_16x16x32_bf16 v[62:65], v[118:121], v[166:169], v[62:65]
	v_mfma_f32_16x16x32_bf16 v[66:69], v[126:129], v[166:169], v[66:69]
	v_mfma_f32_16x16x32_bf16 v[70:73], v[118:121], v[174:177], v[70:73]
	v_mfma_f32_16x16x32_bf16 v[74:77], v[126:129], v[174:177], v[74:77]
	s_waitcnt lgkmcnt(0)
	v_mfma_f32_16x16x32_bf16 v[78:81], v[118:121], v[182:185], v[78:81]
	v_mfma_f32_16x16x32_bf16 v[82:85], v[126:129], v[182:185], v[82:85]
	s_setprio 0
	s_barrier
	s_or_b32 s41, s6, 0x80
	s_mov_b32 m0, s25
	ds_read_b128 v[186:189], v4 offset:49152
	ds_read_b128 v[190:193], v4 offset:50176
	ds_read_b128 v[194:197], v4 offset:51200
	ds_read_b128 v[198:201], v4 offset:52224
	buffer_load_dwordx4 v1, s[8:11], s41 offen lds
	s_mov_b32 m0, s26
	s_nop 0
	buffer_load_dwordx4 v3, s[8:11], s41 offen lds
	s_barrier
	s_setprio 1
	s_waitcnt lgkmcnt(3)
	v_mfma_f32_16x16x32_bf16 v[106:109], v[186:189], v[130:133], v[106:109]
	s_waitcnt lgkmcnt(1)
	v_mfma_f32_16x16x32_bf16 v[22:25], v[194:197], v[130:133], v[22:25]
	v_mfma_f32_16x16x32_bf16 v[26:29], v[186:189], v[162:165], v[26:29]
	v_mfma_f32_16x16x32_bf16 v[30:33], v[194:197], v[162:165], v[30:33]
	v_mfma_f32_16x16x32_bf16 v[34:37], v[186:189], v[170:173], v[34:37]
	v_mfma_f32_16x16x32_bf16 v[38:41], v[194:197], v[170:173], v[38:41]
	v_mfma_f32_16x16x32_bf16 v[42:45], v[186:189], v[178:181], v[42:45]
	v_mfma_f32_16x16x32_bf16 v[46:49], v[194:197], v[178:181], v[46:49]
	v_mfma_f32_16x16x32_bf16 v[106:109], v[190:193], v[134:137], v[106:109]
	s_waitcnt lgkmcnt(0)
	v_mfma_f32_16x16x32_bf16 v[22:25], v[198:201], v[134:137], v[22:25]
	v_mfma_f32_16x16x32_bf16 v[26:29], v[190:193], v[166:169], v[26:29]
	v_mfma_f32_16x16x32_bf16 v[30:33], v[198:201], v[166:169], v[30:33]
	v_mfma_f32_16x16x32_bf16 v[34:37], v[190:193], v[174:177], v[34:37]
	v_mfma_f32_16x16x32_bf16 v[38:41], v[198:201], v[174:177], v[38:41]
	v_mfma_f32_16x16x32_bf16 v[42:45], v[190:193], v[182:185], v[42:45]
	v_mfma_f32_16x16x32_bf16 v[46:49], v[198:201], v[182:185], v[46:49]
	s_setprio 0
	s_mov_b32 m0, s27
	s_barrier
	ds_read_b128 v[130:133], v5 offset:49152
	ds_read_b128 v[134:137], v5 offset:50176
	ds_read_b128 v[162:165], v5 offset:51200
	ds_read_b128 v[166:169], v5 offset:52224
	ds_read_b128 v[170:173], v5 offset:53248
	ds_read_b128 v[174:177], v5 offset:54272
	ds_read_b128 v[178:181], v5 offset:55296
	ds_read_b128 v[182:185], v5 offset:56320
	buffer_load_dwordx4 v0, s[72:75], s7 offen lds
	s_mov_b32 m0, s28
	s_nop 0
	buffer_load_dwordx4 v2, s[72:75], s7 offen lds
	s_barrier
	s_setprio 1
	s_waitcnt lgkmcnt(7)
	v_mfma_f32_16x16x32_bf16 v[138:141], v[114:117], v[130:133], v[138:141]
	v_mfma_f32_16x16x32_bf16 v[142:145], v[122:125], v[130:133], v[142:145]
	s_waitcnt lgkmcnt(5)
	v_mfma_f32_16x16x32_bf16 v[146:149], v[114:117], v[162:165], v[146:149]
	v_mfma_f32_16x16x32_bf16 v[150:153], v[122:125], v[162:165], v[150:153]
	s_waitcnt lgkmcnt(3)
	v_mfma_f32_16x16x32_bf16 v[154:157], v[114:117], v[170:173], v[154:157]
	v_mfma_f32_16x16x32_bf16 v[158:161], v[122:125], v[170:173], v[158:161]
	s_waitcnt lgkmcnt(1)
	v_mfma_f32_16x16x32_bf16 v[6:9], v[114:117], v[178:181], v[6:9]
	v_mfma_f32_16x16x32_bf16 v[10:13], v[122:125], v[178:181], v[10:13]
	v_mfma_f32_16x16x32_bf16 v[138:141], v[118:121], v[134:137], v[138:141]
	v_mfma_f32_16x16x32_bf16 v[142:145], v[126:129], v[134:137], v[142:145]
	v_mfma_f32_16x16x32_bf16 v[146:149], v[118:121], v[166:169], v[146:149]
	v_mfma_f32_16x16x32_bf16 v[150:153], v[126:129], v[166:169], v[150:153]
	v_mfma_f32_16x16x32_bf16 v[154:157], v[118:121], v[174:177], v[154:157]
	v_mfma_f32_16x16x32_bf16 v[158:161], v[126:129], v[174:177], v[158:161]
	s_waitcnt lgkmcnt(0)
	v_mfma_f32_16x16x32_bf16 v[6:9], v[118:121], v[182:185], v[6:9]
	v_mfma_f32_16x16x32_bf16 v[10:13], v[126:129], v[182:185], v[10:13]
	s_setprio 0
	s_barrier
	s_or_b32 s6, s6, 0x10080
	s_mov_b32 m0, s29
	s_nop 0
	buffer_load_dwordx4 v1, s[8:11], s6 offen lds
	s_mov_b32 m0, s30
	s_nop 0
	buffer_load_dwordx4 v3, s[8:11], s6 offen lds
	s_waitcnt vmcnt(6)
	s_barrier
	s_setprio 1
	v_mfma_f32_16x16x32_bf16 v[14:17], v[186:189], v[130:133], v[14:17]
	v_mfma_f32_16x16x32_bf16 v[18:21], v[194:197], v[130:133], v[18:21]
	v_mfma_f32_16x16x32_bf16 v[50:53], v[186:189], v[162:165], v[50:53]
	v_mfma_f32_16x16x32_bf16 v[98:101], v[194:197], v[162:165], v[98:101]
	v_mfma_f32_16x16x32_bf16 v[102:105], v[186:189], v[170:173], v[102:105]
	v_mfma_f32_16x16x32_bf16 v[110:113], v[194:197], v[170:173], v[110:113]
	v_mfma_f32_16x16x32_bf16 v[86:89], v[186:189], v[178:181], v[86:89]
	v_mfma_f32_16x16x32_bf16 v[90:93], v[194:197], v[178:181], v[90:93]
	v_mfma_f32_16x16x32_bf16 v[14:17], v[190:193], v[134:137], v[14:17]
	v_mfma_f32_16x16x32_bf16 v[18:21], v[198:201], v[134:137], v[18:21]
	v_mfma_f32_16x16x32_bf16 v[50:53], v[190:193], v[166:169], v[50:53]
	v_mfma_f32_16x16x32_bf16 v[98:101], v[198:201], v[166:169], v[98:101]
	v_mfma_f32_16x16x32_bf16 v[102:105], v[190:193], v[174:177], v[102:105]
	v_mfma_f32_16x16x32_bf16 v[110:113], v[198:201], v[174:177], v[110:113]
	v_mfma_f32_16x16x32_bf16 v[86:89], v[190:193], v[182:185], v[86:89]
	v_mfma_f32_16x16x32_bf16 v[90:93], v[198:201], v[182:185], v[90:93]
	s_setprio 0
	s_barrier
	s_getreg_b32 s6, hwreg(HW_REG_HW_ID, 0, 6)
	s_and_b32 s6, s6, 63
	s_lshl_b32 s6, s6, 2
	s_add_i32 s6, s6, 0
	s_add_i32 s6, s6, 0x20010
	v_mov_b32_e32 v94, s6
	ds_read_b32 v94, v94
	s_lshl_b32 s6, s40, 8
	v_mbcnt_lo_u32_b32 v95, -1, 0
	v_mbcnt_hi_u32_b32 v95, -1, v95
	v_cvt_pk_bf16_f32 v54, v54, v55
	v_and_b32_e32 v96, 15, v95
	s_waitcnt lgkmcnt(0)
	v_readfirstlane_b32 s7, v94
	s_lshl_b32 s10, s7, 6
	s_ashr_i32 s7, s6, 31
	s_lshl_b64 s[6:7], s[6:7], 11
	s_add_u32 s11, s23, s6
	s_addc_u32 s40, s24, s7
	s_lshl_b32 s6, s39, 8
	s_ashr_i32 s7, s6, 31
	v_or_b32_e32 v94, s10, v95
	s_lshl_b64 s[6:7], s[6:7], 1
	s_add_u32 s6, s11, s6
	v_lshrrev_b32_e32 v94, 2, v94
	s_mov_b32 s11, 0x1fffc0
	v_and_or_b32 v94, v94, s11, v96
	v_mov_b32_e32 v96, 0xf0
	v_lshlrev_b32_e32 v94, 11, v94
	v_bitop3_b32 v95, s10, v96, v95 bitop3:0xc8
	s_addc_u32 s7, s40, s7
	v_cvt_pk_bf16_f32 v55, v56, v57
	v_cvt_pk_bf16_f32 v56, v58, v59
	v_cvt_pk_bf16_f32 v57, v60, v61
	v_or_b32_e32 v96, v94, v95
	global_store_dwordx4 v96, v[54:57], s[6:7]
	v_lshl_add_u64 v[58:59], s[6:7], 0, v[96:97]
	s_mov_b32 s10, 0x8000
	v_cvt_pk_bf16_f32 v54, v106, v107
	v_cvt_pk_bf16_f32 v55, v108, v109
	v_cvt_pk_bf16_f32 v56, v22, v23
	v_cvt_pk_bf16_f32 v57, v24, v25
	global_store_dwordx4 v96, v[54:57], s[6:7] offset:256
	v_cvt_pk_bf16_f32 v22, v62, v63
	v_cvt_pk_bf16_f32 v23, v64, v65
	v_cvt_pk_bf16_f32 v24, v66, v67
	v_cvt_pk_bf16_f32 v25, v68, v69
	v_or_b32_e32 v54, 0x8000, v96
	global_store_dwordx4 v54, v[22:25], s[6:7]
	v_or_b32_e32 v60, 0x100, v95
	v_or_b32_e32 v61, v94, v60
	v_cvt_pk_bf16_f32 v22, v26, v27
	v_add_co_u32_e32 v26, vcc, s10, v58
	v_cvt_pk_bf16_f32 v23, v28, v29
	v_cvt_pk_bf16_f32 v24, v30, v31
	v_cvt_pk_bf16_f32 v25, v32, v33
	v_addc_co_u32_e32 v27, vcc, 0, v59, vcc
	global_store_dwordx4 v[26:27], v[22:25], off offset:256
	v_or_b32_e32 v26, 0x10000, v96
	s_mov_b32 s10, 0x10000
	v_cvt_pk_bf16_f32 v22, v70, v71
	v_cvt_pk_bf16_f32 v23, v72, v73
	v_cvt_pk_bf16_f32 v24, v74, v75
	v_cvt_pk_bf16_f32 v25, v76, v77
	global_store_dwordx4 v26, v[22:25], s[6:7]
	v_add_co_u32_e32 v26, vcc, s10, v58
	s_nop 0
	v_cvt_pk_bf16_f32 v22, v34, v35
	v_cvt_pk_bf16_f32 v23, v36, v37
	v_cvt_pk_bf16_f32 v24, v38, v39
	v_cvt_pk_bf16_f32 v25, v40, v41
	v_addc_co_u32_e32 v27, vcc, 0, v59, vcc
	global_store_dwordx4 v[26:27], v[22:25], off offset:256
	v_or_b32_e32 v26, 0x18000, v94
	v_or_b32_e32 v27, v26, v95
	v_cvt_pk_bf16_f32 v22, v78, v79
	v_cvt_pk_bf16_f32 v23, v80, v81
	v_cvt_pk_bf16_f32 v24, v82, v83
	v_cvt_pk_bf16_f32 v25, v84, v85
	global_store_dwordx4 v27, v[22:25], s[6:7]
	v_or_b32_e32 v26, v26, v60
	v_cvt_pk_bf16_f32 v14, v14, v15
	v_cvt_pk_bf16_f32 v22, v42, v43
	v_cvt_pk_bf16_f32 v23, v44, v45
	v_cvt_pk_bf16_f32 v24, v46, v47
	v_cvt_pk_bf16_f32 v25, v48, v49
	global_store_dwordx4 v26, v[22:25], s[6:7]
	v_add_u32_e32 v26, 0x40000, v96
	v_cvt_pk_bf16_f32 v15, v16, v17
	v_cvt_pk_bf16_f32 v22, v138, v139
	v_cvt_pk_bf16_f32 v23, v140, v141
	v_cvt_pk_bf16_f32 v24, v142, v143
	v_cvt_pk_bf16_f32 v25, v144, v145
	v_cvt_pk_bf16_f32 v16, v18, v19
	v_cvt_pk_bf16_f32 v17, v20, v21
	v_add_u32_e32 v18, 0x40000, v61
	global_store_dwordx4 v26, v[22:25], s[6:7]
	global_store_dwordx4 v18, v[14:17], s[6:7]
	v_add_u32_e32 v18, 0x48000, v96
	v_cvt_pk_bf16_f32 v6, v6, v7
	v_cvt_pk_bf16_f32 v14, v146, v147
	v_cvt_pk_bf16_f32 v15, v148, v149
	v_cvt_pk_bf16_f32 v16, v150, v151
	v_cvt_pk_bf16_f32 v17, v152, v153
	global_store_dwordx4 v18, v[14:17], s[6:7]
	v_cvt_pk_bf16_f32 v7, v8, v9
	v_cvt_pk_bf16_f32 v8, v10, v11
	v_cvt_pk_bf16_f32 v14, v50, v51
	v_cvt_pk_bf16_f32 v15, v52, v53
	v_cvt_pk_bf16_f32 v16, v98, v99
	v_cvt_pk_bf16_f32 v17, v100, v101
	global_store_dwordx4 v18, v[14:17], s[6:7] offset:256
	v_add_u32_e32 v18, 0x50000, v96
	v_cvt_pk_bf16_f32 v9, v12, v13
	v_cvt_pk_bf16_f32 v14, v154, v155
	v_cvt_pk_bf16_f32 v15, v156, v157
	v_cvt_pk_bf16_f32 v16, v158, v159
	v_cvt_pk_bf16_f32 v17, v160, v161
	global_store_dwordx4 v18, v[14:17], s[6:7]
	v_add_u32_e32 v10, 0x58000, v96
	s_andn2_b64 vcc, exec, s[4:5]
	v_cvt_pk_bf16_f32 v14, v102, v103
	v_cvt_pk_bf16_f32 v15, v104, v105
	v_cvt_pk_bf16_f32 v16, v110, v111
	v_cvt_pk_bf16_f32 v17, v112, v113
	global_store_dwordx4 v18, v[14:17], s[6:7] offset:256
	global_store_dwordx4 v10, v[6:9], s[6:7]
	s_mov_b32 s39, s35
	s_mov_b32 s40, s36
	v_cvt_pk_bf16_f32 v6, v86, v87
	v_cvt_pk_bf16_f32 v7, v88, v89
	v_cvt_pk_bf16_f32 v8, v90, v91
	v_cvt_pk_bf16_f32 v9, v92, v93
	s_mov_b32 s43, s38
	s_mov_b32 s42, s37
	global_store_dwordx4 v10, v[6:9], s[6:7] offset:256
	s_cbranch_vccz .LBB0_496

.LBB0_1358:
	ds_read_b128 v[138:141], v135
	ds_read_b128 v[142:145], v135 offset:1024
	ds_read_b128 v[146:149], v135 offset:2048
	ds_read_b128 v[150:153], v135 offset:3072
	s_add_i32 s10, s45, 0xfff80080
	s_cmp_eq_u32 s47, 4
	s_cselect_b32 s50, s15, s10
	s_cselect_b32 s48, s44, s46
	s_add_i32 s49, s50, 0x80
	s_mov_b32 m0, s38
	ds_read_b128 v[154:157], v136
	ds_read_b128 v[158:161], v136 offset:1024
	ds_read_b128 v[162:165], v136 offset:2048
	ds_read_b128 v[166:169], v136 offset:3072
	ds_read_b128 v[170:173], v136 offset:4096
	ds_read_b128 v[174:177], v136 offset:5120
	ds_read_b128 v[178:181], v136 offset:6144
	ds_read_b128 v[182:185], v136 offset:7168
	buffer_load_dwordx4 v131, s[72:75], s45 offen lds
	s_mov_b32 m0, s39
	s_nop 0
	buffer_load_dwordx4 v133, s[72:75], s45 offen lds
	s_waitcnt lgkmcnt(8)
	s_barrier
	s_setprio 1
	s_waitcnt lgkmcnt(7)
	v_mfma_f32_16x16x32_bf16 v[126:129], v[138:141], v[154:157], v[126:129]
	v_mfma_f32_16x16x32_bf16 v[122:125], v[146:149], v[154:157], v[122:125]
	s_waitcnt lgkmcnt(5)
	v_mfma_f32_16x16x32_bf16 v[118:121], v[138:141], v[162:165], v[118:121]
	v_mfma_f32_16x16x32_bf16 v[114:117], v[146:149], v[162:165], v[114:117]
	s_waitcnt lgkmcnt(3)
	v_mfma_f32_16x16x32_bf16 v[102:105], v[138:141], v[170:173], v[102:105]
	v_mfma_f32_16x16x32_bf16 v[98:101], v[146:149], v[170:173], v[98:101]
	s_waitcnt lgkmcnt(1)
	v_mfma_f32_16x16x32_bf16 v[84:87], v[138:141], v[178:181], v[84:87]
	v_mfma_f32_16x16x32_bf16 v[80:83], v[146:149], v[178:181], v[80:83]
	v_mfma_f32_16x16x32_bf16 v[126:129], v[142:145], v[158:161], v[126:129]
	v_mfma_f32_16x16x32_bf16 v[122:125], v[150:153], v[158:161], v[122:125]
	v_mfma_f32_16x16x32_bf16 v[118:121], v[142:145], v[166:169], v[118:121]
	v_mfma_f32_16x16x32_bf16 v[114:117], v[150:153], v[166:169], v[114:117]
	v_mfma_f32_16x16x32_bf16 v[102:105], v[142:145], v[174:177], v[102:105]
	v_mfma_f32_16x16x32_bf16 v[98:101], v[150:153], v[174:177], v[98:101]
	s_waitcnt lgkmcnt(0)
	v_mfma_f32_16x16x32_bf16 v[84:87], v[142:145], v[182:185], v[84:87]
	v_mfma_f32_16x16x32_bf16 v[80:83], v[150:153], v[182:185], v[80:83]
	s_setprio 0
	s_barrier
	s_mov_b32 s10, s74
	s_mov_b32 s11, s75
	s_mov_b32 m0, s21
	ds_read_b128 v[186:189], v135 offset:16384
	ds_read_b128 v[190:193], v135 offset:17408
	ds_read_b128 v[194:197], v135 offset:18432
	ds_read_b128 v[198:201], v135 offset:19456
	buffer_load_dwordx4 v132, s[8:11], s48 offen lds
	s_mov_b32 m0, s22
	s_nop 0
	buffer_load_dwordx4 v134, s[8:11], s48 offen lds
	s_barrier
	s_setprio 1
	s_waitcnt lgkmcnt(3)
	v_mfma_f32_16x16x32_bf16 v[110:113], v[186:189], v[154:157], v[110:113]
	s_waitcnt lgkmcnt(1)
	v_mfma_f32_16x16x32_bf16 v[106:109], v[194:197], v[154:157], v[106:109]
	v_mfma_f32_16x16x32_bf16 v[92:95], v[186:189], v[162:165], v[92:95]
	v_mfma_f32_16x16x32_bf16 v[88:91], v[194:197], v[162:165], v[88:91]
	v_mfma_f32_16x16x32_bf16 v[76:79], v[186:189], v[170:173], v[76:79]
	v_mfma_f32_16x16x32_bf16 v[72:75], v[194:197], v[170:173], v[72:75]
	v_mfma_f32_16x16x32_bf16 v[68:71], v[186:189], v[178:181], v[68:71]
	v_mfma_f32_16x16x32_bf16 v[64:67], v[194:197], v[178:181], v[64:67]
	v_mfma_f32_16x16x32_bf16 v[110:113], v[190:193], v[158:161], v[110:113]
	s_waitcnt lgkmcnt(0)
	v_mfma_f32_16x16x32_bf16 v[106:109], v[198:201], v[158:161], v[106:109]
	v_mfma_f32_16x16x32_bf16 v[92:95], v[190:193], v[166:169], v[92:95]
	v_mfma_f32_16x16x32_bf16 v[88:91], v[198:201], v[166:169], v[88:91]
	v_mfma_f32_16x16x32_bf16 v[76:79], v[190:193], v[174:177], v[76:79]
	v_mfma_f32_16x16x32_bf16 v[72:75], v[198:201], v[174:177], v[72:75]
	v_mfma_f32_16x16x32_bf16 v[68:71], v[190:193], v[182:185], v[68:71]
	v_mfma_f32_16x16x32_bf16 v[64:67], v[198:201], v[182:185], v[64:67]
	s_setprio 0
	s_mov_b32 m0, s2
	s_barrier
	ds_read_b128 v[154:157], v136 offset:16384
	ds_read_b128 v[158:161], v136 offset:17408
	ds_read_b128 v[162:165], v136 offset:18432
	ds_read_b128 v[166:169], v136 offset:19456
	ds_read_b128 v[170:173], v136 offset:20480
	ds_read_b128 v[174:177], v136 offset:21504
	ds_read_b128 v[178:181], v136 offset:22528
	ds_read_b128 v[182:185], v136 offset:23552
	buffer_load_dwordx4 v131, s[72:75], s50 offen lds
	s_mov_b32 m0, s23
	s_nop 0
	buffer_load_dwordx4 v133, s[72:75], s50 offen lds
	s_barrier
	s_setprio 1
	s_waitcnt lgkmcnt(7)
	v_mfma_f32_16x16x32_bf16 v[60:63], v[138:141], v[154:157], v[60:63]
	v_mfma_f32_16x16x32_bf16 v[56:59], v[146:149], v[154:157], v[56:59]
	s_waitcnt lgkmcnt(5)
	v_mfma_f32_16x16x32_bf16 v[52:55], v[138:141], v[162:165], v[52:55]
	v_mfma_f32_16x16x32_bf16 v[48:51], v[146:149], v[162:165], v[48:51]
	s_waitcnt lgkmcnt(3)
	v_mfma_f32_16x16x32_bf16 v[36:39], v[138:141], v[170:173], v[36:39]
	v_mfma_f32_16x16x32_bf16 v[32:35], v[146:149], v[170:173], v[32:35]
	s_waitcnt lgkmcnt(1)
	v_mfma_f32_16x16x32_bf16 v[20:23], v[138:141], v[178:181], v[20:23]
	v_mfma_f32_16x16x32_bf16 v[16:19], v[146:149], v[178:181], v[16:19]
	v_mfma_f32_16x16x32_bf16 v[60:63], v[142:145], v[158:161], v[60:63]
	v_mfma_f32_16x16x32_bf16 v[56:59], v[150:153], v[158:161], v[56:59]
	v_mfma_f32_16x16x32_bf16 v[52:55], v[142:145], v[166:169], v[52:55]
	v_mfma_f32_16x16x32_bf16 v[48:51], v[150:153], v[166:169], v[48:51]
	v_mfma_f32_16x16x32_bf16 v[36:39], v[142:145], v[174:177], v[36:39]
	v_mfma_f32_16x16x32_bf16 v[32:35], v[150:153], v[174:177], v[32:35]
	s_waitcnt lgkmcnt(0)
	v_mfma_f32_16x16x32_bf16 v[20:23], v[142:145], v[182:185], v[20:23]
	v_mfma_f32_16x16x32_bf16 v[16:19], v[150:153], v[182:185], v[16:19]
	s_setprio 0
	s_barrier
	s_add_i32 s51, s48, 0x20000
	s_mov_b32 m0, s24
	s_nop 0
	buffer_load_dwordx4 v132, s[8:11], s51 offen lds
	s_mov_b32 m0, s25
	s_nop 0
	buffer_load_dwordx4 v134, s[8:11], s51 offen lds
	s_waitcnt vmcnt(6)
	s_barrier
	s_setprio 1
	v_mfma_f32_16x16x32_bf16 v[44:47], v[186:189], v[154:157], v[44:47]
	v_mfma_f32_16x16x32_bf16 v[40:43], v[194:197], v[154:157], v[40:43]
	v_mfma_f32_16x16x32_bf16 v[28:31], v[186:189], v[162:165], v[28:31]
	v_mfma_f32_16x16x32_bf16 v[24:27], v[194:197], v[162:165], v[24:27]
	v_mfma_f32_16x16x32_bf16 v[12:15], v[186:189], v[170:173], v[12:15]
	v_mfma_f32_16x16x32_bf16 v[8:11], v[194:197], v[170:173], v[8:11]
	v_mfma_f32_16x16x32_bf16 v[4:7], v[186:189], v[178:181], v[4:7]
	v_mfma_f32_16x16x32_bf16 v[0:3], v[194:197], v[178:181], v[0:3]
	v_mfma_f32_16x16x32_bf16 v[44:47], v[190:193], v[158:161], v[44:47]
	v_mfma_f32_16x16x32_bf16 v[40:43], v[198:201], v[158:161], v[40:43]
	v_mfma_f32_16x16x32_bf16 v[28:31], v[190:193], v[166:169], v[28:31]
	v_mfma_f32_16x16x32_bf16 v[24:27], v[198:201], v[166:169], v[24:27]
	v_mfma_f32_16x16x32_bf16 v[12:15], v[190:193], v[174:177], v[12:15]
	v_mfma_f32_16x16x32_bf16 v[8:11], v[198:201], v[174:177], v[8:11]
	v_mfma_f32_16x16x32_bf16 v[4:7], v[190:193], v[182:185], v[4:7]
	v_mfma_f32_16x16x32_bf16 v[0:3], v[198:201], v[182:185], v[0:3]
	s_setprio 0
	s_barrier
	ds_read_b128 v[138:141], v135 offset:32768
	ds_read_b128 v[142:145], v135 offset:33792
	ds_read_b128 v[146:149], v135 offset:34816
	ds_read_b128 v[150:153], v135 offset:35840
	s_add_i32 s50, s50, 0x80000
	s_mov_b32 m0, s26
	ds_read_b128 v[154:157], v136 offset:32768
	ds_read_b128 v[158:161], v136 offset:33792
	ds_read_b128 v[162:165], v136 offset:34816
	ds_read_b128 v[166:169], v136 offset:35840
	ds_read_b128 v[170:173], v136 offset:36864
	ds_read_b128 v[174:177], v136 offset:37888
	ds_read_b128 v[178:181], v136 offset:38912
	ds_read_b128 v[182:185], v136 offset:39936
	buffer_load_dwordx4 v131, s[72:75], s50 offen lds
	s_mov_b32 m0, s27
	s_nop 0
	buffer_load_dwordx4 v133, s[72:75], s50 offen lds
	s_waitcnt lgkmcnt(8)
	s_barrier
	s_setprio 1
	s_waitcnt lgkmcnt(7)
	v_mfma_f32_16x16x32_bf16 v[126:129], v[138:141], v[154:157], v[126:129]
	v_mfma_f32_16x16x32_bf16 v[122:125], v[146:149], v[154:157], v[122:125]
	s_waitcnt lgkmcnt(5)
	v_mfma_f32_16x16x32_bf16 v[118:121], v[138:141], v[162:165], v[118:121]
	v_mfma_f32_16x16x32_bf16 v[114:117], v[146:149], v[162:165], v[114:117]
	s_waitcnt lgkmcnt(3)
	v_mfma_f32_16x16x32_bf16 v[102:105], v[138:141], v[170:173], v[102:105]
	v_mfma_f32_16x16x32_bf16 v[98:101], v[146:149], v[170:173], v[98:101]
	s_waitcnt lgkmcnt(1)
	v_mfma_f32_16x16x32_bf16 v[84:87], v[138:141], v[178:181], v[84:87]
	v_mfma_f32_16x16x32_bf16 v[80:83], v[146:149], v[178:181], v[80:83]
	v_mfma_f32_16x16x32_bf16 v[126:129], v[142:145], v[158:161], v[126:129]
	v_mfma_f32_16x16x32_bf16 v[122:125], v[150:153], v[158:161], v[122:125]
	v_mfma_f32_16x16x32_bf16 v[118:121], v[142:145], v[166:169], v[118:121]
	v_mfma_f32_16x16x32_bf16 v[114:117], v[150:153], v[166:169], v[114:117]
	v_mfma_f32_16x16x32_bf16 v[102:105], v[142:145], v[174:177], v[102:105]
	v_mfma_f32_16x16x32_bf16 v[98:101], v[150:153], v[174:177], v[98:101]
	s_waitcnt lgkmcnt(0)
	v_mfma_f32_16x16x32_bf16 v[84:87], v[142:145], v[182:185], v[84:87]
	v_mfma_f32_16x16x32_bf16 v[80:83], v[150:153], v[182:185], v[80:83]
	s_setprio 0
	s_barrier
	s_add_i32 s50, s48, 0x80
	s_mov_b32 m0, s30
	ds_read_b128 v[186:189], v135 offset:49152
	ds_read_b128 v[190:193], v135 offset:50176
	ds_read_b128 v[194:197], v135 offset:51200
	ds_read_b128 v[198:201], v135 offset:52224
	buffer_load_dwordx4 v132, s[8:11], s50 offen lds
	s_mov_b32 m0, s31
	s_nop 0
	buffer_load_dwordx4 v134, s[8:11], s50 offen lds
	s_barrier
	s_setprio 1
	s_waitcnt lgkmcnt(3)
	v_mfma_f32_16x16x32_bf16 v[110:113], v[186:189], v[154:157], v[110:113]
	s_waitcnt lgkmcnt(1)
	v_mfma_f32_16x16x32_bf16 v[106:109], v[194:197], v[154:157], v[106:109]
	v_mfma_f32_16x16x32_bf16 v[92:95], v[186:189], v[162:165], v[92:95]
	v_mfma_f32_16x16x32_bf16 v[88:91], v[194:197], v[162:165], v[88:91]
	v_mfma_f32_16x16x32_bf16 v[76:79], v[186:189], v[170:173], v[76:79]
	v_mfma_f32_16x16x32_bf16 v[72:75], v[194:197], v[170:173], v[72:75]
	v_mfma_f32_16x16x32_bf16 v[68:71], v[186:189], v[178:181], v[68:71]
	v_mfma_f32_16x16x32_bf16 v[64:67], v[194:197], v[178:181], v[64:67]
	v_mfma_f32_16x16x32_bf16 v[110:113], v[190:193], v[158:161], v[110:113]
	s_waitcnt lgkmcnt(0)
	v_mfma_f32_16x16x32_bf16 v[106:109], v[198:201], v[158:161], v[106:109]
	v_mfma_f32_16x16x32_bf16 v[92:95], v[190:193], v[166:169], v[92:95]
	v_mfma_f32_16x16x32_bf16 v[88:91], v[198:201], v[166:169], v[88:91]
	v_mfma_f32_16x16x32_bf16 v[76:79], v[190:193], v[174:177], v[76:79]
	v_mfma_f32_16x16x32_bf16 v[72:75], v[198:201], v[174:177], v[72:75]
	v_mfma_f32_16x16x32_bf16 v[68:71], v[190:193], v[182:185], v[68:71]
	v_mfma_f32_16x16x32_bf16 v[64:67], v[198:201], v[182:185], v[64:67]
	s_setprio 0
	s_mov_b32 m0, s34
	s_barrier
	ds_read_b128 v[154:157], v136 offset:49152
	ds_read_b128 v[158:161], v136 offset:50176
	ds_read_b128 v[162:165], v136 offset:51200
	ds_read_b128 v[166:169], v136 offset:52224
	ds_read_b128 v[170:173], v136 offset:53248
	ds_read_b128 v[174:177], v136 offset:54272
	ds_read_b128 v[178:181], v136 offset:55296
	ds_read_b128 v[182:185], v136 offset:56320
	buffer_load_dwordx4 v131, s[72:75], s49 offen lds
	s_mov_b32 m0, s35
	s_nop 0
	buffer_load_dwordx4 v133, s[72:75], s49 offen lds
	s_barrier
	s_setprio 1
	s_waitcnt lgkmcnt(7)
	v_mfma_f32_16x16x32_bf16 v[60:63], v[138:141], v[154:157], v[60:63]
	v_mfma_f32_16x16x32_bf16 v[56:59], v[146:149], v[154:157], v[56:59]
	s_waitcnt lgkmcnt(5)
	v_mfma_f32_16x16x32_bf16 v[52:55], v[138:141], v[162:165], v[52:55]
	v_mfma_f32_16x16x32_bf16 v[48:51], v[146:149], v[162:165], v[48:51]
	s_waitcnt lgkmcnt(3)
	v_mfma_f32_16x16x32_bf16 v[36:39], v[138:141], v[170:173], v[36:39]
	v_mfma_f32_16x16x32_bf16 v[32:35], v[146:149], v[170:173], v[32:35]
	s_waitcnt lgkmcnt(1)
	v_mfma_f32_16x16x32_bf16 v[20:23], v[138:141], v[178:181], v[20:23]
	v_mfma_f32_16x16x32_bf16 v[16:19], v[146:149], v[178:181], v[16:19]
	v_mfma_f32_16x16x32_bf16 v[60:63], v[142:145], v[158:161], v[60:63]
	v_mfma_f32_16x16x32_bf16 v[56:59], v[150:153], v[158:161], v[56:59]
	v_mfma_f32_16x16x32_bf16 v[52:55], v[142:145], v[166:169], v[52:55]
	v_mfma_f32_16x16x32_bf16 v[48:51], v[150:153], v[166:169], v[48:51]
	v_mfma_f32_16x16x32_bf16 v[36:39], v[142:145], v[174:177], v[36:39]
	v_mfma_f32_16x16x32_bf16 v[32:35], v[150:153], v[174:177], v[32:35]
	s_waitcnt lgkmcnt(0)
	v_mfma_f32_16x16x32_bf16 v[20:23], v[142:145], v[182:185], v[20:23]
	v_mfma_f32_16x16x32_bf16 v[16:19], v[150:153], v[182:185], v[16:19]
	s_setprio 0
	s_barrier
	s_add_i32 s48, s48, 0x20080
	s_mov_b32 m0, s36
	s_nop 0
	buffer_load_dwordx4 v132, s[8:11], s48 offen lds
	s_mov_b32 m0, s37
	s_nop 0
	buffer_load_dwordx4 v134, s[8:11], s48 offen lds
	s_waitcnt vmcnt(6)
	s_barrier
	s_setprio 1
	v_mfma_f32_16x16x32_bf16 v[44:47], v[186:189], v[154:157], v[44:47]
	v_mfma_f32_16x16x32_bf16 v[40:43], v[194:197], v[154:157], v[40:43]
	v_mfma_f32_16x16x32_bf16 v[28:31], v[186:189], v[162:165], v[28:31]
	v_mfma_f32_16x16x32_bf16 v[24:27], v[194:197], v[162:165], v[24:27]
	v_mfma_f32_16x16x32_bf16 v[12:15], v[186:189], v[170:173], v[12:15]
	v_mfma_f32_16x16x32_bf16 v[8:11], v[194:197], v[170:173], v[8:11]
	v_mfma_f32_16x16x32_bf16 v[4:7], v[186:189], v[178:181], v[4:7]
	v_mfma_f32_16x16x32_bf16 v[0:3], v[194:197], v[178:181], v[0:3]
	v_mfma_f32_16x16x32_bf16 v[44:47], v[190:193], v[158:161], v[44:47]
	v_mfma_f32_16x16x32_bf16 v[40:43], v[198:201], v[158:161], v[40:43]
	v_mfma_f32_16x16x32_bf16 v[28:31], v[190:193], v[166:169], v[28:31]
	v_mfma_f32_16x16x32_bf16 v[24:27], v[198:201], v[166:169], v[24:27]
	v_mfma_f32_16x16x32_bf16 v[12:15], v[190:193], v[174:177], v[12:15]
	v_mfma_f32_16x16x32_bf16 v[8:11], v[198:201], v[174:177], v[8:11]
	v_mfma_f32_16x16x32_bf16 v[4:7], v[190:193], v[182:185], v[4:7]
	v_mfma_f32_16x16x32_bf16 v[0:3], v[198:201], v[182:185], v[0:3]
	s_setprio 0
	s_add_i32 s47, s47, 2
	s_addk_i32 s45, 0x100
	s_addk_i32 s46, 0x100
	s_cmp_gt_u32 s47, 5
	s_barrier
	s_cbranch_scc0 .LBB0_1358
	s_getreg_b32 s10, hwreg(HW_REG_HW_ID, 0, 6)
	s_and_b32 s10, s10, 63
	s_lshl_b32 s10, s10, 2
	s_add_i32 s10, s10, 0
	s_add_i32 s10, s10, 0x20010
	v_mov_b32_e32 v96, s10
	ds_read_b32 v96, v96
	s_ashr_i32 s15, s14, 31
	s_lshl_b64 s[10:11], s[14:15], 12
	v_mbcnt_lo_u32_b32 v137, -1, 0
	v_mbcnt_hi_u32_b32 v137, -1, v137
	v_cvt_pk_bf16_f32 v126, v126, v127
	s_waitcnt lgkmcnt(0)
	v_readfirstlane_b32 s14, v96
	s_lshl_b32 s14, s14, 6
	s_add_u32 s15, s28, s10
	s_addc_u32 s44, s29, s11
	s_lshl_b32 s10, s42, 8
	s_ashr_i32 s11, s10, 31
	s_lshl_b64 s[10:11], s[10:11], 14
	s_add_u32 s15, s15, s10
	s_addc_u32 s42, s44, s11
	s_lshl_b32 s10, s41, 8
	s_ashr_i32 s11, s10, 31
	v_or_b32_e32 v96, s14, v137
	s_lshl_b64 s[10:11], s[10:11], 1
	v_and_b32_e32 v138, 15, v137
	s_add_u32 s10, s15, s10
	v_lshrrev_b32_e32 v96, 2, v96
	s_mov_b32 s15, 0x3ffc0
	v_and_or_b32 v96, v96, s15, v138
	v_lshlrev_b32_e32 v138, 14, v96
	v_mov_b32_e32 v96, 0xf0
	v_bitop3_b32 v137, s14, v96, v137 bitop3:0xc8
	s_addc_u32 s11, s42, s11
	v_or_b32_e32 v96, v138, v137
	v_cvt_pk_bf16_f32 v127, v128, v129
	v_cvt_pk_bf16_f32 v128, v122, v123
	v_lshl_add_u64 v[122:123], s[10:11], 0, v[96:97]
	s_mov_b32 s14, 0x40000
	v_cvt_pk_bf16_f32 v92, v92, v93
	v_cvt_pk_bf16_f32 v93, v94, v95
	v_cvt_pk_bf16_f32 v94, v88, v89
	v_add_co_u32_e32 v88, vcc, s14, v122
	v_cvt_pk_bf16_f32 v110, v110, v111
	v_cvt_pk_bf16_f32 v111, v112, v113
	v_cvt_pk_bf16_f32 v112, v106, v107
	v_cvt_pk_bf16_f32 v113, v108, v109
	v_addc_co_u32_e32 v89, vcc, 0, v123, vcc
	s_mov_b32 s14, 0x80000
	v_cvt_pk_bf16_f32 v129, v124, v125
	global_store_dwordx4 v96, v[110:113], s[10:11] offset:256
	v_cvt_pk_bf16_f32 v106, v118, v119
	v_cvt_pk_bf16_f32 v107, v120, v121
	v_cvt_pk_bf16_f32 v108, v114, v115
	v_cvt_pk_bf16_f32 v109, v116, v117
	v_or_b32_e32 v110, 0x40000, v96
	v_cvt_pk_bf16_f32 v95, v90, v91
	v_cvt_pk_bf16_f32 v76, v76, v77
	v_cvt_pk_bf16_f32 v77, v78, v79
	v_cvt_pk_bf16_f32 v78, v72, v73
	v_add_co_u32_e32 v72, vcc, s14, v122
	global_store_dwordx4 v96, v[126:129], s[10:11]
	v_or_b32_e32 v124, 0x100, v137
	global_store_dwordx4 v110, v[106:109], s[10:11]
	global_store_dwordx4 v[88:89], v[92:95], off offset:256
	v_cvt_pk_bf16_f32 v88, v102, v103
	v_cvt_pk_bf16_f32 v89, v104, v105
	v_cvt_pk_bf16_f32 v90, v98, v99
	v_cvt_pk_bf16_f32 v91, v100, v101
	v_or_b32_e32 v92, 0x80000, v96
	v_cvt_pk_bf16_f32 v79, v74, v75
	v_addc_co_u32_e32 v73, vcc, 0, v123, vcc
	v_or_b32_e32 v125, v138, v124
	global_store_dwordx4 v92, v[88:91], s[10:11]
	global_store_dwordx4 v[72:73], v[76:79], off offset:256
	v_cvt_pk_bf16_f32 v72, v84, v85
	v_cvt_pk_bf16_f32 v73, v86, v87
	v_or_b32_e32 v76, 0xc0000, v138
	v_cvt_pk_bf16_f32 v74, v80, v81
	v_cvt_pk_bf16_f32 v75, v82, v83
	v_or_b32_e32 v77, v76, v137
	v_cvt_pk_bf16_f32 v68, v68, v69
	v_cvt_pk_bf16_f32 v69, v70, v71
	v_cvt_pk_bf16_f32 v70, v64, v65
	v_cvt_pk_bf16_f32 v71, v66, v67
	v_or_b32_e32 v64, v76, v124
	v_cvt_pk_bf16_f32 v60, v60, v61
	v_cvt_pk_bf16_f32 v61, v62, v63
	v_cvt_pk_bf16_f32 v62, v56, v57
	v_cvt_pk_bf16_f32 v63, v58, v59
	v_add_u32_e32 v56, 0x200000, v96
	v_cvt_pk_bf16_f32 v44, v44, v45
	v_cvt_pk_bf16_f32 v45, v46, v47
	v_cvt_pk_bf16_f32 v46, v40, v41
	v_cvt_pk_bf16_f32 v47, v42, v43
	v_add_u32_e32 v40, 0x200000, v125
	global_store_dwordx4 v77, v[72:75], s[10:11]
	global_store_dwordx4 v64, v[68:71], s[10:11]
	global_store_dwordx4 v56, v[60:63], s[10:11]
	global_store_dwordx4 v40, v[44:47], s[10:11]
	v_cvt_pk_bf16_f32 v28, v28, v29
	v_cvt_pk_bf16_f32 v29, v30, v31
	v_add_u32_e32 v44, 0x240000, v96
	v_cvt_pk_bf16_f32 v30, v24, v25
	v_cvt_pk_bf16_f32 v31, v26, v27
	v_cvt_pk_bf16_f32 v40, v52, v53
	v_cvt_pk_bf16_f32 v41, v54, v55
	v_cvt_pk_bf16_f32 v42, v48, v49
	v_cvt_pk_bf16_f32 v43, v50, v51
	global_store_dwordx4 v44, v[28:31], s[10:11] offset:256
	v_cvt_pk_bf16_f32 v12, v12, v13
	v_cvt_pk_bf16_f32 v13, v14, v15
	v_add_u32_e32 v28, 0x280000, v96
	v_cvt_pk_bf16_f32 v14, v8, v9
	v_cvt_pk_bf16_f32 v15, v10, v11
	global_store_dwordx4 v44, v[40:43], s[10:11]
	v_cvt_pk_bf16_f32 v24, v36, v37
	v_cvt_pk_bf16_f32 v25, v38, v39
	v_cvt_pk_bf16_f32 v26, v32, v33
	v_cvt_pk_bf16_f32 v27, v34, v35
	global_store_dwordx4 v28, v[12:15], s[10:11] offset:256
	v_cvt_pk_bf16_f32 v8, v20, v21
	v_cvt_pk_bf16_f32 v9, v22, v23
	v_cvt_pk_bf16_f32 v10, v16, v17
	v_cvt_pk_bf16_f32 v11, v18, v19
	v_add_u32_e32 v12, 0x2c0000, v96
	v_cvt_pk_bf16_f32 v4, v4, v5
	v_cvt_pk_bf16_f32 v5, v6, v7
	v_cvt_pk_bf16_f32 v6, v0, v1
	v_cvt_pk_bf16_f32 v7, v2, v3
	s_and_b64 vcc, exec, s[4:5]
	s_mov_b32 s14, s16
	s_mov_b32 s41, s17
	s_mov_b32 s42, s18
	s_mov_b32 s46, s43
	s_mov_b32 s45, s19
	global_store_dwordx4 v28, v[24:27], s[10:11]
	global_store_dwordx4 v12, v[8:11], s[10:11]
	global_store_dwordx4 v12, v[4:7], s[10:11] offset:256
	s_cbranch_vccz .LBB0_1352
	s_branch .LBB0_1361

.LBB0_1427:
	s_add_i32 s10, s46, 0xfffc0080
	s_cmp_eq_u32 s48, 12
	s_cselect_b32 s51, s19, s10
	s_cselect_b32 s49, s45, s47
	s_add_i32 s10, 0, 0x10000
	v_add_u32_e32 v213, s10, v228
	v_add_u32_e32 v252, s10, v229
	ds_read_b128 v[72:75], v213
	ds_read_b128 v[84:87], v213 offset:2048
	ds_read_b128 v[76:79], v252
	ds_read_b128 v[88:91], v252 offset:2048
	s_or_b32 s50, s51, 0x80
	s_mov_b32 m0, s42
	ds_read_b128 v[146:149], v230
	ds_read_b128 v[154:157], v230 offset:2048
	ds_read_b128 v[150:153], v231
	ds_read_b128 v[158:161], v231 offset:2048
	ds_read_b128 v[168:171], v230 offset:4096
	ds_read_b128 v[176:179], v230 offset:6144
	ds_read_b128 v[172:175], v231 offset:4096
	ds_read_b128 v[180:183], v231 offset:6144
	buffer_load_dwordx4 v96, s[72:75], s46 offen lds
	s_mov_b32 m0, s43
	s_nop 0
	buffer_load_dwordx4 v218, s[72:75], s46 offen lds
	s_waitcnt lgkmcnt(8)
	s_barrier
	s_setprio 1
	s_waitcnt lgkmcnt(5)
	v_mfma_scale_f32_16x16x128_f8f6f4 v[142:145], v[72:79], v[146:153], v[142:145], v212, v212 op_sel_hi:[0,0,0]
	v_mfma_scale_f32_16x16x128_f8f6f4 v[138:141], v[84:91], v[146:153], v[138:141], v212, v212 op_sel_hi:[0,0,0]
	s_waitcnt lgkmcnt(0)
	v_mfma_scale_f32_16x16x128_f8f6f4 v[92:95], v[72:79], v[176:183], v[92:95], v212, v212 op_sel_hi:[0,0,0]
	v_mfma_scale_f32_16x16x128_f8f6f4 v[80:83], v[84:91], v[176:183], v[80:83], v212, v212 op_sel_hi:[0,0,0]
	v_mfma_scale_f32_16x16x128_f8f6f4 v[162:165], v[72:79], v[154:161], v[126:129], v212, v212 op_sel_hi:[0,0,0]
	v_mfma_scale_f32_16x16x128_f8f6f4 v[184:187], v[84:91], v[154:161], v[122:125], v212, v212 op_sel_hi:[0,0,0]
	v_mfma_scale_f32_16x16x128_f8f6f4 v[188:191], v[72:79], v[168:175], v[110:113], v212, v212 op_sel_hi:[0,0,0]
	v_mfma_scale_f32_16x16x128_f8f6f4 v[192:195], v[84:91], v[168:175], v[106:109], v212, v212 op_sel_hi:[0,0,0]
	s_setprio 0
	s_barrier
	s_mov_b32 s10, s74
	s_mov_b32 s11, s75
	s_mov_b32 m0, s28
	s_nop 1
	ds_read_b128 v[106:109], v213 offset:16384
	ds_read_b128 v[122:125], v213 offset:18432
	ds_read_b128 v[110:113], v252 offset:16384
	ds_read_b128 v[126:129], v252 offset:18432
	buffer_load_dwordx4 v96, s[8:11], s49 offen lds
	s_mov_b32 m0, s29
	s_nop 0
	buffer_load_dwordx4 v218, s[8:11], s49 offen lds
	s_barrier
	s_setprio 1
	s_waitcnt lgkmcnt(1)
	v_mfma_scale_f32_16x16x128_f8f6f4 v[196:199], v[106:113], v[146:153], v[134:137], v212, v212 op_sel_hi:[0,0,0]
	s_waitcnt lgkmcnt(0)
	v_mfma_scale_f32_16x16x128_f8f6f4 v[146:149], v[122:129], v[146:153], v[130:133], v212, v212 op_sel_hi:[0,0,0]
	v_mfma_scale_f32_16x16x128_f8f6f4 v[150:153], v[106:113], v[154:161], v[118:121], v212, v212 op_sel_hi:[0,0,0]
	v_mfma_scale_f32_16x16x128_f8f6f4 v[154:157], v[122:129], v[154:161], v[114:117], v212, v212 op_sel_hi:[0,0,0]
	v_mfma_scale_f32_16x16x128_f8f6f4 v[158:161], v[106:113], v[168:175], v[102:105], v212, v212 op_sel_hi:[0,0,0]
	v_mfma_scale_f32_16x16x128_f8f6f4 v[166:169], v[122:129], v[168:175], v[98:101], v212, v212 op_sel_hi:[0,0,0]
	v_mfma_scale_f32_16x16x128_f8f6f4 v[170:173], v[106:113], v[176:183], v[68:71], v212, v212 op_sel_hi:[0,0,0]
	v_mfma_scale_f32_16x16x128_f8f6f4 v[174:177], v[122:129], v[176:183], v[64:67], v212, v212 op_sel_hi:[0,0,0]
	s_setprio 0
	s_mov_b32 m0, s27
	s_barrier
	s_nop 3
	ds_read_b128 v[64:67], v230 offset:16384
	ds_read_b128 v[98:101], v230 offset:18432
	ds_read_b128 v[68:71], v231 offset:16384
	ds_read_b128 v[102:105], v231 offset:18432
	ds_read_b128 v[114:117], v230 offset:20480
	ds_read_b128 v[130:133], v230 offset:22528
	ds_read_b128 v[118:121], v231 offset:20480
	ds_read_b128 v[134:137], v231 offset:22528
	buffer_load_dwordx4 v96, s[72:75], s51 offen lds
	s_mov_b32 m0, s30
	s_nop 0
	buffer_load_dwordx4 v218, s[72:75], s51 offen lds
	s_barrier
	s_setprio 1
	s_waitcnt lgkmcnt(5)
	v_mfma_scale_f32_16x16x128_f8f6f4 v[60:63], v[72:79], v[64:71], v[60:63], v212, v212 op_sel_hi:[0,0,0]
	v_mfma_scale_f32_16x16x128_f8f6f4 v[56:59], v[84:91], v[64:71], v[56:59], v212, v212 op_sel_hi:[0,0,0]
	s_waitcnt lgkmcnt(4)
	v_mfma_scale_f32_16x16x128_f8f6f4 v[178:181], v[72:79], v[98:105], v[44:47], v212, v212 op_sel_hi:[0,0,0]
	v_mfma_scale_f32_16x16x128_f8f6f4 v[200:203], v[84:91], v[98:105], v[40:43], v212, v212 op_sel_hi:[0,0,0]
	s_waitcnt lgkmcnt(1)
	v_mfma_scale_f32_16x16x128_f8f6f4 v[204:207], v[72:79], v[114:121], v[28:31], v212, v212 op_sel_hi:[0,0,0]
	v_mfma_scale_f32_16x16x128_f8f6f4 v[208:211], v[84:91], v[114:121], v[24:27], v212, v212 op_sel_hi:[0,0,0]
	s_waitcnt lgkmcnt(0)
	v_mfma_scale_f32_16x16x128_f8f6f4 v[214:217], v[72:79], v[130:137], v[12:15], v212, v212 op_sel_hi:[0,0,0]
	v_mfma_scale_f32_16x16x128_f8f6f4 v[220:223], v[84:91], v[130:137], v[8:11], v212, v212 op_sel_hi:[0,0,0]
	s_setprio 0
	s_barrier
	s_add_i32 s52, s49, 0x40000
	s_mov_b32 m0, s31
	s_nop 0
	buffer_load_dwordx4 v96, s[8:11], s52 offen lds
	s_mov_b32 m0, s34
	s_nop 0
	buffer_load_dwordx4 v218, s[8:11], s52 offen lds
	s_waitcnt vmcnt(6)
	s_barrier
	s_setprio 1
	v_mfma_scale_f32_16x16x128_f8f6f4 v[52:55], v[106:113], v[64:71], v[52:55], v212, v212 op_sel_hi:[0,0,0]
	v_mfma_scale_f32_16x16x128_f8f6f4 v[48:51], v[122:129], v[64:71], v[48:51], v212, v212 op_sel_hi:[0,0,0]
	v_mfma_scale_f32_16x16x128_f8f6f4 v[232:235], v[106:113], v[98:105], v[36:39], v212, v212 op_sel_hi:[0,0,0]
	v_mfma_scale_f32_16x16x128_f8f6f4 v[236:239], v[122:129], v[98:105], v[32:35], v212, v212 op_sel_hi:[0,0,0]
	v_mfma_scale_f32_16x16x128_f8f6f4 v[240:243], v[106:113], v[114:121], v[20:23], v212, v212 op_sel_hi:[0,0,0]
	v_mfma_scale_f32_16x16x128_f8f6f4 v[244:247], v[122:129], v[114:121], v[16:19], v212, v212 op_sel_hi:[0,0,0]
	v_mfma_scale_f32_16x16x128_f8f6f4 v[248:251], v[106:113], v[130:137], v[4:7], v212, v212 op_sel_hi:[0,0,0]
	v_mfma_scale_f32_16x16x128_f8f6f4 v[224:227], v[122:129], v[130:137], v[0:3], v212, v212 op_sel_hi:[0,0,0]
	s_setprio 0
	s_barrier
	s_nop 4
	ds_read_b128 v[0:3], v213 offset:32768
	ds_read_b128 v[16:19], v213 offset:34816
	ds_read_b128 v[4:7], v252 offset:32768
	ds_read_b128 v[20:23], v252 offset:34816
	s_add_i32 s51, s51, 0x40000
	s_mov_b32 m0, s35
	ds_read_b128 v[8:11], v230 offset:32768
	ds_read_b128 v[24:27], v230 offset:34816
	ds_read_b128 v[12:15], v231 offset:32768
	ds_read_b128 v[28:31], v231 offset:34816
	ds_read_b128 v[32:35], v230 offset:36864
	ds_read_b128 v[40:43], v230 offset:38912
	ds_read_b128 v[36:39], v231 offset:36864
	ds_read_b128 v[44:47], v231 offset:38912
	buffer_load_dwordx4 v96, s[72:75], s51 offen lds
	s_mov_b32 m0, s36
	s_nop 0
	buffer_load_dwordx4 v218, s[72:75], s51 offen lds
	s_waitcnt lgkmcnt(8)
	s_barrier
	s_setprio 1
	s_waitcnt lgkmcnt(5)
	v_mfma_scale_f32_16x16x128_f8f6f4 v[142:145], v[0:7], v[8:15], v[142:145], v212, v212 op_sel_hi:[0,0,0]
	v_mfma_scale_f32_16x16x128_f8f6f4 v[138:141], v[16:23], v[8:15], v[138:141], v212, v212 op_sel_hi:[0,0,0]
	s_waitcnt lgkmcnt(4)
	v_mfma_scale_f32_16x16x128_f8f6f4 v[126:129], v[0:7], v[24:31], v[162:165], v212, v212 op_sel_hi:[0,0,0]
	v_mfma_scale_f32_16x16x128_f8f6f4 v[122:125], v[16:23], v[24:31], v[184:187], v212, v212 op_sel_hi:[0,0,0]
	s_waitcnt lgkmcnt(1)
	v_mfma_scale_f32_16x16x128_f8f6f4 v[110:113], v[0:7], v[32:39], v[188:191], v212, v212 op_sel_hi:[0,0,0]
	v_mfma_scale_f32_16x16x128_f8f6f4 v[106:109], v[16:23], v[32:39], v[192:195], v212, v212 op_sel_hi:[0,0,0]
	s_waitcnt lgkmcnt(0)
	v_mfma_scale_f32_16x16x128_f8f6f4 v[92:95], v[0:7], v[40:47], v[92:95], v212, v212 op_sel_hi:[0,0,0]
	v_mfma_scale_f32_16x16x128_f8f6f4 v[80:83], v[16:23], v[40:47], v[80:83], v212, v212 op_sel_hi:[0,0,0]
	s_setprio 0
	s_barrier
	s_or_b32 s51, s49, 0x80
	s_mov_b32 m0, s0
	ds_read_b128 v[72:75], v213 offset:49152
	ds_read_b128 v[84:87], v213 offset:51200
	ds_read_b128 v[76:79], v252 offset:49152
	ds_read_b128 v[88:91], v252 offset:51200
	buffer_load_dwordx4 v96, s[8:11], s51 offen lds
	s_mov_b32 m0, s37
	s_nop 0
	buffer_load_dwordx4 v218, s[8:11], s51 offen lds
	s_barrier
	s_setprio 1
	s_waitcnt lgkmcnt(1)
	v_mfma_scale_f32_16x16x128_f8f6f4 v[134:137], v[72:79], v[8:15], v[196:199], v212, v212 op_sel_hi:[0,0,0]
	s_waitcnt lgkmcnt(0)
	v_mfma_scale_f32_16x16x128_f8f6f4 v[130:133], v[84:91], v[8:15], v[146:149], v212, v212 op_sel_hi:[0,0,0]
	v_mfma_scale_f32_16x16x128_f8f6f4 v[118:121], v[72:79], v[24:31], v[150:153], v212, v212 op_sel_hi:[0,0,0]
	v_mfma_scale_f32_16x16x128_f8f6f4 v[114:117], v[84:91], v[24:31], v[154:157], v212, v212 op_sel_hi:[0,0,0]
	v_mfma_scale_f32_16x16x128_f8f6f4 v[102:105], v[72:79], v[32:39], v[158:161], v212, v212 op_sel_hi:[0,0,0]
	v_mfma_scale_f32_16x16x128_f8f6f4 v[98:101], v[84:91], v[32:39], v[166:169], v212, v212 op_sel_hi:[0,0,0]
	v_mfma_scale_f32_16x16x128_f8f6f4 v[68:71], v[72:79], v[40:47], v[170:173], v212, v212 op_sel_hi:[0,0,0]
	v_mfma_scale_f32_16x16x128_f8f6f4 v[64:67], v[84:91], v[40:47], v[174:177], v212, v212 op_sel_hi:[0,0,0]
	s_setprio 0
	s_mov_b32 m0, s38
	s_barrier
	ds_read_b128 v[32:35], v230 offset:49152
	ds_read_b128 v[146:149], v230 offset:51200
	ds_read_b128 v[36:39], v231 offset:49152
	ds_read_b128 v[150:153], v231 offset:51200
	ds_read_b128 v[154:157], v230 offset:53248
	ds_read_b128 v[168:171], v230 offset:55296
	ds_read_b128 v[158:161], v231 offset:53248
	ds_read_b128 v[172:175], v231 offset:55296
	buffer_load_dwordx4 v96, s[72:75], s50 offen lds
	s_mov_b32 m0, s39
	s_nop 0
	buffer_load_dwordx4 v218, s[72:75], s50 offen lds
	s_barrier
	s_setprio 1
	s_waitcnt lgkmcnt(5)
	v_mfma_scale_f32_16x16x128_f8f6f4 v[60:63], v[0:7], v[32:39], v[60:63], v212, v212 op_sel_hi:[0,0,0]
	v_mfma_scale_f32_16x16x128_f8f6f4 v[56:59], v[16:23], v[32:39], v[56:59], v212, v212 op_sel_hi:[0,0,0]
	s_waitcnt lgkmcnt(4)
	v_mfma_scale_f32_16x16x128_f8f6f4 v[44:47], v[0:7], v[146:153], v[178:181], v212, v212 op_sel_hi:[0,0,0]
	v_mfma_scale_f32_16x16x128_f8f6f4 v[40:43], v[16:23], v[146:153], v[200:203], v212, v212 op_sel_hi:[0,0,0]
	s_waitcnt lgkmcnt(1)
	v_mfma_scale_f32_16x16x128_f8f6f4 v[28:31], v[0:7], v[154:161], v[204:207], v212, v212 op_sel_hi:[0,0,0]
	v_mfma_scale_f32_16x16x128_f8f6f4 v[24:27], v[16:23], v[154:161], v[208:211], v212, v212 op_sel_hi:[0,0,0]
	s_waitcnt lgkmcnt(0)
	v_mfma_scale_f32_16x16x128_f8f6f4 v[12:15], v[0:7], v[168:175], v[214:217], v212, v212 op_sel_hi:[0,0,0]
	v_mfma_scale_f32_16x16x128_f8f6f4 v[8:11], v[16:23], v[168:175], v[220:223], v212, v212 op_sel_hi:[0,0,0]
	s_setprio 0
	s_barrier
	s_add_i32 s49, s49, 0x40080
	s_mov_b32 m0, s40
	s_nop 0
	buffer_load_dwordx4 v96, s[8:11], s49 offen lds
	s_mov_b32 m0, s41
	s_nop 0
	buffer_load_dwordx4 v218, s[8:11], s49 offen lds
	s_waitcnt vmcnt(6)
	s_barrier
	s_setprio 1
	v_mfma_scale_f32_16x16x128_f8f6f4 v[52:55], v[72:79], v[32:39], v[52:55], v212, v212 op_sel_hi:[0,0,0]
	v_mfma_scale_f32_16x16x128_f8f6f4 v[48:51], v[84:91], v[32:39], v[48:51], v212, v212 op_sel_hi:[0,0,0]
	v_mfma_scale_f32_16x16x128_f8f6f4 v[36:39], v[72:79], v[146:153], v[232:235], v212, v212 op_sel_hi:[0,0,0]
	v_mfma_scale_f32_16x16x128_f8f6f4 v[32:35], v[84:91], v[146:153], v[236:239], v212, v212 op_sel_hi:[0,0,0]
	v_mfma_scale_f32_16x16x128_f8f6f4 v[20:23], v[72:79], v[154:161], v[240:243], v212, v212 op_sel_hi:[0,0,0]
	v_mfma_scale_f32_16x16x128_f8f6f4 v[16:19], v[84:91], v[154:161], v[244:247], v212, v212 op_sel_hi:[0,0,0]
	v_mfma_scale_f32_16x16x128_f8f6f4 v[4:7], v[72:79], v[168:175], v[248:251], v212, v212 op_sel_hi:[0,0,0]
	v_mfma_scale_f32_16x16x128_f8f6f4 v[0:3], v[84:91], v[168:175], v[224:227], v212, v212 op_sel_hi:[0,0,0]
	s_setprio 0
	s_add_i32 s48, s48, 2
	s_addk_i32 s46, 0x100
	s_addk_i32 s47, 0x100
	s_cmp_gt_u32 s48, 13
	s_barrier
	s_cbranch_scc0 .LBB0_1427
	s_getreg_b32 s10, hwreg(HW_REG_HW_ID, 0, 6)
	s_and_b32 s10, s10, 63
	s_lshl_b32 s10, s10, 2
	s_add_i32 s10, s10, 0
	s_add_i32 s10, s10, 0x20010
	v_mov_b32_e32 v72, s10
	ds_read_b32 v72, v72
	v_mbcnt_lo_u32_b32 v150, -1, 0
	v_mbcnt_hi_u32_b32 v150, -1, v150
	s_lshl_b32 s2, s2, 6
	v_lshrrev_b32_e32 v73, 2, v150
	v_and_b32_e32 v73, 12, v73
	s_waitcnt lgkmcnt(0)
	v_readfirstlane_b32 s10, v72
	s_movk_i32 s45, 0x2000
	s_ashr_i32 s19, s18, 31
	v_lshl_or_b32 v148, s10, 6, v150
	v_lshrrev_b32_e32 v72, 2, v148
	v_and_b32_e32 v72, 48, v72
	v_or3_b32 v146, v72, s2, v73
	v_ashrrev_i32_e32 v147, 31, v146
	v_lshl_add_u64 v[72:73], v[146:147], 2, s[16:17]
	v_add_co_u32_e32 v74, vcc, s45, v72
	v_ashrrev_i32_e32 v148, 2, v148
	s_nop 0
	v_addc_co_u32_e32 v75, vcc, 0, v73, vcc
	global_load_dwordx4 v[88:91], v[72:73], off
	global_load_dwordx4 v[84:87], v[74:75], off
	v_and_b32_e32 v148, 0xffffffc0, v148
	s_lshl_b64 s[10:11], s[18:19], 8
	v_ashrrev_i32_e32 v149, 31, v148
	s_movk_i32 s2, 0x4000
	v_lshl_add_u64 v[148:149], s[10:11], 0, v[148:149]
	v_add_co_u32_e32 v74, vcc, s2, v72
	v_and_or_b32 v148, v150, 15, v148
	s_nop 0
	v_addc_co_u32_e32 v75, vcc, 0, v73, vcc
	s_movk_i32 s2, 0x6000
	v_lshlrev_b64 v[150:151], 14, v[148:149]
	v_add_co_u32_e32 v72, vcc, s2, v72
	v_lshl_add_u64 v[150:151], s[14:15], 0, v[150:151]
	v_lshlrev_b64 v[146:147], 1, v[146:147]
	v_addc_co_u32_e32 v73, vcc, 0, v73, vcc
	v_lshl_add_u64 v[150:151], v[150:151], 0, v[146:147]
	v_add_co_u32_e32 v152, vcc, s45, v150
	global_load_dwordx4 v[76:79], v[74:75], off
	s_nop 0
	global_load_dwordx4 v[72:75], v[72:73], off
	v_addc_co_u32_e32 v153, vcc, 0, v151, vcc
	v_add_co_u32_e32 v154, vcc, s95, v150
	s_mov_b32 s2, 0x41000
	s_nop 0
	v_addc_co_u32_e32 v155, vcc, 0, v151, vcc
	global_load_dwordx2 v[166:167], v[150:151], off
	global_load_dwordx2 v[208:209], v[152:153], off offset:-4096
	global_load_dwordx2 v[204:205], v[152:153], off
	global_load_dwordx2 v[206:207], v[154:155], off
	v_add_co_u32_e32 v152, vcc, s2, v150
	s_mov_b32 s2, 0x43000
	s_nop 0
	v_addc_co_u32_e32 v153, vcc, 0, v151, vcc
	v_add_co_u32_e32 v154, vcc, s2, v150
	s_mov_b32 s2, 0x81000
	s_nop 0
	v_addc_co_u32_e32 v155, vcc, 0, v151, vcc
	global_load_dwordx2 v[200:201], v[152:153], off offset:-4096
	global_load_dwordx2 v[202:203], v[152:153], off
	global_load_dwordx2 v[196:197], v[154:155], off offset:-4096
	global_load_dwordx2 v[198:199], v[154:155], off
	v_add_co_u32_e32 v152, vcc, s2, v150
	s_mov_b32 s2, 0x83000
	s_nop 0
	v_addc_co_u32_e32 v153, vcc, 0, v151, vcc
	v_add_co_u32_e32 v154, vcc, s2, v150
	s_mov_b32 s2, 0xc1000
	s_nop 0
	v_addc_co_u32_e32 v155, vcc, 0, v151, vcc
	global_load_dwordx2 v[192:193], v[152:153], off offset:-4096
	global_load_dwordx2 v[194:195], v[152:153], off
	global_load_dwordx2 v[188:189], v[154:155], off offset:-4096
	global_load_dwordx2 v[190:191], v[154:155], off
	v_add_co_u32_e32 v152, vcc, s2, v150
	s_mov_b32 s2, 0xc3000
	s_nop 0
	v_addc_co_u32_e32 v153, vcc, 0, v151, vcc
	v_lshlrev_b64 v[148:149], 12, v[148:149]
	v_add_co_u32_e32 v154, vcc, s2, v150
	v_lshl_add_u64 v[148:149], s[12:13], 0, v[148:149]
	s_nop 0
	v_addc_co_u32_e32 v155, vcc, 0, v151, vcc
	s_mov_b32 s2, 0x201000
	v_lshl_add_u64 v[146:147], v[148:149], 0, v[146:147]
	v_add_co_u32_e32 v148, vcc, s2, v150
	s_mov_b32 s2, 0x203000
	s_nop 0
	v_addc_co_u32_e32 v149, vcc, 0, v151, vcc
	global_load_dwordx2 v[184:185], v[152:153], off offset:-4096
	global_load_dwordx2 v[186:187], v[152:153], off
	global_load_dwordx2 v[180:181], v[154:155], off offset:-4096
	global_load_dwordx2 v[182:183], v[154:155], off
	v_add_co_u32_e32 v152, vcc, s2, v150
	s_mov_b32 s2, 0x241000
	s_nop 0
	v_addc_co_u32_e32 v153, vcc, 0, v151, vcc
	global_load_dwordx2 v[176:177], v[148:149], off offset:-4096
	global_load_dwordx2 v[178:179], v[148:149], off
	global_load_dwordx2 v[172:173], v[152:153], off offset:-4096
	global_load_dwordx2 v[174:175], v[152:153], off
	v_add_co_u32_e32 v148, vcc, s2, v150
	s_mov_b32 s2, 0x243000
	s_nop 0
	v_addc_co_u32_e32 v149, vcc, 0, v151, vcc
	v_add_co_u32_e32 v152, vcc, s2, v150
	s_mov_b32 s2, 0x281000
	s_nop 0
	v_addc_co_u32_e32 v153, vcc, 0, v151, vcc
	global_load_dwordx2 v[168:169], v[148:149], off offset:-4096
	global_load_dwordx2 v[170:171], v[148:149], off
	global_load_dwordx2 v[162:163], v[152:153], off offset:-4096
	global_load_dwordx2 v[164:165], v[152:153], off
	v_add_co_u32_e32 v148, vcc, s2, v150
	s_mov_b32 s2, 0x283000
	s_nop 0
	v_addc_co_u32_e32 v149, vcc, 0, v151, vcc
	v_add_co_u32_e32 v152, vcc, s2, v150
	s_mov_b32 s2, 0x2c1000
	s_nop 0
	v_addc_co_u32_e32 v153, vcc, 0, v151, vcc
	s_waitcnt vmcnt(27)
	v_pk_fma_f32 v[214:215], v[142:143], s[78:79], v[88:89] op_sel_hi:[1,0,1]
	global_load_dwordx2 v[158:159], v[148:149], off offset:-4096
	global_load_dwordx2 v[160:161], v[148:149], off
	global_load_dwordx2 v[154:155], v[152:153], off offset:-4096
	global_load_dwordx2 v[156:157], v[152:153], off
	v_add_co_u32_e32 v148, vcc, s2, v150
	v_mul_f32_e32 v142, 0xbfb8aa3b, v214
	s_nop 0
	v_addc_co_u32_e32 v149, vcc, 0, v151, vcc
	s_mov_b32 s2, 0x2c3000
	v_exp_f32_e32 v214, v142
	v_add_co_u32_e32 v210, vcc, s2, v150
	v_pk_fma_f32 v[144:145], v[144:145], s[78:79], v[90:91] op_sel_hi:[1,0,1]
	s_nop 0
	v_addc_co_u32_e32 v211, vcc, 0, v151, vcc
	global_load_dwordx2 v[150:151], v[148:149], off offset:-4096
	global_load_dwordx2 v[152:153], v[148:149], off
	global_load_dwordx2 v[142:143], v[210:211], off offset:-4096
	s_nop 0
	global_load_dwordx2 v[148:149], v[210:211], off
	v_mul_f32_e32 v211, 0xbfb8aa3b, v215
	v_mul_f32_e32 v144, 0xbfb8aa3b, v144
	v_add_f32_e32 v210, 1.0, v214
	v_exp_f32_e32 v211, v211
	v_exp_f32_e32 v214, v144
	s_waitcnt vmcnt(34)
	v_pk_fma_f32 v[138:139], v[138:139], s[78:79], v[84:85] op_sel_hi:[1,0,1]
	v_rcp_f32_e32 v144, v210
	v_mul_f32_e32 v139, 0xbfb8aa3b, v139
	v_add_f32_e32 v210, 1.0, v211
	v_add_f32_e32 v211, 1.0, v214
	v_mul_f32_e32 v145, 0xbfb8aa3b, v145
	v_mul_f32_e32 v138, 0xbfb8aa3b, v138
	v_exp_f32_e32 v139, v139
	v_rcp_f32_e32 v214, v211
	v_exp_f32_e32 v145, v145
	v_exp_f32_e32 v211, v138
	v_pk_fma_f32 v[140:141], v[140:141], s[78:79], v[86:87] op_sel_hi:[1,0,1]
	v_add_f32_e32 v139, 1.0, v139
	v_add_f32_e32 v138, 1.0, v145
	v_add_f32_e32 v145, 1.0, v211
	v_rcp_f32_e32 v211, v139
	v_mul_f32_e32 v139, 0xbfb8aa3b, v140
	v_exp_f32_e32 v139, v139
	v_rcp_f32_e32 v145, v145
	v_rcp_f32_e32 v210, v210
	s_waitcnt vmcnt(30)
	v_lshlrev_b32_e32 v217, 16, v208
	v_add_f32_e32 v139, 1.0, v139
	v_lshlrev_b32_e32 v216, 16, v166
	v_rcp_f32_e32 v215, v139
	v_mul_f32_e32 v139, 0xbfb8aa3b, v141
	v_pk_mul_f32 v[144:145], v[144:145], v[216:217]
	v_exp_f32_e32 v139, v139
	v_add_f32_e32 v144, 0, v144
	v_add_f32_e32 v216, v144, v145
	v_and_b32_e32 v145, 0xffff0000, v208
	v_and_b32_e32 v144, 0xffff0000, v166
	v_pk_mul_f32 v[144:145], v[210:211], v[144:145]
	v_add_f32_e32 v139, 1.0, v139
	v_add_f32_e32 v140, 0, v144
	v_rcp_f32_e32 v138, v138
	v_add_f32_e32 v166, v140, v145
	v_lshlrev_b32_e32 v145, 16, v209
	v_lshlrev_b32_e32 v144, 16, v167
	v_rcp_f32_e32 v139, v139
	v_pk_mul_f32 v[140:141], v[214:215], v[144:145]
	v_pk_fma_f32 v[134:135], v[134:135], s[78:79], v[76:77] op_sel_hi:[1,0,1]
	v_add_f32_e32 v140, 0, v140
	v_add_f32_e32 v144, v140, v141
	v_and_b32_e32 v141, 0xffff0000, v209
	v_and_b32_e32 v140, 0xffff0000, v167
	v_pk_mul_f32 v[138:139], v[138:139], v[140:141]
	v_pk_fma_f32 v[136:137], v[136:137], s[78:79], v[78:79] op_sel_hi:[1,0,1]
	v_mul_f32_e32 v135, 0xbfb8aa3b, v135
	v_add_f32_e32 v138, 0, v138
	v_exp_f32_e32 v135, v135
	v_mul_f32_e32 v136, 0xbfb8aa3b, v136
	v_add_f32_e32 v145, v138, v139
	v_exp_f32_e32 v138, v136
	v_add_f32_e32 v135, 1.0, v135
	v_pk_fma_f32 v[130:131], v[130:131], s[78:79], v[72:73] op_sel_hi:[1,0,1]
	v_rcp_f32_e32 v136, v135
	v_add_f32_e32 v135, 1.0, v138
	v_mul_f32_e32 v131, 0xbfb8aa3b, v131
	v_rcp_f32_e32 v138, v135
	v_mul_f32_e32 v135, 0xbfb8aa3b, v137
	v_mul_f32_e32 v130, 0xbfb8aa3b, v130
	v_exp_f32_e32 v131, v131
	v_exp_f32_e32 v135, v135
	v_exp_f32_e32 v137, v130
	v_mul_f32_e32 v134, 0xbfb8aa3b, v134
	v_exp_f32_e32 v134, v134
	v_pk_fma_f32 v[132:133], v[132:133], s[78:79], v[74:75] op_sel_hi:[1,0,1]
	v_add_f32_e32 v131, 1.0, v131
	v_add_f32_e32 v130, 1.0, v135
	v_add_f32_e32 v135, 1.0, v137
	v_rcp_f32_e32 v137, v131
	v_mul_f32_e32 v131, 0xbfb8aa3b, v132
	v_exp_f32_e32 v131, v131
	v_add_f32_e32 v134, 1.0, v134
	v_rcp_f32_e32 v134, v134
	v_rcp_f32_e32 v135, v135
	v_add_f32_e32 v131, 1.0, v131
	s_waitcnt vmcnt(28)
	v_lshlrev_b32_e32 v141, 16, v206
	v_lshlrev_b32_e32 v140, 16, v204
	v_rcp_f32_e32 v139, v131
	v_mul_f32_e32 v131, 0xbfb8aa3b, v133
	v_pk_mul_f32 v[134:135], v[134:135], v[140:141]
	v_exp_f32_e32 v131, v131
	v_add_f32_e32 v134, v216, v134
	v_add_f32_e32 v140, v134, v135
	v_and_b32_e32 v135, 0xffff0000, v206
	v_and_b32_e32 v134, 0xffff0000, v204
	v_pk_mul_f32 v[134:135], v[136:137], v[134:135]
	v_add_f32_e32 v131, 1.0, v131
	v_add_f32_e32 v132, v166, v134
	v_rcp_f32_e32 v130, v130
	v_add_f32_e32 v136, v132, v135
	v_lshlrev_b32_e32 v135, 16, v207
	v_lshlrev_b32_e32 v134, 16, v205
	v_rcp_f32_e32 v131, v131
	v_pk_mul_f32 v[132:133], v[138:139], v[134:135]
	v_pk_fma_f32 v[126:127], v[126:127], s[78:79], v[88:89] op_sel_hi:[1,0,1]
	v_add_f32_e32 v132, v144, v132
	v_add_f32_e32 v134, v132, v133
	v_and_b32_e32 v133, 0xffff0000, v207
	v_and_b32_e32 v132, 0xffff0000, v205
	v_pk_mul_f32 v[130:131], v[130:131], v[132:133]
	v_pk_fma_f32 v[128:129], v[128:129], s[78:79], v[90:91] op_sel_hi:[1,0,1]
	v_add_f32_e32 v130, v145, v130
	v_mul_f32_e32 v127, 0xbfb8aa3b, v127
	v_add_f32_e32 v131, v130, v131
	v_cvt_pk_bf16_f32 v130, v140, v136
	v_exp_f32_e32 v127, v127
	v_mul_f32_e32 v128, 0xbfb8aa3b, v128
	v_cvt_pk_bf16_f32 v131, v134, v131
	global_store_dwordx2 v[146:147], v[130:131], off
	v_exp_f32_e32 v130, v128
	v_add_f32_e32 v127, 1.0, v127
	v_pk_fma_f32 v[122:123], v[122:123], s[78:79], v[84:85] op_sel_hi:[1,0,1]
	v_rcp_f32_e32 v128, v127
	v_add_f32_e32 v127, 1.0, v130
	v_mul_f32_e32 v123, 0xbfb8aa3b, v123
	v_rcp_f32_e32 v130, v127
	v_mul_f32_e32 v127, 0xbfb8aa3b, v129
	v_mul_f32_e32 v122, 0xbfb8aa3b, v122
	v_exp_f32_e32 v123, v123
	v_exp_f32_e32 v127, v127
	v_exp_f32_e32 v129, v122
	v_mul_f32_e32 v126, 0xbfb8aa3b, v126
	v_exp_f32_e32 v126, v126
	v_pk_fma_f32 v[124:125], v[124:125], s[78:79], v[86:87] op_sel_hi:[1,0,1]
	v_add_f32_e32 v123, 1.0, v123
	v_add_f32_e32 v122, 1.0, v127
	v_add_f32_e32 v127, 1.0, v129
	v_rcp_f32_e32 v129, v123
	v_mul_f32_e32 v123, 0xbfb8aa3b, v124
	v_exp_f32_e32 v123, v123
	v_add_f32_e32 v126, 1.0, v126
	v_rcp_f32_e32 v126, v126
	v_rcp_f32_e32 v127, v127
	v_add_f32_e32 v123, 1.0, v123
	s_waitcnt vmcnt(27)
	v_lshlrev_b32_e32 v133, 16, v202
	v_lshlrev_b32_e32 v132, 16, v200
	v_rcp_f32_e32 v131, v123
	v_mul_f32_e32 v123, 0xbfb8aa3b, v125
	v_pk_mul_f32 v[126:127], v[126:127], v[132:133]
	v_exp_f32_e32 v123, v123
	v_add_f32_e32 v126, 0, v126
	v_add_f32_e32 v132, v126, v127
	v_and_b32_e32 v127, 0xffff0000, v202
	v_and_b32_e32 v126, 0xffff0000, v200
	v_pk_mul_f32 v[126:127], v[128:129], v[126:127]
	v_add_f32_e32 v123, 1.0, v123
	v_add_f32_e32 v124, 0, v126
	v_rcp_f32_e32 v122, v122
	v_add_f32_e32 v128, v124, v127
	v_lshlrev_b32_e32 v127, 16, v203
	v_lshlrev_b32_e32 v126, 16, v201
	v_rcp_f32_e32 v123, v123
	v_pk_mul_f32 v[124:125], v[130:131], v[126:127]
	v_pk_fma_f32 v[118:119], v[118:119], s[78:79], v[76:77] op_sel_hi:[1,0,1]
	v_add_f32_e32 v124, 0, v124
	v_add_f32_e32 v126, v124, v125
	v_and_b32_e32 v125, 0xffff0000, v203
	v_and_b32_e32 v124, 0xffff0000, v201
	v_pk_mul_f32 v[122:123], v[122:123], v[124:125]
	v_pk_fma_f32 v[120:121], v[120:121], s[78:79], v[78:79] op_sel_hi:[1,0,1]
	v_mul_f32_e32 v119, 0xbfb8aa3b, v119
	v_add_f32_e32 v122, 0, v122
	v_exp_f32_e32 v119, v119
	v_mul_f32_e32 v120, 0xbfb8aa3b, v120
	v_add_f32_e32 v127, v122, v123
	v_exp_f32_e32 v122, v120
	v_add_f32_e32 v119, 1.0, v119
	v_pk_fma_f32 v[114:115], v[114:115], s[78:79], v[72:73] op_sel_hi:[1,0,1]
	v_rcp_f32_e32 v120, v119
	v_add_f32_e32 v119, 1.0, v122
	v_mul_f32_e32 v115, 0xbfb8aa3b, v115
	v_rcp_f32_e32 v122, v119
	v_mul_f32_e32 v119, 0xbfb8aa3b, v121
	v_mul_f32_e32 v114, 0xbfb8aa3b, v114
	v_exp_f32_e32 v115, v115
	v_exp_f32_e32 v119, v119
	v_exp_f32_e32 v121, v114
	v_mul_f32_e32 v118, 0xbfb8aa3b, v118
	v_exp_f32_e32 v118, v118
	v_pk_fma_f32 v[116:117], v[116:117], s[78:79], v[74:75] op_sel_hi:[1,0,1]
	v_add_f32_e32 v115, 1.0, v115
	v_add_f32_e32 v114, 1.0, v119
	v_add_f32_e32 v119, 1.0, v121
	v_rcp_f32_e32 v121, v115
	v_mul_f32_e32 v115, 0xbfb8aa3b, v116
	v_exp_f32_e32 v115, v115
	v_add_f32_e32 v118, 1.0, v118
	v_rcp_f32_e32 v118, v118
	v_rcp_f32_e32 v119, v119
	v_add_f32_e32 v115, 1.0, v115
	s_waitcnt vmcnt(25)
	v_lshlrev_b32_e32 v125, 16, v198
	v_lshlrev_b32_e32 v124, 16, v196
	v_rcp_f32_e32 v123, v115
	v_mul_f32_e32 v115, 0xbfb8aa3b, v117
	v_pk_mul_f32 v[118:119], v[118:119], v[124:125]
	v_exp_f32_e32 v115, v115
	v_add_f32_e32 v118, v132, v118
	v_add_f32_e32 v124, v118, v119
	v_and_b32_e32 v119, 0xffff0000, v198
	v_and_b32_e32 v118, 0xffff0000, v196
	v_pk_mul_f32 v[118:119], v[120:121], v[118:119]
	v_add_f32_e32 v115, 1.0, v115
	v_add_f32_e32 v116, v128, v118
	v_rcp_f32_e32 v114, v114
	v_add_f32_e32 v120, v116, v119
	v_lshlrev_b32_e32 v119, 16, v199
	v_lshlrev_b32_e32 v118, 16, v197
	v_rcp_f32_e32 v115, v115
	v_pk_mul_f32 v[116:117], v[122:123], v[118:119]
	v_pk_fma_f32 v[110:111], v[110:111], s[78:79], v[88:89] op_sel_hi:[1,0,1]
	v_add_f32_e32 v116, v126, v116
	v_add_f32_e32 v118, v116, v117
	v_and_b32_e32 v117, 0xffff0000, v199
	v_and_b32_e32 v116, 0xffff0000, v197
	v_pk_mul_f32 v[114:115], v[114:115], v[116:117]
	s_mov_b32 s2, 0x10000
	v_add_f32_e32 v114, v127, v114
	v_add_co_u32_e32 v116, vcc, s2, v146
	v_pk_fma_f32 v[112:113], v[112:113], s[78:79], v[90:91] op_sel_hi:[1,0,1]
	v_mul_f32_e32 v111, 0xbfb8aa3b, v111
	v_add_f32_e32 v115, v114, v115
	v_cvt_pk_bf16_f32 v114, v124, v120
	v_addc_co_u32_e32 v117, vcc, 0, v147, vcc
	v_exp_f32_e32 v111, v111
	v_mul_f32_e32 v112, 0xbfb8aa3b, v112
	v_cvt_pk_bf16_f32 v115, v118, v115
	global_store_dwordx2 v[116:117], v[114:115], off
	v_exp_f32_e32 v114, v112
	v_add_f32_e32 v111, 1.0, v111
	v_pk_fma_f32 v[106:107], v[106:107], s[78:79], v[84:85] op_sel_hi:[1,0,1]
	v_rcp_f32_e32 v112, v111
	v_add_f32_e32 v111, 1.0, v114
	v_mul_f32_e32 v107, 0xbfb8aa3b, v107
	v_rcp_f32_e32 v114, v111
	v_mul_f32_e32 v111, 0xbfb8aa3b, v113
	v_mul_f32_e32 v106, 0xbfb8aa3b, v106
	v_exp_f32_e32 v107, v107
	v_exp_f32_e32 v111, v111
	v_exp_f32_e32 v113, v106
	v_mul_f32_e32 v110, 0xbfb8aa3b, v110
	v_exp_f32_e32 v110, v110
	v_pk_fma_f32 v[108:109], v[108:109], s[78:79], v[86:87] op_sel_hi:[1,0,1]
	v_add_f32_e32 v107, 1.0, v107
	v_add_f32_e32 v106, 1.0, v111
	v_add_f32_e32 v111, 1.0, v113
	v_rcp_f32_e32 v113, v107
	v_mul_f32_e32 v107, 0xbfb8aa3b, v108
	v_exp_f32_e32 v107, v107
	v_add_f32_e32 v110, 1.0, v110
	v_rcp_f32_e32 v110, v110
	v_rcp_f32_e32 v111, v111
	v_add_f32_e32 v107, 1.0, v107
	s_waitcnt vmcnt(24)
	v_lshlrev_b32_e32 v117, 16, v194
	v_lshlrev_b32_e32 v116, 16, v192
	v_rcp_f32_e32 v115, v107
	v_mul_f32_e32 v107, 0xbfb8aa3b, v109
	v_pk_mul_f32 v[110:111], v[110:111], v[116:117]
	v_exp_f32_e32 v107, v107
	v_add_f32_e32 v110, 0, v110
	v_add_f32_e32 v116, v110, v111
	v_and_b32_e32 v111, 0xffff0000, v194
	v_and_b32_e32 v110, 0xffff0000, v192
	v_pk_mul_f32 v[110:111], v[112:113], v[110:111]
	v_add_f32_e32 v107, 1.0, v107
	v_add_f32_e32 v108, 0, v110
	v_rcp_f32_e32 v106, v106
	v_add_f32_e32 v112, v108, v111
	v_lshlrev_b32_e32 v111, 16, v195
	v_lshlrev_b32_e32 v110, 16, v193
	v_rcp_f32_e32 v107, v107
	v_pk_mul_f32 v[108:109], v[114:115], v[110:111]
	v_pk_fma_f32 v[102:103], v[102:103], s[78:79], v[76:77] op_sel_hi:[1,0,1]
	v_add_f32_e32 v108, 0, v108
	v_add_f32_e32 v110, v108, v109
	v_and_b32_e32 v109, 0xffff0000, v195
	v_and_b32_e32 v108, 0xffff0000, v193
	v_pk_mul_f32 v[106:107], v[106:107], v[108:109]
	v_pk_fma_f32 v[104:105], v[104:105], s[78:79], v[78:79] op_sel_hi:[1,0,1]
	v_mul_f32_e32 v103, 0xbfb8aa3b, v103
	v_add_f32_e32 v106, 0, v106
	v_exp_f32_e32 v103, v103
	v_mul_f32_e32 v104, 0xbfb8aa3b, v104
	v_add_f32_e32 v111, v106, v107
	v_exp_f32_e32 v106, v104
	v_add_f32_e32 v103, 1.0, v103
	v_pk_fma_f32 v[98:99], v[98:99], s[78:79], v[72:73] op_sel_hi:[1,0,1]
	v_rcp_f32_e32 v104, v103
	v_add_f32_e32 v103, 1.0, v106
	v_mul_f32_e32 v99, 0xbfb8aa3b, v99
	v_rcp_f32_e32 v106, v103
	v_mul_f32_e32 v103, 0xbfb8aa3b, v105
	v_mul_f32_e32 v98, 0xbfb8aa3b, v98
	v_exp_f32_e32 v99, v99
	v_exp_f32_e32 v103, v103
	v_exp_f32_e32 v105, v98
	v_mul_f32_e32 v102, 0xbfb8aa3b, v102
	v_exp_f32_e32 v102, v102
	v_pk_fma_f32 v[100:101], v[100:101], s[78:79], v[74:75] op_sel_hi:[1,0,1]
	v_add_f32_e32 v99, 1.0, v99
	v_add_f32_e32 v98, 1.0, v103
	v_add_f32_e32 v103, 1.0, v105
	v_rcp_f32_e32 v105, v99
	v_mul_f32_e32 v99, 0xbfb8aa3b, v100
	v_exp_f32_e32 v99, v99
	v_add_f32_e32 v102, 1.0, v102
	v_rcp_f32_e32 v102, v102
	v_rcp_f32_e32 v103, v103
	v_add_f32_e32 v99, 1.0, v99
	s_waitcnt vmcnt(22)
	v_lshlrev_b32_e32 v109, 16, v190
	v_lshlrev_b32_e32 v108, 16, v188
	v_rcp_f32_e32 v107, v99
	v_mul_f32_e32 v99, 0xbfb8aa3b, v101
	v_pk_mul_f32 v[102:103], v[102:103], v[108:109]
	v_exp_f32_e32 v99, v99
	v_add_f32_e32 v102, v116, v102
	v_add_f32_e32 v108, v102, v103
	v_and_b32_e32 v103, 0xffff0000, v190
	v_and_b32_e32 v102, 0xffff0000, v188
	v_pk_mul_f32 v[102:103], v[104:105], v[102:103]
	v_add_f32_e32 v99, 1.0, v99
	v_add_f32_e32 v100, v112, v102
	v_rcp_f32_e32 v98, v98
	v_add_f32_e32 v104, v100, v103
	v_lshlrev_b32_e32 v103, 16, v191
	v_lshlrev_b32_e32 v102, 16, v189
	v_rcp_f32_e32 v99, v99
	v_pk_mul_f32 v[100:101], v[106:107], v[102:103]
	v_pk_fma_f32 v[92:93], v[92:93], s[78:79], v[88:89] op_sel_hi:[1,0,1]
	v_add_f32_e32 v100, v110, v100
	v_add_f32_e32 v102, v100, v101
	v_and_b32_e32 v101, 0xffff0000, v191
	v_and_b32_e32 v100, 0xffff0000, v189
	v_pk_mul_f32 v[98:99], v[98:99], v[100:101]
	v_add_co_u32_e32 v100, vcc, s75, v146
	v_add_f32_e32 v98, v111, v98
	v_pk_fma_f32 v[94:95], v[94:95], s[78:79], v[90:91] op_sel_hi:[1,0,1]
	v_mul_f32_e32 v93, 0xbfb8aa3b, v93
	v_add_f32_e32 v99, v98, v99
	v_cvt_pk_bf16_f32 v98, v108, v104
	v_addc_co_u32_e32 v101, vcc, 0, v147, vcc
	v_exp_f32_e32 v93, v93
	v_mul_f32_e32 v94, 0xbfb8aa3b, v94
	v_cvt_pk_bf16_f32 v99, v102, v99
	global_store_dwordx2 v[100:101], v[98:99], off
	v_exp_f32_e32 v98, v94
	v_add_f32_e32 v93, 1.0, v93
	v_pk_fma_f32 v[80:81], v[80:81], s[78:79], v[84:85] op_sel_hi:[1,0,1]
	v_rcp_f32_e32 v94, v93
	v_add_f32_e32 v93, 1.0, v98
	v_mul_f32_e32 v81, 0xbfb8aa3b, v81
	v_rcp_f32_e32 v98, v93
	v_mul_f32_e32 v93, 0xbfb8aa3b, v95
	v_mul_f32_e32 v80, 0xbfb8aa3b, v80
	v_exp_f32_e32 v81, v81
	v_exp_f32_e32 v93, v93
	v_exp_f32_e32 v95, v80
	v_mul_f32_e32 v92, 0xbfb8aa3b, v92
	v_exp_f32_e32 v92, v92
	v_pk_fma_f32 v[82:83], v[82:83], s[78:79], v[86:87] op_sel_hi:[1,0,1]
	v_add_f32_e32 v81, 1.0, v81
	v_add_f32_e32 v80, 1.0, v93
	v_add_f32_e32 v93, 1.0, v95
	v_rcp_f32_e32 v95, v81
	v_mul_f32_e32 v81, 0xbfb8aa3b, v82
	v_exp_f32_e32 v81, v81
	v_add_f32_e32 v92, 1.0, v92
	v_rcp_f32_e32 v92, v92
	v_rcp_f32_e32 v93, v93
	v_add_f32_e32 v81, 1.0, v81
	s_waitcnt vmcnt(21)
	v_lshlrev_b32_e32 v101, 16, v186
	v_lshlrev_b32_e32 v100, 16, v184
	v_rcp_f32_e32 v99, v81
	v_mul_f32_e32 v81, 0xbfb8aa3b, v83
	v_pk_mul_f32 v[92:93], v[92:93], v[100:101]
	v_exp_f32_e32 v81, v81
	v_add_f32_e32 v92, 0, v92
	v_add_f32_e32 v100, v92, v93
	v_and_b32_e32 v93, 0xffff0000, v186
	v_and_b32_e32 v92, 0xffff0000, v184
	v_pk_mul_f32 v[92:93], v[94:95], v[92:93]
	v_add_f32_e32 v81, 1.0, v81
	v_add_f32_e32 v82, 0, v92
	v_rcp_f32_e32 v80, v80
	v_add_f32_e32 v94, v82, v93
	v_lshlrev_b32_e32 v93, 16, v187
	v_lshlrev_b32_e32 v92, 16, v185
	v_rcp_f32_e32 v81, v81
	v_pk_mul_f32 v[82:83], v[98:99], v[92:93]
	v_pk_fma_f32 v[68:69], v[68:69], s[78:79], v[76:77] op_sel_hi:[1,0,1]
	v_add_f32_e32 v82, 0, v82
	v_add_f32_e32 v92, v82, v83
	v_and_b32_e32 v83, 0xffff0000, v187
	v_and_b32_e32 v82, 0xffff0000, v185
	v_pk_mul_f32 v[80:81], v[80:81], v[82:83]
	v_pk_fma_f32 v[70:71], v[70:71], s[78:79], v[78:79] op_sel_hi:[1,0,1]
	v_mul_f32_e32 v69, 0xbfb8aa3b, v69
	v_add_f32_e32 v80, 0, v80
	v_exp_f32_e32 v69, v69
	v_mul_f32_e32 v70, 0xbfb8aa3b, v70
	v_add_f32_e32 v93, v80, v81
	v_exp_f32_e32 v80, v70
	v_add_f32_e32 v69, 1.0, v69
	v_pk_fma_f32 v[64:65], v[64:65], s[78:79], v[72:73] op_sel_hi:[1,0,1]
	v_rcp_f32_e32 v70, v69
	v_add_f32_e32 v69, 1.0, v80
	v_mul_f32_e32 v65, 0xbfb8aa3b, v65
	v_rcp_f32_e32 v80, v69
	v_mul_f32_e32 v69, 0xbfb8aa3b, v71
	v_mul_f32_e32 v64, 0xbfb8aa3b, v64
	v_exp_f32_e32 v65, v65
	v_exp_f32_e32 v69, v69
	v_exp_f32_e32 v71, v64
	v_mul_f32_e32 v68, 0xbfb8aa3b, v68
	v_exp_f32_e32 v68, v68
	v_pk_fma_f32 v[66:67], v[66:67], s[78:79], v[74:75] op_sel_hi:[1,0,1]
	v_add_f32_e32 v65, 1.0, v65
	v_add_f32_e32 v64, 1.0, v69
	v_add_f32_e32 v69, 1.0, v71
	v_rcp_f32_e32 v71, v65
	v_mul_f32_e32 v65, 0xbfb8aa3b, v66
	v_exp_f32_e32 v65, v65
	v_add_f32_e32 v68, 1.0, v68
	v_rcp_f32_e32 v68, v68
	v_rcp_f32_e32 v69, v69
	v_add_f32_e32 v65, 1.0, v65
	s_waitcnt vmcnt(19)
	v_lshlrev_b32_e32 v83, 16, v182
	v_lshlrev_b32_e32 v82, 16, v180
	v_rcp_f32_e32 v81, v65
	v_mul_f32_e32 v65, 0xbfb8aa3b, v67
	v_pk_mul_f32 v[68:69], v[68:69], v[82:83]
	v_exp_f32_e32 v65, v65
	v_add_f32_e32 v68, v100, v68
	v_add_f32_e32 v82, v68, v69
	v_and_b32_e32 v69, 0xffff0000, v182
	v_and_b32_e32 v68, 0xffff0000, v180
	v_pk_mul_f32 v[68:69], v[70:71], v[68:69]
	v_add_f32_e32 v65, 1.0, v65
	v_add_f32_e32 v66, v94, v68
	v_rcp_f32_e32 v64, v64
	v_add_f32_e32 v70, v66, v69
	v_lshlrev_b32_e32 v69, 16, v183
	v_lshlrev_b32_e32 v68, 16, v181
	v_rcp_f32_e32 v65, v65
	v_pk_mul_f32 v[66:67], v[80:81], v[68:69]
	v_pk_fma_f32 v[60:61], v[60:61], s[78:79], v[88:89] op_sel_hi:[1,0,1]
	v_add_f32_e32 v66, v92, v66
	v_add_f32_e32 v68, v66, v67
	v_and_b32_e32 v67, 0xffff0000, v183
	v_and_b32_e32 v66, 0xffff0000, v181
	v_pk_mul_f32 v[64:65], v[64:65], v[66:67]
	s_mov_b32 s2, 0x30000
	v_add_f32_e32 v64, v93, v64
	v_add_co_u32_e32 v66, vcc, s2, v146
	v_pk_fma_f32 v[62:63], v[62:63], s[78:79], v[90:91] op_sel_hi:[1,0,1]
	v_mul_f32_e32 v61, 0xbfb8aa3b, v61
	v_add_f32_e32 v65, v64, v65
	v_cvt_pk_bf16_f32 v64, v82, v70
	v_addc_co_u32_e32 v67, vcc, 0, v147, vcc
	v_exp_f32_e32 v61, v61
	v_mul_f32_e32 v62, 0xbfb8aa3b, v62
	v_cvt_pk_bf16_f32 v65, v68, v65
	global_store_dwordx2 v[66:67], v[64:65], off
	v_exp_f32_e32 v64, v62
	v_add_f32_e32 v61, 1.0, v61
	v_pk_fma_f32 v[56:57], v[56:57], s[78:79], v[84:85] op_sel_hi:[1,0,1]
	v_rcp_f32_e32 v62, v61
	v_add_f32_e32 v61, 1.0, v64
	v_mul_f32_e32 v57, 0xbfb8aa3b, v57
	v_rcp_f32_e32 v64, v61
	v_mul_f32_e32 v61, 0xbfb8aa3b, v63
	v_mul_f32_e32 v56, 0xbfb8aa3b, v56
	v_exp_f32_e32 v57, v57
	v_exp_f32_e32 v61, v61
	v_exp_f32_e32 v63, v56
	v_mul_f32_e32 v60, 0xbfb8aa3b, v60
	v_exp_f32_e32 v60, v60
	v_pk_fma_f32 v[58:59], v[58:59], s[78:79], v[86:87] op_sel_hi:[1,0,1]
	v_add_f32_e32 v57, 1.0, v57
	v_add_f32_e32 v56, 1.0, v61
	v_add_f32_e32 v61, 1.0, v63
	v_rcp_f32_e32 v63, v57
	v_mul_f32_e32 v57, 0xbfb8aa3b, v58
	v_exp_f32_e32 v57, v57
	v_add_f32_e32 v60, 1.0, v60
	v_rcp_f32_e32 v60, v60
	v_rcp_f32_e32 v61, v61
	v_add_f32_e32 v57, 1.0, v57
	s_waitcnt vmcnt(18)
	v_lshlrev_b32_e32 v67, 16, v178
	v_lshlrev_b32_e32 v66, 16, v176
	v_rcp_f32_e32 v65, v57
	v_mul_f32_e32 v57, 0xbfb8aa3b, v59
	v_pk_mul_f32 v[60:61], v[60:61], v[66:67]
	v_exp_f32_e32 v57, v57
	v_add_f32_e32 v60, 0, v60
	v_add_f32_e32 v66, v60, v61
	v_and_b32_e32 v61, 0xffff0000, v178
	v_and_b32_e32 v60, 0xffff0000, v176
	v_pk_mul_f32 v[60:61], v[62:63], v[60:61]
	v_add_f32_e32 v57, 1.0, v57
	v_add_f32_e32 v58, 0, v60
	v_rcp_f32_e32 v56, v56
	v_add_f32_e32 v62, v58, v61
	v_lshlrev_b32_e32 v61, 16, v179
	v_lshlrev_b32_e32 v60, 16, v177
	v_rcp_f32_e32 v57, v57
	v_pk_mul_f32 v[58:59], v[64:65], v[60:61]
	v_pk_fma_f32 v[52:53], v[52:53], s[78:79], v[76:77] op_sel_hi:[1,0,1]
	v_add_f32_e32 v58, 0, v58
	v_add_f32_e32 v60, v58, v59
	v_and_b32_e32 v59, 0xffff0000, v179
	v_and_b32_e32 v58, 0xffff0000, v177
	v_pk_mul_f32 v[56:57], v[56:57], v[58:59]
	v_pk_fma_f32 v[54:55], v[54:55], s[78:79], v[78:79] op_sel_hi:[1,0,1]
	v_mul_f32_e32 v53, 0xbfb8aa3b, v53
	v_add_f32_e32 v56, 0, v56
	v_exp_f32_e32 v53, v53
	v_mul_f32_e32 v54, 0xbfb8aa3b, v54
	v_add_f32_e32 v61, v56, v57
	v_exp_f32_e32 v56, v54
	v_add_f32_e32 v53, 1.0, v53
	v_pk_fma_f32 v[48:49], v[48:49], s[78:79], v[72:73] op_sel_hi:[1,0,1]
	v_rcp_f32_e32 v54, v53
	v_add_f32_e32 v53, 1.0, v56
	v_mul_f32_e32 v49, 0xbfb8aa3b, v49
	v_rcp_f32_e32 v56, v53
	v_mul_f32_e32 v53, 0xbfb8aa3b, v55
	v_mul_f32_e32 v48, 0xbfb8aa3b, v48
	v_exp_f32_e32 v49, v49
	v_exp_f32_e32 v53, v53
	v_exp_f32_e32 v55, v48
	v_mul_f32_e32 v52, 0xbfb8aa3b, v52
	v_exp_f32_e32 v52, v52
	v_pk_fma_f32 v[50:51], v[50:51], s[78:79], v[74:75] op_sel_hi:[1,0,1]
	v_add_f32_e32 v49, 1.0, v49
	v_add_f32_e32 v48, 1.0, v53
	v_add_f32_e32 v53, 1.0, v55
	v_rcp_f32_e32 v55, v49
	v_mul_f32_e32 v49, 0xbfb8aa3b, v50
	v_exp_f32_e32 v49, v49
	v_add_f32_e32 v52, 1.0, v52
	v_rcp_f32_e32 v52, v52
	v_rcp_f32_e32 v53, v53
	v_add_f32_e32 v49, 1.0, v49
	s_waitcnt vmcnt(16)
	v_lshlrev_b32_e32 v59, 16, v174
	v_lshlrev_b32_e32 v58, 16, v172
	v_rcp_f32_e32 v57, v49
	v_mul_f32_e32 v49, 0xbfb8aa3b, v51
	v_pk_mul_f32 v[52:53], v[52:53], v[58:59]
	v_exp_f32_e32 v49, v49
	v_add_f32_e32 v52, v66, v52
	v_add_f32_e32 v58, v52, v53
	v_and_b32_e32 v53, 0xffff0000, v174
	v_and_b32_e32 v52, 0xffff0000, v172
	v_pk_mul_f32 v[52:53], v[54:55], v[52:53]
	v_add_f32_e32 v49, 1.0, v49
	v_add_f32_e32 v50, v62, v52
	v_rcp_f32_e32 v48, v48
	v_add_f32_e32 v54, v50, v53
	v_lshlrev_b32_e32 v53, 16, v175
	v_lshlrev_b32_e32 v52, 16, v173
	v_rcp_f32_e32 v49, v49
	v_pk_mul_f32 v[50:51], v[56:57], v[52:53]
	v_pk_fma_f32 v[44:45], v[44:45], s[78:79], v[88:89] op_sel_hi:[1,0,1]
	v_add_f32_e32 v50, v60, v50
	v_add_f32_e32 v52, v50, v51
	v_and_b32_e32 v51, 0xffff0000, v175
	v_and_b32_e32 v50, 0xffff0000, v173
	v_pk_mul_f32 v[48:49], v[48:49], v[50:51]
	s_mov_b32 s2, 0x80000
	v_add_f32_e32 v48, v61, v48
	v_add_co_u32_e32 v50, vcc, s2, v146
	v_pk_fma_f32 v[46:47], v[46:47], s[78:79], v[90:91] op_sel_hi:[1,0,1]
	v_mul_f32_e32 v45, 0xbfb8aa3b, v45
	v_add_f32_e32 v49, v48, v49
	v_cvt_pk_bf16_f32 v48, v58, v54
	v_addc_co_u32_e32 v51, vcc, 0, v147, vcc
	v_exp_f32_e32 v45, v45
	v_mul_f32_e32 v46, 0xbfb8aa3b, v46
	v_cvt_pk_bf16_f32 v49, v52, v49
	global_store_dwordx2 v[50:51], v[48:49], off
	v_exp_f32_e32 v48, v46
	v_add_f32_e32 v45, 1.0, v45
	v_pk_fma_f32 v[40:41], v[40:41], s[78:79], v[84:85] op_sel_hi:[1,0,1]
	v_rcp_f32_e32 v46, v45
	v_add_f32_e32 v45, 1.0, v48
	v_mul_f32_e32 v41, 0xbfb8aa3b, v41
	v_rcp_f32_e32 v48, v45
	v_mul_f32_e32 v45, 0xbfb8aa3b, v47
	v_mul_f32_e32 v40, 0xbfb8aa3b, v40
	v_exp_f32_e32 v41, v41
	v_exp_f32_e32 v45, v45
	v_exp_f32_e32 v47, v40
	v_mul_f32_e32 v44, 0xbfb8aa3b, v44
	v_exp_f32_e32 v44, v44
	v_pk_fma_f32 v[42:43], v[42:43], s[78:79], v[86:87] op_sel_hi:[1,0,1]
	v_add_f32_e32 v41, 1.0, v41
	v_add_f32_e32 v40, 1.0, v45
	v_add_f32_e32 v45, 1.0, v47
	v_rcp_f32_e32 v47, v41
	v_mul_f32_e32 v41, 0xbfb8aa3b, v42
	v_exp_f32_e32 v41, v41
	v_add_f32_e32 v44, 1.0, v44
	v_rcp_f32_e32 v44, v44
	v_rcp_f32_e32 v45, v45
	v_add_f32_e32 v41, 1.0, v41
	s_waitcnt vmcnt(15)
	v_lshlrev_b32_e32 v51, 16, v170
	v_lshlrev_b32_e32 v50, 16, v168
	v_rcp_f32_e32 v49, v41
	v_mul_f32_e32 v41, 0xbfb8aa3b, v43
	v_pk_mul_f32 v[44:45], v[44:45], v[50:51]
	v_exp_f32_e32 v41, v41
	v_add_f32_e32 v44, 0, v44
	v_add_f32_e32 v50, v44, v45
	v_and_b32_e32 v45, 0xffff0000, v170
	v_and_b32_e32 v44, 0xffff0000, v168
	v_pk_mul_f32 v[44:45], v[46:47], v[44:45]
	v_add_f32_e32 v41, 1.0, v41
	v_add_f32_e32 v42, 0, v44
	v_rcp_f32_e32 v40, v40
	v_add_f32_e32 v46, v42, v45
	v_lshlrev_b32_e32 v45, 16, v171
	v_lshlrev_b32_e32 v44, 16, v169
	v_rcp_f32_e32 v41, v41
	v_pk_mul_f32 v[42:43], v[48:49], v[44:45]
	v_pk_fma_f32 v[36:37], v[36:37], s[78:79], v[76:77] op_sel_hi:[1,0,1]
	v_add_f32_e32 v42, 0, v42
	v_add_f32_e32 v44, v42, v43
	v_and_b32_e32 v43, 0xffff0000, v171
	v_and_b32_e32 v42, 0xffff0000, v169
	v_pk_mul_f32 v[40:41], v[40:41], v[42:43]
	v_pk_fma_f32 v[38:39], v[38:39], s[78:79], v[78:79] op_sel_hi:[1,0,1]
	v_mul_f32_e32 v37, 0xbfb8aa3b, v37
	v_add_f32_e32 v40, 0, v40
	v_exp_f32_e32 v37, v37
	v_mul_f32_e32 v38, 0xbfb8aa3b, v38
	v_add_f32_e32 v45, v40, v41
	v_exp_f32_e32 v40, v38
	v_add_f32_e32 v37, 1.0, v37
	v_pk_fma_f32 v[32:33], v[32:33], s[78:79], v[72:73] op_sel_hi:[1,0,1]
	v_rcp_f32_e32 v38, v37
	v_add_f32_e32 v37, 1.0, v40
	v_mul_f32_e32 v33, 0xbfb8aa3b, v33
	v_rcp_f32_e32 v40, v37
	v_mul_f32_e32 v37, 0xbfb8aa3b, v39
	v_mul_f32_e32 v32, 0xbfb8aa3b, v32
	v_exp_f32_e32 v33, v33
	v_exp_f32_e32 v37, v37
	v_exp_f32_e32 v39, v32
	v_mul_f32_e32 v36, 0xbfb8aa3b, v36
	v_exp_f32_e32 v36, v36
	v_pk_fma_f32 v[34:35], v[34:35], s[78:79], v[74:75] op_sel_hi:[1,0,1]
	v_add_f32_e32 v33, 1.0, v33
	v_add_f32_e32 v32, 1.0, v37
	v_add_f32_e32 v37, 1.0, v39
	v_rcp_f32_e32 v39, v33
	v_mul_f32_e32 v33, 0xbfb8aa3b, v34
	v_exp_f32_e32 v33, v33
	v_add_f32_e32 v36, 1.0, v36
	v_rcp_f32_e32 v36, v36
	v_rcp_f32_e32 v37, v37
	v_add_f32_e32 v33, 1.0, v33
	s_waitcnt vmcnt(13)
	v_lshlrev_b32_e32 v43, 16, v164
	v_lshlrev_b32_e32 v42, 16, v162
	v_rcp_f32_e32 v41, v33
	v_mul_f32_e32 v33, 0xbfb8aa3b, v35
	v_pk_mul_f32 v[36:37], v[36:37], v[42:43]
	v_exp_f32_e32 v33, v33
	v_add_f32_e32 v36, v50, v36
	v_add_f32_e32 v42, v36, v37
	v_and_b32_e32 v37, 0xffff0000, v164
	v_and_b32_e32 v36, 0xffff0000, v162
	v_pk_mul_f32 v[36:37], v[38:39], v[36:37]
	v_add_f32_e32 v33, 1.0, v33
	v_add_f32_e32 v34, v46, v36
	v_rcp_f32_e32 v32, v32
	v_add_f32_e32 v38, v34, v37
	v_lshlrev_b32_e32 v37, 16, v165
	v_lshlrev_b32_e32 v36, 16, v163
	v_rcp_f32_e32 v33, v33
	v_pk_mul_f32 v[34:35], v[40:41], v[36:37]
	v_pk_fma_f32 v[28:29], v[28:29], s[78:79], v[88:89] op_sel_hi:[1,0,1]
	v_add_f32_e32 v34, v44, v34
	v_add_f32_e32 v36, v34, v35
	v_and_b32_e32 v35, 0xffff0000, v165
	v_and_b32_e32 v34, 0xffff0000, v163
	v_pk_mul_f32 v[32:33], v[32:33], v[34:35]
	s_mov_b32 s2, 0x90000
	v_add_f32_e32 v32, v45, v32
	v_add_co_u32_e32 v34, vcc, s2, v146
	v_pk_fma_f32 v[30:31], v[30:31], s[78:79], v[90:91] op_sel_hi:[1,0,1]
	v_mul_f32_e32 v29, 0xbfb8aa3b, v29
	v_add_f32_e32 v33, v32, v33
	v_cvt_pk_bf16_f32 v32, v42, v38
	v_addc_co_u32_e32 v35, vcc, 0, v147, vcc
	v_exp_f32_e32 v29, v29
	v_mul_f32_e32 v30, 0xbfb8aa3b, v30
	v_cvt_pk_bf16_f32 v33, v36, v33
	global_store_dwordx2 v[34:35], v[32:33], off
	v_exp_f32_e32 v32, v30
	v_add_f32_e32 v29, 1.0, v29
	v_pk_fma_f32 v[24:25], v[24:25], s[78:79], v[84:85] op_sel_hi:[1,0,1]
	v_rcp_f32_e32 v30, v29
	v_add_f32_e32 v29, 1.0, v32
	v_mul_f32_e32 v25, 0xbfb8aa3b, v25
	v_rcp_f32_e32 v32, v29
	v_mul_f32_e32 v29, 0xbfb8aa3b, v31
	v_mul_f32_e32 v24, 0xbfb8aa3b, v24
	v_exp_f32_e32 v25, v25
	v_exp_f32_e32 v29, v29
	v_exp_f32_e32 v31, v24
	v_mul_f32_e32 v28, 0xbfb8aa3b, v28
	v_exp_f32_e32 v28, v28
	v_pk_fma_f32 v[26:27], v[26:27], s[78:79], v[86:87] op_sel_hi:[1,0,1]
	v_add_f32_e32 v25, 1.0, v25
	v_add_f32_e32 v24, 1.0, v29
	v_add_f32_e32 v29, 1.0, v31
	v_rcp_f32_e32 v31, v25
	v_mul_f32_e32 v25, 0xbfb8aa3b, v26
	v_exp_f32_e32 v25, v25
	v_add_f32_e32 v28, 1.0, v28
	v_rcp_f32_e32 v28, v28
	v_rcp_f32_e32 v29, v29
	v_add_f32_e32 v25, 1.0, v25
	s_waitcnt vmcnt(12)
	v_lshlrev_b32_e32 v35, 16, v160
	v_lshlrev_b32_e32 v34, 16, v158
	v_rcp_f32_e32 v33, v25
	v_mul_f32_e32 v25, 0xbfb8aa3b, v27
	v_pk_mul_f32 v[28:29], v[28:29], v[34:35]
	v_exp_f32_e32 v25, v25
	v_add_f32_e32 v28, 0, v28
	v_add_f32_e32 v34, v28, v29
	v_and_b32_e32 v29, 0xffff0000, v160
	v_and_b32_e32 v28, 0xffff0000, v158
	v_pk_mul_f32 v[28:29], v[30:31], v[28:29]
	v_add_f32_e32 v25, 1.0, v25
	v_add_f32_e32 v26, 0, v28
	v_rcp_f32_e32 v24, v24
	v_add_f32_e32 v30, v26, v29
	v_lshlrev_b32_e32 v29, 16, v161
	v_lshlrev_b32_e32 v28, 16, v159
	v_rcp_f32_e32 v25, v25
	v_pk_mul_f32 v[26:27], v[32:33], v[28:29]
	v_pk_fma_f32 v[20:21], v[20:21], s[78:79], v[76:77] op_sel_hi:[1,0,1]
	v_add_f32_e32 v26, 0, v26
	v_add_f32_e32 v28, v26, v27
	v_and_b32_e32 v27, 0xffff0000, v161
	v_and_b32_e32 v26, 0xffff0000, v159
	v_pk_mul_f32 v[24:25], v[24:25], v[26:27]
	v_pk_fma_f32 v[22:23], v[22:23], s[78:79], v[78:79] op_sel_hi:[1,0,1]
	v_mul_f32_e32 v21, 0xbfb8aa3b, v21
	v_add_f32_e32 v24, 0, v24
	v_exp_f32_e32 v21, v21
	v_mul_f32_e32 v22, 0xbfb8aa3b, v22
	v_add_f32_e32 v29, v24, v25
	v_exp_f32_e32 v24, v22
	v_add_f32_e32 v21, 1.0, v21
	v_pk_fma_f32 v[16:17], v[16:17], s[78:79], v[72:73] op_sel_hi:[1,0,1]
	v_rcp_f32_e32 v22, v21
	v_add_f32_e32 v21, 1.0, v24
	v_mul_f32_e32 v17, 0xbfb8aa3b, v17
	v_rcp_f32_e32 v24, v21
	v_mul_f32_e32 v21, 0xbfb8aa3b, v23
	v_mul_f32_e32 v16, 0xbfb8aa3b, v16
	v_exp_f32_e32 v17, v17
	v_exp_f32_e32 v21, v21
	v_exp_f32_e32 v23, v16
	v_mul_f32_e32 v20, 0xbfb8aa3b, v20
	v_exp_f32_e32 v20, v20
	v_pk_fma_f32 v[18:19], v[18:19], s[78:79], v[74:75] op_sel_hi:[1,0,1]
	v_add_f32_e32 v17, 1.0, v17
	v_add_f32_e32 v16, 1.0, v21
	v_add_f32_e32 v21, 1.0, v23
	v_rcp_f32_e32 v23, v17
	v_mul_f32_e32 v17, 0xbfb8aa3b, v18
	v_exp_f32_e32 v17, v17
	v_add_f32_e32 v20, 1.0, v20
	v_rcp_f32_e32 v20, v20
	v_rcp_f32_e32 v21, v21
	v_add_f32_e32 v17, 1.0, v17
	s_waitcnt vmcnt(10)
	v_lshlrev_b32_e32 v27, 16, v156
	v_lshlrev_b32_e32 v26, 16, v154
	v_rcp_f32_e32 v25, v17
	v_mul_f32_e32 v17, 0xbfb8aa3b, v19
	v_pk_mul_f32 v[20:21], v[20:21], v[26:27]
	v_exp_f32_e32 v17, v17
	v_add_f32_e32 v20, v34, v20
	v_add_f32_e32 v26, v20, v21
	v_and_b32_e32 v21, 0xffff0000, v156
	v_and_b32_e32 v20, 0xffff0000, v154
	v_pk_mul_f32 v[20:21], v[22:23], v[20:21]
	v_add_f32_e32 v17, 1.0, v17
	v_add_f32_e32 v18, v30, v20
	v_rcp_f32_e32 v16, v16
	v_add_f32_e32 v22, v18, v21
	v_lshlrev_b32_e32 v21, 16, v157
	v_lshlrev_b32_e32 v20, 16, v155
	v_rcp_f32_e32 v17, v17
	v_pk_mul_f32 v[18:19], v[24:25], v[20:21]
	v_pk_fma_f32 v[12:13], v[12:13], s[78:79], v[88:89] op_sel_hi:[1,0,1]
	v_add_f32_e32 v18, v28, v18
	v_add_f32_e32 v20, v18, v19
	v_and_b32_e32 v19, 0xffff0000, v157
	v_and_b32_e32 v18, 0xffff0000, v155
	v_pk_mul_f32 v[16:17], v[16:17], v[18:19]
	s_mov_b32 s2, 0xa0000
	v_add_f32_e32 v16, v29, v16
	v_add_co_u32_e32 v18, vcc, s2, v146
	v_pk_fma_f32 v[14:15], v[14:15], s[78:79], v[90:91] op_sel_hi:[1,0,1]
	v_mul_f32_e32 v13, 0xbfb8aa3b, v13
	v_add_f32_e32 v17, v16, v17
	v_cvt_pk_bf16_f32 v16, v26, v22
	v_addc_co_u32_e32 v19, vcc, 0, v147, vcc
	v_exp_f32_e32 v13, v13
	v_mul_f32_e32 v14, 0xbfb8aa3b, v14
	v_cvt_pk_bf16_f32 v17, v20, v17
	global_store_dwordx2 v[18:19], v[16:17], off
	v_exp_f32_e32 v16, v14
	v_add_f32_e32 v13, 1.0, v13
	v_pk_fma_f32 v[8:9], v[8:9], s[78:79], v[84:85] op_sel_hi:[1,0,1]
	v_rcp_f32_e32 v14, v13
	v_add_f32_e32 v13, 1.0, v16
	v_mul_f32_e32 v9, 0xbfb8aa3b, v9
	v_rcp_f32_e32 v16, v13
	v_mul_f32_e32 v13, 0xbfb8aa3b, v15
	v_mul_f32_e32 v8, 0xbfb8aa3b, v8
	v_exp_f32_e32 v9, v9
	v_exp_f32_e32 v13, v13
	v_exp_f32_e32 v15, v8
	v_mul_f32_e32 v12, 0xbfb8aa3b, v12
	v_exp_f32_e32 v12, v12
	v_pk_fma_f32 v[10:11], v[10:11], s[78:79], v[86:87] op_sel_hi:[1,0,1]
	v_add_f32_e32 v9, 1.0, v9
	v_add_f32_e32 v8, 1.0, v13
	v_add_f32_e32 v13, 1.0, v15
	v_rcp_f32_e32 v15, v9
	v_mul_f32_e32 v9, 0xbfb8aa3b, v10
	v_exp_f32_e32 v9, v9
	v_add_f32_e32 v12, 1.0, v12
	v_rcp_f32_e32 v12, v12
	v_rcp_f32_e32 v13, v13
	v_add_f32_e32 v9, 1.0, v9
	s_waitcnt vmcnt(9)
	v_lshlrev_b32_e32 v19, 16, v152
	v_lshlrev_b32_e32 v18, 16, v150
	v_rcp_f32_e32 v17, v9
	v_mul_f32_e32 v9, 0xbfb8aa3b, v11
	v_pk_mul_f32 v[12:13], v[12:13], v[18:19]
	v_exp_f32_e32 v9, v9
	v_add_f32_e32 v12, 0, v12
	v_add_f32_e32 v18, v12, v13
	v_and_b32_e32 v13, 0xffff0000, v152
	v_and_b32_e32 v12, 0xffff0000, v150
	v_pk_mul_f32 v[12:13], v[14:15], v[12:13]
	v_add_f32_e32 v9, 1.0, v9
	v_add_f32_e32 v10, 0, v12
	v_rcp_f32_e32 v8, v8
	v_add_f32_e32 v14, v10, v13
	v_lshlrev_b32_e32 v13, 16, v153
	v_lshlrev_b32_e32 v12, 16, v151
	v_rcp_f32_e32 v9, v9
	v_pk_mul_f32 v[10:11], v[16:17], v[12:13]
	v_pk_fma_f32 v[4:5], v[4:5], s[78:79], v[76:77] op_sel_hi:[1,0,1]
	v_add_f32_e32 v10, 0, v10
	v_add_f32_e32 v12, v10, v11
	v_and_b32_e32 v11, 0xffff0000, v153
	v_and_b32_e32 v10, 0xffff0000, v151
	v_pk_mul_f32 v[8:9], v[8:9], v[10:11]
	v_pk_fma_f32 v[6:7], v[6:7], s[78:79], v[78:79] op_sel_hi:[1,0,1]
	v_mul_f32_e32 v5, 0xbfb8aa3b, v5
	v_add_f32_e32 v8, 0, v8
	v_exp_f32_e32 v5, v5
	v_mul_f32_e32 v6, 0xbfb8aa3b, v6
	v_add_f32_e32 v13, v8, v9
	v_exp_f32_e32 v8, v6
	v_add_f32_e32 v5, 1.0, v5
	v_pk_fma_f32 v[0:1], v[0:1], s[78:79], v[72:73] op_sel_hi:[1,0,1]
	v_rcp_f32_e32 v6, v5
	v_add_f32_e32 v5, 1.0, v8
	v_mul_f32_e32 v1, 0xbfb8aa3b, v1
	v_rcp_f32_e32 v8, v5
	v_mul_f32_e32 v5, 0xbfb8aa3b, v7
	v_mul_f32_e32 v0, 0xbfb8aa3b, v0
	v_exp_f32_e32 v1, v1
	v_exp_f32_e32 v5, v5
	v_exp_f32_e32 v7, v0
	v_mul_f32_e32 v4, 0xbfb8aa3b, v4
	v_exp_f32_e32 v4, v4
	v_pk_fma_f32 v[2:3], v[2:3], s[78:79], v[74:75] op_sel_hi:[1,0,1]
	v_add_f32_e32 v1, 1.0, v1
	v_add_f32_e32 v0, 1.0, v5
	v_add_f32_e32 v5, 1.0, v7
	v_rcp_f32_e32 v7, v1
	v_mul_f32_e32 v1, 0xbfb8aa3b, v2
	v_exp_f32_e32 v1, v1
	v_add_f32_e32 v4, 1.0, v4
	v_rcp_f32_e32 v4, v4
	v_rcp_f32_e32 v5, v5
	v_add_f32_e32 v1, 1.0, v1
	s_waitcnt vmcnt(7)
	v_lshlrev_b32_e32 v11, 16, v148
	v_lshlrev_b32_e32 v10, 16, v142
	v_rcp_f32_e32 v9, v1
	v_mul_f32_e32 v1, 0xbfb8aa3b, v3
	v_pk_mul_f32 v[4:5], v[4:5], v[10:11]
	v_exp_f32_e32 v1, v1
	v_add_f32_e32 v4, v18, v4
	v_add_f32_e32 v10, v4, v5
	v_and_b32_e32 v5, 0xffff0000, v148
	v_and_b32_e32 v4, 0xffff0000, v142
	v_pk_mul_f32 v[4:5], v[6:7], v[4:5]
	v_add_f32_e32 v1, 1.0, v1
	v_add_f32_e32 v2, v14, v4
	v_rcp_f32_e32 v0, v0
	v_add_f32_e32 v6, v2, v5
	v_lshlrev_b32_e32 v5, 16, v149
	v_lshlrev_b32_e32 v4, 16, v143
	v_rcp_f32_e32 v1, v1
	v_pk_mul_f32 v[2:3], v[8:9], v[4:5]
	s_mov_b32 s2, s20
	v_add_f32_e32 v2, v12, v2
	v_add_f32_e32 v4, v2, v3
	v_and_b32_e32 v3, 0xffff0000, v149
	v_and_b32_e32 v2, 0xffff0000, v143
	v_pk_mul_f32 v[0:1], v[0:1], v[2:3]
	v_add_co_u32_e32 v2, vcc, 0xb0000, v146
	v_add_f32_e32 v0, v13, v0
	s_nop 0
	v_addc_co_u32_e32 v3, vcc, 0, v147, vcc
	v_add_f32_e32 v1, v0, v1
	s_and_b64 vcc, exec, s[4:5]
	s_mov_b32 s18, s21
	s_mov_b32 s47, s23
	s_mov_b32 s46, s22
	v_mov_b32_e32 v213, 0x358637bd
	v_mov_b32_e32 v252, 0x3ba10414
	v_mov_b32_e32 v242, 2
	v_cvt_pk_bf16_f32 v0, v10, v6
	v_cvt_pk_bf16_f32 v1, v4, v1
	global_store_dwordx2 v[2:3], v[0:1], off
	s_cbranch_vccz .LBB0_1421
	s_branch .LBB0_1430

.LBB0_1496:
	ds_read_b128 v[32:35], v153
	ds_read_b128 v[36:39], v153 offset:1024
	ds_read_b128 v[40:43], v153 offset:2048
	ds_read_b128 v[44:47], v153 offset:3072
	s_add_i32 s10, s50, 0xfff80080
	s_cmp_eq_u32 s52, 28
	s_cselect_b32 s55, s48, s10
	s_cselect_b32 s53, s49, s51
	s_or_b32 s54, s55, 0x80
	s_mov_b32 m0, s44
	ds_read_b128 v[156:159], v154
	ds_read_b128 v[160:163], v154 offset:1024
	ds_read_b128 v[164:167], v154 offset:2048
	ds_read_b128 v[168:171], v154 offset:3072
	ds_read_b128 v[172:175], v154 offset:4096
	ds_read_b128 v[176:179], v154 offset:5120
	ds_read_b128 v[180:183], v154 offset:6144
	ds_read_b128 v[184:187], v154 offset:7168
	buffer_load_dwordx4 v149, s[72:75], s50 offen lds
	s_mov_b32 m0, s45
	s_nop 0
	buffer_load_dwordx4 v151, s[72:75], s50 offen lds
	s_waitcnt lgkmcnt(8)
	s_barrier
	s_setprio 1
	s_waitcnt lgkmcnt(7)
	v_mfma_f32_16x16x32_bf16 v[142:145], v[32:35], v[156:159], v[142:145]
	v_mfma_f32_16x16x32_bf16 v[138:141], v[40:43], v[156:159], v[138:141]
	s_waitcnt lgkmcnt(5)
	v_mfma_f32_16x16x32_bf16 v[134:137], v[32:35], v[164:167], v[134:137]
	v_mfma_f32_16x16x32_bf16 v[130:133], v[40:43], v[164:167], v[130:133]
	s_waitcnt lgkmcnt(3)
	v_mfma_f32_16x16x32_bf16 v[110:113], v[32:35], v[172:175], v[110:113]
	v_mfma_f32_16x16x32_bf16 v[106:109], v[40:43], v[172:175], v[106:109]
	s_waitcnt lgkmcnt(1)
	v_mfma_f32_16x16x32_bf16 v[102:105], v[32:35], v[180:183], v[102:105]
	v_mfma_f32_16x16x32_bf16 v[98:101], v[40:43], v[180:183], v[98:101]
	v_mfma_f32_16x16x32_bf16 v[142:145], v[36:39], v[160:163], v[142:145]
	v_mfma_f32_16x16x32_bf16 v[138:141], v[44:47], v[160:163], v[138:141]
	v_mfma_f32_16x16x32_bf16 v[134:137], v[36:39], v[168:171], v[134:137]
	v_mfma_f32_16x16x32_bf16 v[130:133], v[44:47], v[168:171], v[130:133]
	v_mfma_f32_16x16x32_bf16 v[110:113], v[36:39], v[176:179], v[110:113]
	v_mfma_f32_16x16x32_bf16 v[106:109], v[44:47], v[176:179], v[106:109]
	s_waitcnt lgkmcnt(0)
	v_mfma_f32_16x16x32_bf16 v[102:105], v[36:39], v[184:187], v[102:105]
	v_mfma_f32_16x16x32_bf16 v[98:101], v[44:47], v[184:187], v[98:101]
	s_setprio 0
	s_barrier
	s_mov_b32 s10, s74
	s_mov_b32 s11, s75
	s_mov_b32 m0, s29
	ds_read_b128 v[188:191], v153 offset:16384
	ds_read_b128 v[192:195], v153 offset:17408
	ds_read_b128 v[196:199], v153 offset:18432
	ds_read_b128 v[200:203], v153 offset:19456
	buffer_load_dwordx4 v150, s[8:11], s53 offen lds
	s_mov_b32 m0, s30
	s_nop 0
	buffer_load_dwordx4 v152, s[8:11], s53 offen lds
	s_barrier
	s_setprio 1
	s_waitcnt lgkmcnt(3)
	v_mfma_f32_16x16x32_bf16 v[126:129], v[188:191], v[156:159], v[126:129]
	s_waitcnt lgkmcnt(1)
	v_mfma_f32_16x16x32_bf16 v[122:125], v[196:199], v[156:159], v[122:125]
	v_mfma_f32_16x16x32_bf16 v[118:121], v[188:191], v[164:167], v[118:121]
	v_mfma_f32_16x16x32_bf16 v[114:117], v[196:199], v[164:167], v[114:117]
	v_mfma_f32_16x16x32_bf16 v[92:95], v[188:191], v[172:175], v[92:95]
	v_mfma_f32_16x16x32_bf16 v[88:91], v[196:199], v[172:175], v[88:91]
	v_mfma_f32_16x16x32_bf16 v[84:87], v[188:191], v[180:183], v[84:87]
	v_mfma_f32_16x16x32_bf16 v[80:83], v[196:199], v[180:183], v[80:83]
	v_mfma_f32_16x16x32_bf16 v[126:129], v[192:195], v[160:163], v[126:129]
	s_waitcnt lgkmcnt(0)
	v_mfma_f32_16x16x32_bf16 v[122:125], v[200:203], v[160:163], v[122:125]
	v_mfma_f32_16x16x32_bf16 v[118:121], v[192:195], v[168:171], v[118:121]
	v_mfma_f32_16x16x32_bf16 v[114:117], v[200:203], v[168:171], v[114:117]
	v_mfma_f32_16x16x32_bf16 v[92:95], v[192:195], v[176:179], v[92:95]
	v_mfma_f32_16x16x32_bf16 v[88:91], v[200:203], v[176:179], v[88:91]
	v_mfma_f32_16x16x32_bf16 v[84:87], v[192:195], v[184:187], v[84:87]
	v_mfma_f32_16x16x32_bf16 v[80:83], v[200:203], v[184:187], v[80:83]
	s_setprio 0
	s_mov_b32 m0, s28
	s_barrier
	ds_read_b128 v[156:159], v154 offset:16384
	ds_read_b128 v[160:163], v154 offset:17408
	ds_read_b128 v[164:167], v154 offset:18432
	ds_read_b128 v[168:171], v154 offset:19456
	ds_read_b128 v[172:175], v154 offset:20480
	ds_read_b128 v[176:179], v154 offset:21504
	ds_read_b128 v[180:183], v154 offset:22528
	ds_read_b128 v[184:187], v154 offset:23552
	buffer_load_dwordx4 v149, s[72:75], s55 offen lds
	s_mov_b32 m0, s31
	s_nop 0
	buffer_load_dwordx4 v151, s[72:75], s55 offen lds
	s_barrier
	s_setprio 1
	s_waitcnt lgkmcnt(7)
	v_mfma_f32_16x16x32_bf16 v[76:79], v[32:35], v[156:159], v[76:79]
	v_mfma_f32_16x16x32_bf16 v[72:75], v[40:43], v[156:159], v[72:75]
	s_waitcnt lgkmcnt(5)
	v_mfma_f32_16x16x32_bf16 v[68:71], v[32:35], v[164:167], v[68:71]
	v_mfma_f32_16x16x32_bf16 v[64:67], v[40:43], v[164:167], v[64:67]
	s_waitcnt lgkmcnt(3)
	v_mfma_f32_16x16x32_bf16 v[28:31], v[32:35], v[172:175], v[28:31]
	v_mfma_f32_16x16x32_bf16 v[24:27], v[40:43], v[172:175], v[24:27]
	s_waitcnt lgkmcnt(1)
	v_mfma_f32_16x16x32_bf16 v[16:19], v[32:35], v[180:183], v[16:19]
	v_mfma_f32_16x16x32_bf16 v[8:11], v[40:43], v[180:183], v[8:11]
	v_mfma_f32_16x16x32_bf16 v[76:79], v[36:39], v[160:163], v[76:79]
	v_mfma_f32_16x16x32_bf16 v[72:75], v[44:47], v[160:163], v[72:75]
	v_mfma_f32_16x16x32_bf16 v[68:71], v[36:39], v[168:171], v[68:71]
	v_mfma_f32_16x16x32_bf16 v[64:67], v[44:47], v[168:171], v[64:67]
	v_mfma_f32_16x16x32_bf16 v[28:31], v[36:39], v[176:179], v[28:31]
	v_mfma_f32_16x16x32_bf16 v[24:27], v[44:47], v[176:179], v[24:27]
	s_waitcnt lgkmcnt(0)
	v_mfma_f32_16x16x32_bf16 v[16:19], v[36:39], v[184:187], v[16:19]
	v_mfma_f32_16x16x32_bf16 v[8:11], v[44:47], v[184:187], v[8:11]
	s_setprio 0
	s_barrier
	s_add_i32 s56, s53, 0x80000
	s_mov_b32 m0, s34
	s_nop 0
	buffer_load_dwordx4 v150, s[8:11], s56 offen lds
	s_mov_b32 m0, s35
	s_nop 0
	buffer_load_dwordx4 v152, s[8:11], s56 offen lds
	s_waitcnt vmcnt(6)
	s_barrier
	s_setprio 1
	v_mfma_f32_16x16x32_bf16 v[20:23], v[188:191], v[172:175], v[20:23]
	v_mfma_f32_16x16x32_bf16 v[12:15], v[196:199], v[172:175], v[12:15]
	v_mfma_f32_16x16x32_bf16 v[4:7], v[188:191], v[180:183], v[4:7]
	v_mfma_f32_16x16x32_bf16 v[0:3], v[196:199], v[180:183], v[0:3]
	v_mfma_f32_16x16x32_bf16 v[32:35], v[188:191], v[156:159], v[60:63]
	v_mfma_f32_16x16x32_bf16 v[36:39], v[196:199], v[156:159], v[56:59]
	v_mfma_f32_16x16x32_bf16 v[40:43], v[188:191], v[164:167], v[52:55]
	v_mfma_f32_16x16x32_bf16 v[44:47], v[196:199], v[164:167], v[48:51]
	v_mfma_f32_16x16x32_bf16 v[20:23], v[192:195], v[176:179], v[20:23]
	v_mfma_f32_16x16x32_bf16 v[12:15], v[200:203], v[176:179], v[12:15]
	v_mfma_f32_16x16x32_bf16 v[4:7], v[192:195], v[184:187], v[4:7]
	v_mfma_f32_16x16x32_bf16 v[0:3], v[200:203], v[184:187], v[0:3]
	v_mfma_f32_16x16x32_bf16 v[32:35], v[192:195], v[160:163], v[32:35]
	v_mfma_f32_16x16x32_bf16 v[36:39], v[200:203], v[160:163], v[36:39]
	v_mfma_f32_16x16x32_bf16 v[40:43], v[192:195], v[168:171], v[40:43]
	v_mfma_f32_16x16x32_bf16 v[44:47], v[200:203], v[168:171], v[44:47]
	s_setprio 0
	s_barrier
	ds_read_b128 v[48:51], v153 offset:32768
	ds_read_b128 v[52:55], v153 offset:33792
	ds_read_b128 v[56:59], v153 offset:34816
	ds_read_b128 v[60:63], v153 offset:35840
	s_add_i32 s55, s55, 0x80000
	s_mov_b32 m0, s36
	ds_read_b128 v[156:159], v154 offset:32768
	ds_read_b128 v[160:163], v154 offset:33792
	ds_read_b128 v[164:167], v154 offset:34816
	ds_read_b128 v[168:171], v154 offset:35840
	ds_read_b128 v[172:175], v154 offset:36864
	ds_read_b128 v[176:179], v154 offset:37888
	ds_read_b128 v[180:183], v154 offset:38912
	ds_read_b128 v[184:187], v154 offset:39936
	buffer_load_dwordx4 v149, s[72:75], s55 offen lds
	s_mov_b32 m0, s37
	s_nop 0
	buffer_load_dwordx4 v151, s[72:75], s55 offen lds
	s_waitcnt lgkmcnt(8)
	s_barrier
	s_setprio 1
	s_waitcnt lgkmcnt(7)
	v_mfma_f32_16x16x32_bf16 v[142:145], v[48:51], v[156:159], v[142:145]
	v_mfma_f32_16x16x32_bf16 v[138:141], v[56:59], v[156:159], v[138:141]
	s_waitcnt lgkmcnt(5)
	v_mfma_f32_16x16x32_bf16 v[134:137], v[48:51], v[164:167], v[134:137]
	v_mfma_f32_16x16x32_bf16 v[130:133], v[56:59], v[164:167], v[130:133]
	s_waitcnt lgkmcnt(3)
	v_mfma_f32_16x16x32_bf16 v[110:113], v[48:51], v[172:175], v[110:113]
	v_mfma_f32_16x16x32_bf16 v[106:109], v[56:59], v[172:175], v[106:109]
	s_waitcnt lgkmcnt(1)
	v_mfma_f32_16x16x32_bf16 v[102:105], v[48:51], v[180:183], v[102:105]
	v_mfma_f32_16x16x32_bf16 v[98:101], v[56:59], v[180:183], v[98:101]
	v_mfma_f32_16x16x32_bf16 v[142:145], v[52:55], v[160:163], v[142:145]
	v_mfma_f32_16x16x32_bf16 v[138:141], v[60:63], v[160:163], v[138:141]
	v_mfma_f32_16x16x32_bf16 v[134:137], v[52:55], v[168:171], v[134:137]
	v_mfma_f32_16x16x32_bf16 v[130:133], v[60:63], v[168:171], v[130:133]
	v_mfma_f32_16x16x32_bf16 v[110:113], v[52:55], v[176:179], v[110:113]
	v_mfma_f32_16x16x32_bf16 v[106:109], v[60:63], v[176:179], v[106:109]
	s_waitcnt lgkmcnt(0)
	v_mfma_f32_16x16x32_bf16 v[102:105], v[52:55], v[184:187], v[102:105]
	v_mfma_f32_16x16x32_bf16 v[98:101], v[60:63], v[184:187], v[98:101]
	s_setprio 0
	s_barrier
	s_or_b32 s55, s53, 0x80
	s_mov_b32 m0, s38
	ds_read_b128 v[188:191], v153 offset:49152
	ds_read_b128 v[192:195], v153 offset:50176
	ds_read_b128 v[196:199], v153 offset:51200
	ds_read_b128 v[200:203], v153 offset:52224
	buffer_load_dwordx4 v150, s[8:11], s55 offen lds
	s_mov_b32 m0, s39
	s_nop 0
	buffer_load_dwordx4 v152, s[8:11], s55 offen lds
	s_barrier
	s_setprio 1
	s_waitcnt lgkmcnt(3)
	v_mfma_f32_16x16x32_bf16 v[126:129], v[188:191], v[156:159], v[126:129]
	s_waitcnt lgkmcnt(1)
	v_mfma_f32_16x16x32_bf16 v[122:125], v[196:199], v[156:159], v[122:125]
	v_mfma_f32_16x16x32_bf16 v[118:121], v[188:191], v[164:167], v[118:121]
	v_mfma_f32_16x16x32_bf16 v[114:117], v[196:199], v[164:167], v[114:117]
	v_mfma_f32_16x16x32_bf16 v[92:95], v[188:191], v[172:175], v[92:95]
	v_mfma_f32_16x16x32_bf16 v[88:91], v[196:199], v[172:175], v[88:91]
	v_mfma_f32_16x16x32_bf16 v[84:87], v[188:191], v[180:183], v[84:87]
	v_mfma_f32_16x16x32_bf16 v[80:83], v[196:199], v[180:183], v[80:83]
	v_mfma_f32_16x16x32_bf16 v[126:129], v[192:195], v[160:163], v[126:129]
	s_waitcnt lgkmcnt(0)
	v_mfma_f32_16x16x32_bf16 v[122:125], v[200:203], v[160:163], v[122:125]
	v_mfma_f32_16x16x32_bf16 v[118:121], v[192:195], v[168:171], v[118:121]
	v_mfma_f32_16x16x32_bf16 v[114:117], v[200:203], v[168:171], v[114:117]
	v_mfma_f32_16x16x32_bf16 v[92:95], v[192:195], v[176:179], v[92:95]
	v_mfma_f32_16x16x32_bf16 v[88:91], v[200:203], v[176:179], v[88:91]
	v_mfma_f32_16x16x32_bf16 v[84:87], v[192:195], v[184:187], v[84:87]
	v_mfma_f32_16x16x32_bf16 v[80:83], v[200:203], v[184:187], v[80:83]
	s_setprio 0
	s_mov_b32 m0, s40
	s_barrier
	ds_read_b128 v[156:159], v154 offset:49152
	ds_read_b128 v[160:163], v154 offset:50176
	ds_read_b128 v[164:167], v154 offset:51200
	ds_read_b128 v[168:171], v154 offset:52224
	ds_read_b128 v[172:175], v154 offset:53248
	ds_read_b128 v[176:179], v154 offset:54272
	ds_read_b128 v[180:183], v154 offset:55296
	ds_read_b128 v[184:187], v154 offset:56320
	buffer_load_dwordx4 v149, s[72:75], s54 offen lds
	s_mov_b32 m0, s41
	s_nop 0
	buffer_load_dwordx4 v151, s[72:75], s54 offen lds
	s_barrier
	s_setprio 1
	s_waitcnt lgkmcnt(7)
	v_mfma_f32_16x16x32_bf16 v[76:79], v[48:51], v[156:159], v[76:79]
	v_mfma_f32_16x16x32_bf16 v[72:75], v[56:59], v[156:159], v[72:75]
	s_waitcnt lgkmcnt(5)
	v_mfma_f32_16x16x32_bf16 v[68:71], v[48:51], v[164:167], v[68:71]
	v_mfma_f32_16x16x32_bf16 v[64:67], v[56:59], v[164:167], v[64:67]
	s_waitcnt lgkmcnt(3)
	v_mfma_f32_16x16x32_bf16 v[28:31], v[48:51], v[172:175], v[28:31]
	v_mfma_f32_16x16x32_bf16 v[24:27], v[56:59], v[172:175], v[24:27]
	s_waitcnt lgkmcnt(1)
	v_mfma_f32_16x16x32_bf16 v[16:19], v[48:51], v[180:183], v[16:19]
	v_mfma_f32_16x16x32_bf16 v[8:11], v[56:59], v[180:183], v[8:11]
	v_mfma_f32_16x16x32_bf16 v[76:79], v[52:55], v[160:163], v[76:79]
	v_mfma_f32_16x16x32_bf16 v[72:75], v[60:63], v[160:163], v[72:75]
	v_mfma_f32_16x16x32_bf16 v[68:71], v[52:55], v[168:171], v[68:71]
	v_mfma_f32_16x16x32_bf16 v[64:67], v[60:63], v[168:171], v[64:67]
	v_mfma_f32_16x16x32_bf16 v[28:31], v[52:55], v[176:179], v[28:31]
	v_mfma_f32_16x16x32_bf16 v[24:27], v[60:63], v[176:179], v[24:27]
	s_waitcnt lgkmcnt(0)
	v_mfma_f32_16x16x32_bf16 v[16:19], v[52:55], v[184:187], v[16:19]
	v_mfma_f32_16x16x32_bf16 v[8:11], v[60:63], v[184:187], v[8:11]
	s_setprio 0
	s_barrier
	s_add_i32 s53, s53, 0x80080
	s_mov_b32 m0, s42
	s_nop 0
	buffer_load_dwordx4 v150, s[8:11], s53 offen lds
	s_mov_b32 m0, s43
	s_nop 0
	buffer_load_dwordx4 v152, s[8:11], s53 offen lds
	s_waitcnt vmcnt(6)
	s_barrier
	s_setprio 1
	v_mfma_f32_16x16x32_bf16 v[32:35], v[188:191], v[156:159], v[32:35]
	v_mfma_f32_16x16x32_bf16 v[60:63], v[192:195], v[160:163], v[32:35]
	v_mfma_f32_16x16x32_bf16 v[32:35], v[196:199], v[156:159], v[36:39]
	v_mfma_f32_16x16x32_bf16 v[56:59], v[200:203], v[160:163], v[32:35]
	v_mfma_f32_16x16x32_bf16 v[32:35], v[188:191], v[164:167], v[40:43]
	v_mfma_f32_16x16x32_bf16 v[52:55], v[192:195], v[168:171], v[32:35]
	v_mfma_f32_16x16x32_bf16 v[32:35], v[196:199], v[164:167], v[44:47]
	v_mfma_f32_16x16x32_bf16 v[20:23], v[188:191], v[172:175], v[20:23]
	v_mfma_f32_16x16x32_bf16 v[12:15], v[196:199], v[172:175], v[12:15]
	v_mfma_f32_16x16x32_bf16 v[4:7], v[188:191], v[180:183], v[4:7]
	v_mfma_f32_16x16x32_bf16 v[0:3], v[196:199], v[180:183], v[0:3]
	v_mfma_f32_16x16x32_bf16 v[48:51], v[200:203], v[168:171], v[32:35]
	v_mfma_f32_16x16x32_bf16 v[20:23], v[192:195], v[176:179], v[20:23]
	v_mfma_f32_16x16x32_bf16 v[12:15], v[200:203], v[176:179], v[12:15]
	v_mfma_f32_16x16x32_bf16 v[4:7], v[192:195], v[184:187], v[4:7]
	v_mfma_f32_16x16x32_bf16 v[0:3], v[200:203], v[184:187], v[0:3]
	s_setprio 0
	s_add_i32 s52, s52, 2
	s_addk_i32 s50, 0x100
	s_addk_i32 s51, 0x100
	s_cmp_gt_u32 s52, 29
	s_barrier
	s_cbranch_scc0 .LBB0_1496
	s_getreg_b32 s10, hwreg(HW_REG_HW_ID, 0, 6)
	s_and_b32 s10, s10, 63
	s_lshl_b32 s10, s10, 2
	s_add_i32 s10, s10, 0
	s_add_i32 s10, s10, 0x20010
	v_mov_b32_e32 v32, s10
	ds_read_b32 v32, v32
	s_min_i32 s11, s2, 64
	s_ashr_i32 s11, s11, 3
	v_mbcnt_lo_u32_b32 v155, -1, 0
	v_mbcnt_hi_u32_b32 v155, -1, v155
	s_mov_b32 s51, s23
	s_waitcnt lgkmcnt(0)
	v_readfirstlane_b32 s10, v32
	v_lshrrev_b32_e32 v34, 1, v155
	v_and_b32_e32 v157, 24, v34
	v_lshl_or_b32 v146, s10, 6, v155
	s_lshl_b32 s10, s47, 8
	s_mul_hi_i32 s47, s11, 0xc000
	s_mul_i32 s11, s11, 0xc000
	s_add_u32 s50, s0, s11
	s_addc_u32 s47, s24, s47
	s_ashr_i32 s11, s10, 31
	s_lshl_b64 s[48:49], s[10:11], 2
	v_lshrrev_b32_e32 v32, 1, v146
	s_add_u32 s48, s50, s48
	v_and_b32_e32 v156, 0x60, v32
	s_addc_u32 s49, s47, s49
	v_lshlrev_b32_e32 v96, 2, v156
	v_lshl_add_u64 v[32:33], s[48:49], 0, v[96:97]
	v_lshlrev_b32_e32 v96, 2, v157
	v_lshl_add_u64 v[36:37], v[32:33], 0, v[96:97]
	v_ashrrev_i32_e32 v96, 2, v146
	s_lshl_b32 s48, s2, 8
	v_and_b32_e32 v146, 0xffffffc0, v96
	s_ashr_i32 s49, s48, 31
	v_ashrrev_i32_e32 v147, 31, v146
	v_lshl_add_u64 v[146:147], v[146:147], 0, s[48:49]
	v_and_or_b32 v146, v155, 15, v146
	v_lshlrev_b64 v[146:147], 12, v[146:147]
	v_lshl_add_u64 v[146:147], s[12:13], 0, v[146:147]
	v_lshl_add_u64 v[146:147], s[10:11], 1, v[146:147]
	v_lshlrev_b32_e32 v96, 1, v156
	v_lshl_add_u64 v[146:147], v[146:147], 0, v[96:97]
	v_lshlrev_b32_e32 v96, 1, v157
	v_lshl_add_u64 v[146:147], v[146:147], 0, v[96:97]
	global_load_dwordx4 v[40:43], v[36:37], off offset:16
	global_load_dwordx4 v[44:47], v[36:37], off
	global_load_dwordx4 v[32:35], v[36:37], off offset:528
	s_nop 0
	global_load_dwordx4 v[36:39], v[36:37], off offset:512
	s_mov_b32 s2, 0x10000
	global_load_dwordx4 v[156:159], v[146:147], off
	v_add_co_u32_e32 v176, vcc, s2, v146
	s_mov_b32 s2, 0x30000
	s_nop 0
	v_addc_co_u32_e32 v177, vcc, 0, v147, vcc
	s_mov_b32 s47, s20
	s_mov_b32 s50, s22
	s_waitcnt vmcnt(0)
	v_lshlrev_b32_e32 v160, 16, v156
	v_and_b32_e32 v161, 0xffff0000, v156
	v_lshlrev_b32_e32 v162, 16, v157
	v_and_b32_e32 v163, 0xffff0000, v157
	v_lshlrev_b32_e32 v164, 16, v158
	v_and_b32_e32 v165, 0xffff0000, v158
	v_lshlrev_b32_e32 v166, 16, v159
	v_and_b32_e32 v167, 0xffff0000, v159
	global_load_dwordx4 v[156:159], v[146:147], off offset:256
	v_pk_fma_f32 v[144:145], v[144:145], v[46:47], v[162:163]
	v_pk_fma_f32 v[142:143], v[142:143], v[44:45], v[160:161]
	v_pk_fma_f32 v[160:161], v[140:141], v[42:43], v[166:167]
	v_pk_fma_f32 v[140:141], v[138:139], v[40:41], v[164:165]
	v_cvt_pk_bf16_f32 v138, v142, v143
	v_cvt_pk_bf16_f32 v139, v144, v145
	v_cvt_pk_bf16_f32 v140, v140, v141
	v_cvt_pk_bf16_f32 v141, v160, v161
	global_store_dwordx4 v[146:147], v[138:141], off
	s_waitcnt vmcnt(1)
	v_lshlrev_b32_e32 v168, 16, v156
	v_and_b32_e32 v169, 0xffff0000, v156
	v_lshlrev_b32_e32 v170, 16, v157
	v_and_b32_e32 v171, 0xffff0000, v157
	v_lshlrev_b32_e32 v172, 16, v158
	v_and_b32_e32 v173, 0xffff0000, v158
	v_lshlrev_b32_e32 v174, 16, v159
	v_and_b32_e32 v175, 0xffff0000, v159
	global_load_dwordx4 v[156:159], v[176:177], off
	v_pk_fma_f32 v[128:129], v[128:129], v[38:39], v[170:171]
	v_pk_fma_f32 v[126:127], v[126:127], v[36:37], v[168:169]
	v_pk_fma_f32 v[138:139], v[124:125], v[34:35], v[174:175]
	v_pk_fma_f32 v[124:125], v[122:123], v[32:33], v[172:173]
	v_cvt_pk_bf16_f32 v122, v126, v127
	v_cvt_pk_bf16_f32 v123, v128, v129
	v_cvt_pk_bf16_f32 v124, v124, v125
	v_cvt_pk_bf16_f32 v125, v138, v139
	global_store_dwordx4 v[146:147], v[122:125], off offset:256
	s_waitcnt vmcnt(1)
	v_lshlrev_b32_e32 v178, 16, v156
	v_and_b32_e32 v179, 0xffff0000, v156
	v_lshlrev_b32_e32 v180, 16, v157
	v_and_b32_e32 v181, 0xffff0000, v157
	v_lshlrev_b32_e32 v182, 16, v158
	v_and_b32_e32 v183, 0xffff0000, v158
	v_lshlrev_b32_e32 v184, 16, v159
	v_and_b32_e32 v185, 0xffff0000, v159
	global_load_dwordx4 v[156:159], v[176:177], off offset:256
	v_pk_fma_f32 v[124:125], v[136:137], v[46:47], v[180:181]
	v_pk_fma_f32 v[122:123], v[134:135], v[44:45], v[178:179]
	v_pk_fma_f32 v[126:127], v[132:133], v[42:43], v[184:185]
	v_pk_fma_f32 v[128:129], v[130:131], v[40:41], v[182:183]
	v_cvt_pk_bf16_f32 v122, v122, v123
	v_cvt_pk_bf16_f32 v123, v124, v125
	v_cvt_pk_bf16_f32 v124, v128, v129
	v_cvt_pk_bf16_f32 v125, v126, v127
	global_store_dwordx4 v[176:177], v[122:125], off
	s_waitcnt vmcnt(1)
	v_lshlrev_b32_e32 v186, 16, v156
	v_and_b32_e32 v187, 0xffff0000, v156
	v_lshlrev_b32_e32 v156, 16, v157
	v_and_b32_e32 v157, 0xffff0000, v157
	v_lshlrev_b32_e32 v188, 16, v158
	v_and_b32_e32 v189, 0xffff0000, v158
	v_lshlrev_b32_e32 v158, 16, v159
	v_and_b32_e32 v159, 0xffff0000, v159
	v_pk_fma_f32 v[118:119], v[118:119], v[36:37], v[186:187]
	v_pk_fma_f32 v[120:121], v[120:121], v[38:39], v[156:157]
	v_pk_fma_f32 v[122:123], v[116:117], v[34:35], v[158:159]
	v_pk_fma_f32 v[116:117], v[114:115], v[32:33], v[188:189]
	v_cvt_pk_bf16_f32 v114, v118, v119
	v_add_co_u32_e32 v118, vcc, s75, v146
	v_cvt_pk_bf16_f32 v115, v120, v121
	v_cvt_pk_bf16_f32 v116, v116, v117
	v_cvt_pk_bf16_f32 v117, v122, v123
	v_addc_co_u32_e32 v119, vcc, 0, v147, vcc
	global_store_dwordx4 v[176:177], v[114:117], off offset:256
	global_load_dwordx4 v[114:117], v[118:119], off
	v_add_co_u32_e32 v136, vcc, s2, v146
	s_mov_b32 s2, 0x80000
	s_nop 0
	v_addc_co_u32_e32 v137, vcc, 0, v147, vcc
	s_waitcnt vmcnt(0)
	v_lshlrev_b32_e32 v120, 16, v114
	v_and_b32_e32 v121, 0xffff0000, v114
	v_lshlrev_b32_e32 v122, 16, v115
	v_and_b32_e32 v123, 0xffff0000, v115
	v_lshlrev_b32_e32 v124, 16, v116
	v_and_b32_e32 v125, 0xffff0000, v116
	v_lshlrev_b32_e32 v126, 16, v117
	v_and_b32_e32 v127, 0xffff0000, v117
	global_load_dwordx4 v[114:117], v[118:119], off offset:256
	v_pk_fma_f32 v[112:113], v[112:113], v[46:47], v[122:123]
	v_pk_fma_f32 v[110:111], v[110:111], v[44:45], v[120:121]
	v_pk_fma_f32 v[120:121], v[108:109], v[42:43], v[126:127]
	v_pk_fma_f32 v[108:109], v[106:107], v[40:41], v[124:125]
	v_cvt_pk_bf16_f32 v106, v110, v111
	v_cvt_pk_bf16_f32 v107, v112, v113
	v_cvt_pk_bf16_f32 v108, v108, v109
	v_cvt_pk_bf16_f32 v109, v120, v121
	global_store_dwordx4 v[118:119], v[106:109], off
	s_waitcnt vmcnt(1)
	v_lshlrev_b32_e32 v128, 16, v114
	v_and_b32_e32 v129, 0xffff0000, v114
	v_lshlrev_b32_e32 v130, 16, v115
	v_and_b32_e32 v131, 0xffff0000, v115
	v_lshlrev_b32_e32 v132, 16, v116
	v_and_b32_e32 v133, 0xffff0000, v116
	v_lshlrev_b32_e32 v134, 16, v117
	v_and_b32_e32 v135, 0xffff0000, v117
	global_load_dwordx4 v[114:117], v[136:137], off
	v_pk_fma_f32 v[94:95], v[94:95], v[38:39], v[130:131]
	v_pk_fma_f32 v[92:93], v[92:93], v[36:37], v[128:129]
	v_pk_fma_f32 v[106:107], v[90:91], v[34:35], v[134:135]
	v_pk_fma_f32 v[90:91], v[88:89], v[32:33], v[132:133]
	v_cvt_pk_bf16_f32 v88, v92, v93
	v_cvt_pk_bf16_f32 v89, v94, v95
	v_cvt_pk_bf16_f32 v90, v90, v91
	v_cvt_pk_bf16_f32 v91, v106, v107
	global_store_dwordx4 v[118:119], v[88:91], off offset:256
	s_waitcnt vmcnt(1)
	v_lshlrev_b32_e32 v138, 16, v114
	v_and_b32_e32 v139, 0xffff0000, v114
	v_lshlrev_b32_e32 v140, 16, v115
	v_and_b32_e32 v141, 0xffff0000, v115
	v_lshlrev_b32_e32 v142, 16, v116
	v_and_b32_e32 v143, 0xffff0000, v116
	v_lshlrev_b32_e32 v144, 16, v117
	v_and_b32_e32 v145, 0xffff0000, v117
	global_load_dwordx4 v[114:117], v[136:137], off offset:256
	v_pk_fma_f32 v[90:91], v[104:105], v[46:47], v[140:141]
	v_pk_fma_f32 v[88:89], v[102:103], v[44:45], v[138:139]
	v_pk_fma_f32 v[92:93], v[100:101], v[42:43], v[144:145]
	v_pk_fma_f32 v[94:95], v[98:99], v[40:41], v[142:143]
	v_cvt_pk_bf16_f32 v88, v88, v89
	v_cvt_pk_bf16_f32 v89, v90, v91
	v_cvt_pk_bf16_f32 v90, v94, v95
	v_cvt_pk_bf16_f32 v91, v92, v93
	global_store_dwordx4 v[136:137], v[88:91], off
	s_waitcnt vmcnt(1)
	v_lshlrev_b32_e32 v156, 16, v114
	v_and_b32_e32 v157, 0xffff0000, v114
	v_lshlrev_b32_e32 v114, 16, v115
	v_and_b32_e32 v115, 0xffff0000, v115
	v_lshlrev_b32_e32 v158, 16, v116
	v_and_b32_e32 v159, 0xffff0000, v116
	v_lshlrev_b32_e32 v116, 16, v117
	v_and_b32_e32 v117, 0xffff0000, v117
	v_pk_fma_f32 v[86:87], v[86:87], v[38:39], v[114:115]
	v_pk_fma_f32 v[84:85], v[84:85], v[36:37], v[156:157]
	v_pk_fma_f32 v[88:89], v[82:83], v[34:35], v[116:117]
	v_pk_fma_f32 v[82:83], v[80:81], v[32:33], v[158:159]
	v_cvt_pk_bf16_f32 v80, v84, v85
	v_cvt_pk_bf16_f32 v81, v86, v87
	v_cvt_pk_bf16_f32 v82, v82, v83
	v_cvt_pk_bf16_f32 v83, v88, v89
	global_store_dwordx4 v[136:137], v[80:83], off offset:256
	s_nop 1
	v_add_co_u32_e32 v80, vcc, s2, v146
	s_mov_b32 s2, 0x90000
	s_nop 0
	v_addc_co_u32_e32 v81, vcc, 0, v147, vcc
	global_load_dwordx4 v[82:85], v[80:81], off
	v_add_co_u32_e32 v104, vcc, s2, v146
	s_mov_b32 s2, 0xa0000
	s_nop 0
	v_addc_co_u32_e32 v105, vcc, 0, v147, vcc
	s_waitcnt vmcnt(0)
	v_lshlrev_b32_e32 v86, 16, v82
	v_and_b32_e32 v87, 0xffff0000, v82
	v_lshlrev_b32_e32 v88, 16, v83
	v_and_b32_e32 v89, 0xffff0000, v83
	v_lshlrev_b32_e32 v90, 16, v84
	v_and_b32_e32 v91, 0xffff0000, v84
	v_lshlrev_b32_e32 v92, 16, v85
	v_and_b32_e32 v93, 0xffff0000, v85
	global_load_dwordx4 v[82:85], v[80:81], off offset:256
	v_pk_fma_f32 v[78:79], v[78:79], v[46:47], v[88:89]
	v_pk_fma_f32 v[76:77], v[76:77], v[44:45], v[86:87]
	v_pk_fma_f32 v[86:87], v[74:75], v[42:43], v[92:93]
	v_pk_fma_f32 v[74:75], v[72:73], v[40:41], v[90:91]
	v_cvt_pk_bf16_f32 v72, v76, v77
	v_cvt_pk_bf16_f32 v73, v78, v79
	v_cvt_pk_bf16_f32 v74, v74, v75
	v_cvt_pk_bf16_f32 v75, v86, v87
	global_store_dwordx4 v[80:81], v[72:75], off
	s_waitcnt vmcnt(1)
	v_lshlrev_b32_e32 v94, 16, v82
	v_and_b32_e32 v95, 0xffff0000, v82
	v_lshlrev_b32_e32 v98, 16, v83
	v_and_b32_e32 v99, 0xffff0000, v83
	v_lshlrev_b32_e32 v100, 16, v84
	v_and_b32_e32 v101, 0xffff0000, v84
	v_lshlrev_b32_e32 v102, 16, v85
	v_and_b32_e32 v103, 0xffff0000, v85
	global_load_dwordx4 v[82:85], v[104:105], off
	v_pk_fma_f32 v[62:63], v[62:63], v[38:39], v[98:99]
	v_pk_fma_f32 v[60:61], v[60:61], v[36:37], v[94:95]
	v_pk_fma_f32 v[72:73], v[58:59], v[34:35], v[102:103]
	v_pk_fma_f32 v[58:59], v[56:57], v[32:33], v[100:101]
	v_cvt_pk_bf16_f32 v56, v60, v61
	v_cvt_pk_bf16_f32 v57, v62, v63
	v_cvt_pk_bf16_f32 v58, v58, v59
	v_cvt_pk_bf16_f32 v59, v72, v73
	global_store_dwordx4 v[80:81], v[56:59], off offset:256
	s_waitcnt vmcnt(1)
	v_lshlrev_b32_e32 v106, 16, v82
	v_and_b32_e32 v107, 0xffff0000, v82
	v_lshlrev_b32_e32 v108, 16, v83
	v_and_b32_e32 v109, 0xffff0000, v83
	v_lshlrev_b32_e32 v110, 16, v84
	v_and_b32_e32 v111, 0xffff0000, v84
	v_lshlrev_b32_e32 v112, 16, v85
	v_and_b32_e32 v113, 0xffff0000, v85
	global_load_dwordx4 v[82:85], v[104:105], off offset:256
	v_pk_fma_f32 v[58:59], v[70:71], v[46:47], v[108:109]
	v_pk_fma_f32 v[56:57], v[68:69], v[44:45], v[106:107]
	v_pk_fma_f32 v[60:61], v[66:67], v[42:43], v[112:113]
	v_pk_fma_f32 v[62:63], v[64:65], v[40:41], v[110:111]
	v_cvt_pk_bf16_f32 v56, v56, v57
	v_cvt_pk_bf16_f32 v57, v58, v59
	v_cvt_pk_bf16_f32 v58, v62, v63
	v_cvt_pk_bf16_f32 v59, v60, v61
	global_store_dwordx4 v[104:105], v[56:59], off
	s_waitcnt vmcnt(1)
	v_lshlrev_b32_e32 v114, 16, v82
	v_and_b32_e32 v115, 0xffff0000, v82
	v_lshlrev_b32_e32 v82, 16, v83
	v_and_b32_e32 v83, 0xffff0000, v83
	v_lshlrev_b32_e32 v116, 16, v84
	v_and_b32_e32 v117, 0xffff0000, v84
	v_lshlrev_b32_e32 v84, 16, v85
	v_and_b32_e32 v85, 0xffff0000, v85
	v_pk_fma_f32 v[52:53], v[52:53], v[36:37], v[114:115]
	v_pk_fma_f32 v[54:55], v[54:55], v[38:39], v[82:83]
	v_pk_fma_f32 v[56:57], v[50:51], v[34:35], v[84:85]
	v_pk_fma_f32 v[50:51], v[48:49], v[32:33], v[116:117]
	v_cvt_pk_bf16_f32 v48, v52, v53
	v_add_co_u32_e32 v52, vcc, s2, v146
	v_cvt_pk_bf16_f32 v49, v54, v55
	v_cvt_pk_bf16_f32 v50, v50, v51
	v_cvt_pk_bf16_f32 v51, v56, v57
	v_addc_co_u32_e32 v53, vcc, 0, v147, vcc
	global_store_dwordx4 v[104:105], v[48:51], off offset:256
	global_load_dwordx4 v[48:51], v[52:53], off
	s_mov_b32 s2, 0xb0000
	v_add_co_u32_e32 v62, vcc, s2, v146
	s_mov_b32 s2, s21
	s_nop 0
	v_addc_co_u32_e32 v63, vcc, 0, v147, vcc
	s_and_b64 vcc, exec, s[4:5]
	s_waitcnt vmcnt(0)
	v_lshlrev_b32_e32 v56, 16, v48
	v_and_b32_e32 v57, 0xffff0000, v48
	v_lshlrev_b32_e32 v60, 16, v49
	v_and_b32_e32 v61, 0xffff0000, v49
	v_lshlrev_b32_e32 v54, 16, v50
	v_and_b32_e32 v55, 0xffff0000, v50
	v_lshlrev_b32_e32 v58, 16, v51
	v_and_b32_e32 v59, 0xffff0000, v51
	global_load_dwordx4 v[48:51], v[52:53], off offset:256
	v_pk_fma_f32 v[30:31], v[30:31], v[46:47], v[60:61]
	v_pk_fma_f32 v[28:29], v[28:29], v[44:45], v[56:57]
	v_pk_fma_f32 v[56:57], v[26:27], v[42:43], v[58:59]
	v_pk_fma_f32 v[26:27], v[24:25], v[40:41], v[54:55]
	v_cvt_pk_bf16_f32 v24, v28, v29
	v_cvt_pk_bf16_f32 v25, v30, v31
	v_cvt_pk_bf16_f32 v26, v26, v27
	v_cvt_pk_bf16_f32 v27, v56, v57
	global_store_dwordx4 v[52:53], v[24:27], off
	s_waitcnt vmcnt(1)
	v_lshlrev_b32_e32 v66, 16, v48
	v_and_b32_e32 v67, 0xffff0000, v48
	v_lshlrev_b32_e32 v70, 16, v49
	v_and_b32_e32 v71, 0xffff0000, v49
	v_lshlrev_b32_e32 v64, 16, v50
	v_and_b32_e32 v65, 0xffff0000, v50
	v_lshlrev_b32_e32 v68, 16, v51
	v_and_b32_e32 v69, 0xffff0000, v51
	global_load_dwordx4 v[48:51], v[62:63], off
	v_pk_fma_f32 v[22:23], v[22:23], v[38:39], v[70:71]
	v_pk_fma_f32 v[20:21], v[20:21], v[36:37], v[66:67]
	v_pk_fma_f32 v[24:25], v[14:15], v[34:35], v[68:69]
	v_pk_fma_f32 v[14:15], v[12:13], v[32:33], v[64:65]
	v_cvt_pk_bf16_f32 v12, v20, v21
	v_cvt_pk_bf16_f32 v13, v22, v23
	v_cvt_pk_bf16_f32 v14, v14, v15
	v_cvt_pk_bf16_f32 v15, v24, v25
	global_store_dwordx4 v[52:53], v[12:15], off offset:256
	s_waitcnt vmcnt(1)
	v_lshlrev_b32_e32 v74, 16, v48
	v_and_b32_e32 v75, 0xffff0000, v48
	v_lshlrev_b32_e32 v78, 16, v49
	v_and_b32_e32 v79, 0xffff0000, v49
	v_lshlrev_b32_e32 v72, 16, v50
	v_and_b32_e32 v73, 0xffff0000, v50
	v_lshlrev_b32_e32 v76, 16, v51
	v_and_b32_e32 v77, 0xffff0000, v51
	global_load_dwordx4 v[48:51], v[62:63], off offset:256
	v_pk_fma_f32 v[12:13], v[18:19], v[46:47], v[78:79]
	v_pk_fma_f32 v[14:15], v[16:17], v[44:45], v[74:75]
	v_pk_fma_f32 v[16:17], v[10:11], v[42:43], v[76:77]
	v_pk_fma_f32 v[10:11], v[8:9], v[40:41], v[72:73]
	v_cvt_pk_bf16_f32 v8, v14, v15
	v_cvt_pk_bf16_f32 v9, v12, v13
	v_cvt_pk_bf16_f32 v10, v10, v11
	v_cvt_pk_bf16_f32 v11, v16, v17
	global_store_dwordx4 v[62:63], v[8:11], off
	s_waitcnt vmcnt(1)
	v_lshlrev_b32_e32 v80, 16, v48
	v_and_b32_e32 v81, 0xffff0000, v48
	v_lshlrev_b32_e32 v48, 16, v49
	v_and_b32_e32 v49, 0xffff0000, v49
	v_lshlrev_b32_e32 v82, 16, v50
	v_and_b32_e32 v83, 0xffff0000, v50
	v_lshlrev_b32_e32 v50, 16, v51
	v_and_b32_e32 v51, 0xffff0000, v51
	v_pk_fma_f32 v[6:7], v[6:7], v[38:39], v[48:49]
	v_pk_fma_f32 v[4:5], v[4:5], v[36:37], v[80:81]
	v_pk_fma_f32 v[8:9], v[2:3], v[34:35], v[50:51]
	v_pk_fma_f32 v[2:3], v[0:1], v[32:33], v[82:83]
	v_cvt_pk_bf16_f32 v0, v4, v5
	v_cvt_pk_bf16_f32 v1, v6, v7
	v_cvt_pk_bf16_f32 v2, v2, v3
	v_cvt_pk_bf16_f32 v3, v8, v9
	global_store_dwordx4 v[62:63], v[0:3], off offset:256
	s_cbranch_vccz .LBB0_1490
	s_branch .LBB0_1499

.LBB0_1514:
	ds_read_b128 v[64:67], v154
	ds_read_b128 v[68:71], v154 offset:1024
	ds_read_b128 v[72:75], v154 offset:2048
	ds_read_b128 v[76:79], v154 offset:3072
	s_add_i32 s10, s49, 0xfff80080
	s_cmp_eq_u32 s51, 28
	s_cselect_b32 s54, s47, s10
	s_cselect_b32 s52, s48, s50
	s_or_b32 s53, s54, 0x80
	s_mov_b32 m0, s41
	ds_read_b128 v[146:149], v155
	ds_read_b128 v[156:159], v155 offset:1024
	ds_read_b128 v[160:163], v155 offset:2048
	ds_read_b128 v[164:167], v155 offset:3072
	ds_read_b128 v[168:171], v155 offset:4096
	ds_read_b128 v[172:175], v155 offset:5120
	ds_read_b128 v[176:179], v155 offset:6144
	ds_read_b128 v[180:183], v155 offset:7168
	buffer_load_dwordx4 v150, s[72:75], s49 offen lds
	s_mov_b32 m0, s42
	s_nop 0
	buffer_load_dwordx4 v152, s[72:75], s49 offen lds
	s_waitcnt lgkmcnt(8)
	s_barrier
	s_setprio 1
	s_waitcnt lgkmcnt(7)
	v_mfma_f32_16x16x32_bf16 v[142:145], v[64:67], v[146:149], v[142:145]
	v_mfma_f32_16x16x32_bf16 v[138:141], v[72:75], v[146:149], v[138:141]
	s_waitcnt lgkmcnt(5)
	v_mfma_f32_16x16x32_bf16 v[134:137], v[64:67], v[160:163], v[134:137]
	v_mfma_f32_16x16x32_bf16 v[130:133], v[72:75], v[160:163], v[130:133]
	s_waitcnt lgkmcnt(3)
	v_mfma_f32_16x16x32_bf16 v[110:113], v[64:67], v[168:171], v[110:113]
	v_mfma_f32_16x16x32_bf16 v[106:109], v[72:75], v[168:171], v[106:109]
	s_waitcnt lgkmcnt(1)
	v_mfma_f32_16x16x32_bf16 v[102:105], v[64:67], v[176:179], v[102:105]
	v_mfma_f32_16x16x32_bf16 v[98:101], v[72:75], v[176:179], v[98:101]
	v_mfma_f32_16x16x32_bf16 v[142:145], v[68:71], v[156:159], v[142:145]
	v_mfma_f32_16x16x32_bf16 v[138:141], v[76:79], v[156:159], v[138:141]
	v_mfma_f32_16x16x32_bf16 v[134:137], v[68:71], v[164:167], v[134:137]
	v_mfma_f32_16x16x32_bf16 v[130:133], v[76:79], v[164:167], v[130:133]
	v_mfma_f32_16x16x32_bf16 v[110:113], v[68:71], v[172:175], v[110:113]
	v_mfma_f32_16x16x32_bf16 v[106:109], v[76:79], v[172:175], v[106:109]
	s_waitcnt lgkmcnt(0)
	v_mfma_f32_16x16x32_bf16 v[102:105], v[68:71], v[180:183], v[102:105]
	v_mfma_f32_16x16x32_bf16 v[98:101], v[76:79], v[180:183], v[98:101]
	s_setprio 0
	s_barrier
	s_mov_b32 s10, s74
	s_mov_b32 s11, s75
	s_mov_b32 m0, s26
	ds_read_b128 v[184:187], v154 offset:16384
	ds_read_b128 v[188:191], v154 offset:17408
	ds_read_b128 v[192:195], v154 offset:18432
	ds_read_b128 v[196:199], v154 offset:19456
	buffer_load_dwordx4 v151, s[8:11], s52 offen lds
	s_mov_b32 m0, s27
	s_nop 0
	buffer_load_dwordx4 v153, s[8:11], s52 offen lds
	s_barrier
	s_setprio 1
	s_waitcnt lgkmcnt(3)
	v_mfma_f32_16x16x32_bf16 v[126:129], v[184:187], v[146:149], v[126:129]
	s_waitcnt lgkmcnt(1)
	v_mfma_f32_16x16x32_bf16 v[122:125], v[192:195], v[146:149], v[122:125]
	v_mfma_f32_16x16x32_bf16 v[118:121], v[184:187], v[160:163], v[118:121]
	v_mfma_f32_16x16x32_bf16 v[114:117], v[192:195], v[160:163], v[114:117]
	v_mfma_f32_16x16x32_bf16 v[92:95], v[184:187], v[168:171], v[92:95]
	v_mfma_f32_16x16x32_bf16 v[88:91], v[192:195], v[168:171], v[88:91]
	v_mfma_f32_16x16x32_bf16 v[84:87], v[184:187], v[176:179], v[84:87]
	v_mfma_f32_16x16x32_bf16 v[80:83], v[192:195], v[176:179], v[80:83]
	v_mfma_f32_16x16x32_bf16 v[126:129], v[188:191], v[156:159], v[126:129]
	s_waitcnt lgkmcnt(0)
	v_mfma_f32_16x16x32_bf16 v[122:125], v[196:199], v[156:159], v[122:125]
	v_mfma_f32_16x16x32_bf16 v[118:121], v[188:191], v[164:167], v[118:121]
	v_mfma_f32_16x16x32_bf16 v[114:117], v[196:199], v[164:167], v[114:117]
	v_mfma_f32_16x16x32_bf16 v[92:95], v[188:191], v[172:175], v[92:95]
	v_mfma_f32_16x16x32_bf16 v[88:91], v[196:199], v[172:175], v[88:91]
	v_mfma_f32_16x16x32_bf16 v[84:87], v[188:191], v[180:183], v[84:87]
	v_mfma_f32_16x16x32_bf16 v[80:83], v[196:199], v[180:183], v[80:83]
	s_setprio 0
	s_mov_b32 m0, s23
	s_barrier
	ds_read_b128 v[146:149], v155 offset:16384
	ds_read_b128 v[156:159], v155 offset:17408
	ds_read_b128 v[160:163], v155 offset:18432
	ds_read_b128 v[164:167], v155 offset:19456
	ds_read_b128 v[168:171], v155 offset:20480
	ds_read_b128 v[172:175], v155 offset:21504
	ds_read_b128 v[176:179], v155 offset:22528
	ds_read_b128 v[180:183], v155 offset:23552
	buffer_load_dwordx4 v150, s[72:75], s54 offen lds
	s_mov_b32 m0, s28
	s_nop 0
	buffer_load_dwordx4 v152, s[72:75], s54 offen lds
	s_barrier
	s_setprio 1
	s_waitcnt lgkmcnt(7)
	v_mfma_f32_16x16x32_bf16 v[60:63], v[64:67], v[146:149], v[60:63]
	v_mfma_f32_16x16x32_bf16 v[56:59], v[72:75], v[146:149], v[56:59]
	s_waitcnt lgkmcnt(5)
	v_mfma_f32_16x16x32_bf16 v[52:55], v[64:67], v[160:163], v[52:55]
	v_mfma_f32_16x16x32_bf16 v[48:51], v[72:75], v[160:163], v[48:51]
	s_waitcnt lgkmcnt(3)
	v_mfma_f32_16x16x32_bf16 v[28:31], v[64:67], v[168:171], v[28:31]
	v_mfma_f32_16x16x32_bf16 v[24:27], v[72:75], v[168:171], v[24:27]
	s_waitcnt lgkmcnt(1)
	v_mfma_f32_16x16x32_bf16 v[20:23], v[64:67], v[176:179], v[20:23]
	v_mfma_f32_16x16x32_bf16 v[16:19], v[72:75], v[176:179], v[16:19]
	v_mfma_f32_16x16x32_bf16 v[60:63], v[68:71], v[156:159], v[60:63]
	v_mfma_f32_16x16x32_bf16 v[56:59], v[76:79], v[156:159], v[56:59]
	v_mfma_f32_16x16x32_bf16 v[52:55], v[68:71], v[164:167], v[52:55]
	v_mfma_f32_16x16x32_bf16 v[48:51], v[76:79], v[164:167], v[48:51]
	v_mfma_f32_16x16x32_bf16 v[28:31], v[68:71], v[172:175], v[28:31]
	v_mfma_f32_16x16x32_bf16 v[24:27], v[76:79], v[172:175], v[24:27]
	s_waitcnt lgkmcnt(0)
	v_mfma_f32_16x16x32_bf16 v[20:23], v[68:71], v[180:183], v[20:23]
	v_mfma_f32_16x16x32_bf16 v[16:19], v[76:79], v[180:183], v[16:19]
	s_setprio 0
	s_barrier
	s_add_i32 s55, s52, 0x80000
	s_mov_b32 m0, s29
	s_nop 0
	buffer_load_dwordx4 v151, s[8:11], s55 offen lds
	s_mov_b32 m0, s30
	s_nop 0
	buffer_load_dwordx4 v153, s[8:11], s55 offen lds
	s_waitcnt vmcnt(6)
	s_barrier
	s_setprio 1
	v_mfma_f32_16x16x32_bf16 v[44:47], v[184:187], v[146:149], v[44:47]
	v_mfma_f32_16x16x32_bf16 v[40:43], v[192:195], v[146:149], v[40:43]
	v_mfma_f32_16x16x32_bf16 v[36:39], v[184:187], v[160:163], v[36:39]
	v_mfma_f32_16x16x32_bf16 v[32:35], v[192:195], v[160:163], v[32:35]
	v_mfma_f32_16x16x32_bf16 v[12:15], v[184:187], v[168:171], v[12:15]
	v_mfma_f32_16x16x32_bf16 v[8:11], v[192:195], v[168:171], v[8:11]
	v_mfma_f32_16x16x32_bf16 v[4:7], v[184:187], v[176:179], v[4:7]
	v_mfma_f32_16x16x32_bf16 v[0:3], v[192:195], v[176:179], v[0:3]
	v_mfma_f32_16x16x32_bf16 v[44:47], v[188:191], v[156:159], v[44:47]
	v_mfma_f32_16x16x32_bf16 v[40:43], v[196:199], v[156:159], v[40:43]
	v_mfma_f32_16x16x32_bf16 v[36:39], v[188:191], v[164:167], v[36:39]
	v_mfma_f32_16x16x32_bf16 v[32:35], v[196:199], v[164:167], v[32:35]
	v_mfma_f32_16x16x32_bf16 v[12:15], v[188:191], v[172:175], v[12:15]
	v_mfma_f32_16x16x32_bf16 v[8:11], v[196:199], v[172:175], v[8:11]
	v_mfma_f32_16x16x32_bf16 v[4:7], v[188:191], v[180:183], v[4:7]
	v_mfma_f32_16x16x32_bf16 v[0:3], v[196:199], v[180:183], v[0:3]
	s_setprio 0
	s_barrier
	ds_read_b128 v[64:67], v154 offset:32768
	ds_read_b128 v[68:71], v154 offset:33792
	ds_read_b128 v[72:75], v154 offset:34816
	ds_read_b128 v[76:79], v154 offset:35840
	s_add_i32 s54, s54, 0x80000
	s_mov_b32 m0, s31
	ds_read_b128 v[146:149], v155 offset:32768
	ds_read_b128 v[156:159], v155 offset:33792
	ds_read_b128 v[160:163], v155 offset:34816
	ds_read_b128 v[164:167], v155 offset:35840
	ds_read_b128 v[168:171], v155 offset:36864
	ds_read_b128 v[172:175], v155 offset:37888
	ds_read_b128 v[176:179], v155 offset:38912
	ds_read_b128 v[180:183], v155 offset:39936
	buffer_load_dwordx4 v150, s[72:75], s54 offen lds
	s_mov_b32 m0, s34
	s_nop 0
	buffer_load_dwordx4 v152, s[72:75], s54 offen lds
	s_waitcnt lgkmcnt(8)
	s_barrier
	s_setprio 1
	s_waitcnt lgkmcnt(7)
	v_mfma_f32_16x16x32_bf16 v[142:145], v[64:67], v[146:149], v[142:145]
	v_mfma_f32_16x16x32_bf16 v[138:141], v[72:75], v[146:149], v[138:141]
	s_waitcnt lgkmcnt(5)
	v_mfma_f32_16x16x32_bf16 v[134:137], v[64:67], v[160:163], v[134:137]
	v_mfma_f32_16x16x32_bf16 v[130:133], v[72:75], v[160:163], v[130:133]
	s_waitcnt lgkmcnt(3)
	v_mfma_f32_16x16x32_bf16 v[110:113], v[64:67], v[168:171], v[110:113]
	v_mfma_f32_16x16x32_bf16 v[106:109], v[72:75], v[168:171], v[106:109]
	s_waitcnt lgkmcnt(1)
	v_mfma_f32_16x16x32_bf16 v[102:105], v[64:67], v[176:179], v[102:105]
	v_mfma_f32_16x16x32_bf16 v[98:101], v[72:75], v[176:179], v[98:101]
	v_mfma_f32_16x16x32_bf16 v[142:145], v[68:71], v[156:159], v[142:145]
	v_mfma_f32_16x16x32_bf16 v[138:141], v[76:79], v[156:159], v[138:141]
	v_mfma_f32_16x16x32_bf16 v[134:137], v[68:71], v[164:167], v[134:137]
	v_mfma_f32_16x16x32_bf16 v[130:133], v[76:79], v[164:167], v[130:133]
	v_mfma_f32_16x16x32_bf16 v[110:113], v[68:71], v[172:175], v[110:113]
	v_mfma_f32_16x16x32_bf16 v[106:109], v[76:79], v[172:175], v[106:109]
	s_waitcnt lgkmcnt(0)
	v_mfma_f32_16x16x32_bf16 v[102:105], v[68:71], v[180:183], v[102:105]
	v_mfma_f32_16x16x32_bf16 v[98:101], v[76:79], v[180:183], v[98:101]
	s_setprio 0
	s_barrier
	s_or_b32 s54, s52, 0x80
	s_mov_b32 m0, s35
	ds_read_b128 v[184:187], v154 offset:49152
	ds_read_b128 v[188:191], v154 offset:50176
	ds_read_b128 v[192:195], v154 offset:51200
	ds_read_b128 v[196:199], v154 offset:52224
	buffer_load_dwordx4 v151, s[8:11], s54 offen lds
	s_mov_b32 m0, s36
	s_nop 0
	buffer_load_dwordx4 v153, s[8:11], s54 offen lds
	s_barrier
	s_setprio 1
	s_waitcnt lgkmcnt(3)
	v_mfma_f32_16x16x32_bf16 v[126:129], v[184:187], v[146:149], v[126:129]
	s_waitcnt lgkmcnt(1)
	v_mfma_f32_16x16x32_bf16 v[122:125], v[192:195], v[146:149], v[122:125]
	v_mfma_f32_16x16x32_bf16 v[118:121], v[184:187], v[160:163], v[118:121]
	v_mfma_f32_16x16x32_bf16 v[114:117], v[192:195], v[160:163], v[114:117]
	v_mfma_f32_16x16x32_bf16 v[92:95], v[184:187], v[168:171], v[92:95]
	v_mfma_f32_16x16x32_bf16 v[88:91], v[192:195], v[168:171], v[88:91]
	v_mfma_f32_16x16x32_bf16 v[84:87], v[184:187], v[176:179], v[84:87]
	v_mfma_f32_16x16x32_bf16 v[80:83], v[192:195], v[176:179], v[80:83]
	v_mfma_f32_16x16x32_bf16 v[126:129], v[188:191], v[156:159], v[126:129]
	s_waitcnt lgkmcnt(0)
	v_mfma_f32_16x16x32_bf16 v[122:125], v[196:199], v[156:159], v[122:125]
	v_mfma_f32_16x16x32_bf16 v[118:121], v[188:191], v[164:167], v[118:121]
	v_mfma_f32_16x16x32_bf16 v[114:117], v[196:199], v[164:167], v[114:117]
	v_mfma_f32_16x16x32_bf16 v[92:95], v[188:191], v[172:175], v[92:95]
	v_mfma_f32_16x16x32_bf16 v[88:91], v[196:199], v[172:175], v[88:91]
	v_mfma_f32_16x16x32_bf16 v[84:87], v[188:191], v[180:183], v[84:87]
	v_mfma_f32_16x16x32_bf16 v[80:83], v[196:199], v[180:183], v[80:83]
	s_setprio 0
	s_mov_b32 m0, s37
	s_barrier
	ds_read_b128 v[146:149], v155 offset:49152
	ds_read_b128 v[156:159], v155 offset:50176
	ds_read_b128 v[160:163], v155 offset:51200
	ds_read_b128 v[164:167], v155 offset:52224
	ds_read_b128 v[168:171], v155 offset:53248
	ds_read_b128 v[172:175], v155 offset:54272
	ds_read_b128 v[176:179], v155 offset:55296
	ds_read_b128 v[180:183], v155 offset:56320
	buffer_load_dwordx4 v150, s[72:75], s53 offen lds
	s_mov_b32 m0, s38
	s_nop 0
	buffer_load_dwordx4 v152, s[72:75], s53 offen lds
	s_barrier
	s_setprio 1
	s_waitcnt lgkmcnt(7)
	v_mfma_f32_16x16x32_bf16 v[60:63], v[64:67], v[146:149], v[60:63]
	v_mfma_f32_16x16x32_bf16 v[56:59], v[72:75], v[146:149], v[56:59]
	s_waitcnt lgkmcnt(5)
	v_mfma_f32_16x16x32_bf16 v[52:55], v[64:67], v[160:163], v[52:55]
	v_mfma_f32_16x16x32_bf16 v[48:51], v[72:75], v[160:163], v[48:51]
	s_waitcnt lgkmcnt(3)
	v_mfma_f32_16x16x32_bf16 v[28:31], v[64:67], v[168:171], v[28:31]
	v_mfma_f32_16x16x32_bf16 v[24:27], v[72:75], v[168:171], v[24:27]
	s_waitcnt lgkmcnt(1)
	v_mfma_f32_16x16x32_bf16 v[20:23], v[64:67], v[176:179], v[20:23]
	v_mfma_f32_16x16x32_bf16 v[16:19], v[72:75], v[176:179], v[16:19]
	v_mfma_f32_16x16x32_bf16 v[60:63], v[68:71], v[156:159], v[60:63]
	v_mfma_f32_16x16x32_bf16 v[56:59], v[76:79], v[156:159], v[56:59]
	v_mfma_f32_16x16x32_bf16 v[52:55], v[68:71], v[164:167], v[52:55]
	v_mfma_f32_16x16x32_bf16 v[48:51], v[76:79], v[164:167], v[48:51]
	v_mfma_f32_16x16x32_bf16 v[28:31], v[68:71], v[172:175], v[28:31]
	v_mfma_f32_16x16x32_bf16 v[24:27], v[76:79], v[172:175], v[24:27]
	s_waitcnt lgkmcnt(0)
	v_mfma_f32_16x16x32_bf16 v[20:23], v[68:71], v[180:183], v[20:23]
	v_mfma_f32_16x16x32_bf16 v[16:19], v[76:79], v[180:183], v[16:19]
	s_setprio 0
	s_barrier
	s_add_i32 s52, s52, 0x80080
	s_mov_b32 m0, s39
	s_nop 0
	buffer_load_dwordx4 v151, s[8:11], s52 offen lds
	s_mov_b32 m0, s40
	s_nop 0
	buffer_load_dwordx4 v153, s[8:11], s52 offen lds
	s_waitcnt vmcnt(6)
	s_barrier
	s_setprio 1
	v_mfma_f32_16x16x32_bf16 v[44:47], v[184:187], v[146:149], v[44:47]
	v_mfma_f32_16x16x32_bf16 v[40:43], v[192:195], v[146:149], v[40:43]
	v_mfma_f32_16x16x32_bf16 v[36:39], v[184:187], v[160:163], v[36:39]
	v_mfma_f32_16x16x32_bf16 v[32:35], v[192:195], v[160:163], v[32:35]
	v_mfma_f32_16x16x32_bf16 v[12:15], v[184:187], v[168:171], v[12:15]
	v_mfma_f32_16x16x32_bf16 v[8:11], v[192:195], v[168:171], v[8:11]
	v_mfma_f32_16x16x32_bf16 v[4:7], v[184:187], v[176:179], v[4:7]
	v_mfma_f32_16x16x32_bf16 v[0:3], v[192:195], v[176:179], v[0:3]
	v_mfma_f32_16x16x32_bf16 v[44:47], v[188:191], v[156:159], v[44:47]
	v_mfma_f32_16x16x32_bf16 v[40:43], v[196:199], v[156:159], v[40:43]
	v_mfma_f32_16x16x32_bf16 v[36:39], v[188:191], v[164:167], v[36:39]
	v_mfma_f32_16x16x32_bf16 v[32:35], v[196:199], v[164:167], v[32:35]
	v_mfma_f32_16x16x32_bf16 v[12:15], v[188:191], v[172:175], v[12:15]
	v_mfma_f32_16x16x32_bf16 v[8:11], v[196:199], v[172:175], v[8:11]
	v_mfma_f32_16x16x32_bf16 v[4:7], v[188:191], v[180:183], v[4:7]
	v_mfma_f32_16x16x32_bf16 v[0:3], v[196:199], v[180:183], v[0:3]
	s_setprio 0
	s_add_i32 s51, s51, 2
	s_addk_i32 s49, 0x100
	s_addk_i32 s50, 0x100
	s_cmp_gt_u32 s51, 29
	s_barrier
	s_cbranch_scc0 .LBB0_1514
	s_getreg_b32 s10, hwreg(HW_REG_HW_ID, 0, 6)
	s_and_b32 s10, s10, 63
	s_lshl_b32 s10, s10, 2
	s_add_i32 s10, s10, 0
	s_add_i32 s10, s10, 0x20010
	v_mov_b32_e32 v64, s10
	ds_read_b32 v64, v64
	v_mbcnt_lo_u32_b32 v148, -1, 0
	v_mbcnt_hi_u32_b32 v148, -1, v148
	s_mov_b32 s50, s17
	v_lshrrev_b32_e32 v66, 1, v148
	v_and_b32_e32 v156, 24, v66
	s_waitcnt lgkmcnt(0)
	v_readfirstlane_b32 s10, v64
	s_nop 1
	v_lshl_or_b32 v146, s10, 6, v148
	s_lshl_b32 s10, s2, 8
	s_min_i32 s2, s46, 64
	s_ashr_i32 s2, s2, 3
	s_mul_hi_i32 s11, s2, 0xc000
	s_mul_i32 s2, s2, 0xc000
	s_add_u32 s2, s0, s2
	s_addc_u32 s47, s24, s11
	s_ashr_i32 s11, s10, 31
	s_lshl_b64 s[48:49], s[10:11], 2
	v_lshrrev_b32_e32 v64, 1, v146
	s_add_u32 s48, s2, s48
	v_and_b32_e32 v149, 0x60, v64
	s_addc_u32 s49, s47, s49
	v_lshlrev_b32_e32 v96, 2, v149
	v_lshl_add_u64 v[64:65], s[48:49], 0, v[96:97]
	v_lshlrev_b32_e32 v96, 2, v156
	v_lshl_add_u64 v[68:69], v[64:65], 0, v[96:97]
	v_ashrrev_i32_e32 v96, 2, v146
	s_lshl_b32 s48, s46, 8
	v_and_b32_e32 v146, 0xffffffc0, v96
	s_ashr_i32 s49, s48, 31
	v_ashrrev_i32_e32 v147, 31, v146
	v_lshl_add_u64 v[146:147], v[146:147], 0, s[48:49]
	v_and_or_b32 v146, v148, 15, v146
	s_cmp_gt_i32 s46, 63
	v_lshlrev_b64 v[146:147], 11, v[146:147]
	v_lshl_add_u64 v[146:147], v[146:147], 0, s[10:11]
	s_cselect_b32 s2, s44, s21
	s_cselect_b32 s10, s43, s20
	v_or3_b32 v146, v146, v149, v156
	v_mov_b32_e32 v148, s10
	v_mov_b32_e32 v149, s2
	v_lshl_add_u64 v[148:149], v[146:147], 2, v[148:149]
	global_load_dwordx4 v[72:75], v[68:69], off offset:16
	global_load_dwordx4 v[76:79], v[68:69], off
	global_load_dwordx4 v[64:67], v[68:69], off offset:528
	s_nop 0
	global_load_dwordx4 v[68:71], v[68:69], off offset:512
	s_nop 0
	global_load_dwordx4 v[156:159], v[148:149], off offset:16
	global_load_dwordx4 v[160:163], v[148:149], off
	global_load_dwordx4 v[164:167], v[148:149], off offset:528
	global_load_dwordx4 v[168:171], v[148:149], off offset:512
	s_mov_b64 s[10:11], 0x20000
	v_add_co_u32_e32 v180, vcc, s75, v148
	v_lshl_add_u64 v[176:177], v[148:149], 0, s[10:11]
	s_nop 0
	v_addc_co_u32_e32 v181, vcc, 0, v149, vcc
	global_load_dwordx4 v[172:175], v[180:181], off
	s_nop 0
	global_load_dwordx4 v[176:179], v[176:177], off offset:16
	s_mov_b64 s[10:11], 0x20200
	v_lshl_add_u64 v[184:185], v[148:149], 0, s[10:11]
	global_load_dwordx4 v[180:183], v[180:181], off offset:512
	s_nop 0
	global_load_dwordx4 v[184:187], v[184:185], off offset:16
	v_lshl_add_u64 v[146:147], v[146:147], 1, s[12:13]
	s_mov_b32 s2, 0x10000
	s_mov_b64 s[10:11], 0x40000
	s_mov_b32 s46, s15
	s_mov_b32 s49, s16
	s_waitcnt vmcnt(7)
	v_pk_fma_f32 v[158:159], v[140:141], v[74:75], v[158:159]
	s_waitcnt vmcnt(6)
	v_pk_fma_f32 v[144:145], v[144:145], v[78:79], v[162:163]
	v_pk_fma_f32 v[142:143], v[142:143], v[76:77], v[160:161]
	v_pk_fma_f32 v[140:141], v[138:139], v[72:73], v[156:157]
	v_cvt_pk_bf16_f32 v138, v142, v143
	v_cvt_pk_bf16_f32 v139, v144, v145
	v_cvt_pk_bf16_f32 v140, v140, v141
	v_cvt_pk_bf16_f32 v141, v158, v159
	global_store_dwordx4 v[146:147], v[138:141], off
	s_waitcnt vmcnt(5)
	v_pk_fma_f32 v[128:129], v[128:129], v[70:71], v[170:171]
	v_pk_fma_f32 v[126:127], v[126:127], v[68:69], v[168:169]
	v_pk_fma_f32 v[138:139], v[124:125], v[66:67], v[166:167]
	v_pk_fma_f32 v[124:125], v[122:123], v[64:65], v[164:165]
	v_cvt_pk_bf16_f32 v122, v126, v127
	v_cvt_pk_bf16_f32 v123, v128, v129
	v_cvt_pk_bf16_f32 v124, v124, v125
	v_cvt_pk_bf16_f32 v125, v138, v139
	global_store_dwordx4 v[146:147], v[122:125], off offset:256
	s_waitcnt vmcnt(4)
	v_pk_fma_f32 v[126:127], v[132:133], v[74:75], v[178:179]
	v_pk_fma_f32 v[128:129], v[130:131], v[72:73], v[176:177]
	v_pk_fma_f32 v[124:125], v[136:137], v[78:79], v[174:175]
	v_pk_fma_f32 v[122:123], v[134:135], v[76:77], v[172:173]
	s_waitcnt vmcnt(3)
	v_pk_fma_f32 v[120:121], v[120:121], v[70:71], v[182:183]
	v_cvt_pk_bf16_f32 v122, v122, v123
	v_cvt_pk_bf16_f32 v123, v124, v125
	v_cvt_pk_bf16_f32 v125, v126, v127
	v_add_co_u32_e32 v126, vcc, s2, v146
	v_cvt_pk_bf16_f32 v124, v128, v129
	s_nop 0
	v_addc_co_u32_e32 v127, vcc, 0, v147, vcc
	global_store_dwordx4 v[126:127], v[122:125], off
	v_pk_fma_f32 v[118:119], v[118:119], v[68:69], v[180:181]
	s_mov_b32 s2, 0x40000
	s_waitcnt vmcnt(3)
	v_pk_fma_f32 v[122:123], v[116:117], v[66:67], v[186:187]
	v_pk_fma_f32 v[116:117], v[114:115], v[64:65], v[184:185]
	v_cvt_pk_bf16_f32 v114, v118, v119
	v_cvt_pk_bf16_f32 v115, v120, v121
	v_cvt_pk_bf16_f32 v116, v116, v117
	v_cvt_pk_bf16_f32 v117, v122, v123
	v_add_co_u32_e32 v122, vcc, s2, v148
	global_store_dwordx4 v[126:127], v[114:117], off offset:256
	v_lshl_add_u64 v[118:119], v[148:149], 0, s[10:11]
	v_addc_co_u32_e32 v123, vcc, 0, v149, vcc
	global_load_dwordx4 v[114:117], v[122:123], off
	s_nop 0
	global_load_dwordx4 v[118:121], v[118:119], off offset:16
	s_mov_b64 s[10:11], 0x40200
	v_lshl_add_u64 v[126:127], v[148:149], 0, s[10:11]
	s_mov_b32 s2, 0x60000
	global_load_dwordx4 v[122:125], v[122:123], off offset:512
	s_nop 0
	global_load_dwordx4 v[126:129], v[126:127], off offset:16
	s_mov_b64 s[10:11], 0x60000
	v_add_co_u32_e32 v138, vcc, s2, v148
	v_lshl_add_u64 v[134:135], v[148:149], 0, s[10:11]
	s_nop 0
	v_addc_co_u32_e32 v139, vcc, 0, v149, vcc
	global_load_dwordx4 v[130:133], v[138:139], off
	s_nop 0
	global_load_dwordx4 v[134:137], v[134:135], off offset:16
	s_mov_b64 s[10:11], 0x60200
	v_lshl_add_u64 v[142:143], v[148:149], 0, s[10:11]
	global_load_dwordx4 v[138:141], v[138:139], off offset:512
	s_nop 0
	global_load_dwordx4 v[142:145], v[142:143], off offset:16
	s_mov_b32 s2, 0x30000
	s_mov_b64 s[10:11], 0x100000
	s_waitcnt vmcnt(7)
	v_pk_fma_f32 v[110:111], v[110:111], v[76:77], v[114:115]
	v_pk_fma_f32 v[112:113], v[112:113], v[78:79], v[116:117]
	s_waitcnt vmcnt(6)
	v_pk_fma_f32 v[114:115], v[108:109], v[74:75], v[120:121]
	v_pk_fma_f32 v[108:109], v[106:107], v[72:73], v[118:119]
	v_cvt_pk_bf16_f32 v106, v110, v111
	v_add_co_u32_e32 v110, vcc, s75, v146
	v_cvt_pk_bf16_f32 v107, v112, v113
	v_cvt_pk_bf16_f32 v108, v108, v109
	v_cvt_pk_bf16_f32 v109, v114, v115
	v_addc_co_u32_e32 v111, vcc, 0, v147, vcc
	global_store_dwordx4 v[110:111], v[106:109], off
	s_waitcnt vmcnt(6)
	v_pk_fma_f32 v[94:95], v[94:95], v[70:71], v[124:125]
	v_pk_fma_f32 v[92:93], v[92:93], v[68:69], v[122:123]
	s_waitcnt vmcnt(5)
	v_pk_fma_f32 v[106:107], v[90:91], v[66:67], v[128:129]
	v_pk_fma_f32 v[90:91], v[88:89], v[64:65], v[126:127]
	v_cvt_pk_bf16_f32 v88, v92, v93
	v_cvt_pk_bf16_f32 v89, v94, v95
	v_cvt_pk_bf16_f32 v90, v90, v91
	v_cvt_pk_bf16_f32 v91, v106, v107
	global_store_dwordx4 v[110:111], v[88:91], off offset:256
	s_waitcnt vmcnt(4)
	v_pk_fma_f32 v[92:93], v[100:101], v[74:75], v[136:137]
	v_pk_fma_f32 v[94:95], v[98:99], v[72:73], v[134:135]
	v_pk_fma_f32 v[90:91], v[104:105], v[78:79], v[132:133]
	v_pk_fma_f32 v[88:89], v[102:103], v[76:77], v[130:131]
	s_waitcnt vmcnt(3)
	v_pk_fma_f32 v[86:87], v[86:87], v[70:71], v[140:141]
	v_cvt_pk_bf16_f32 v88, v88, v89
	v_cvt_pk_bf16_f32 v89, v90, v91
	v_cvt_pk_bf16_f32 v91, v92, v93
	v_add_co_u32_e32 v92, vcc, s2, v146
	v_cvt_pk_bf16_f32 v90, v94, v95
	s_nop 0
	v_addc_co_u32_e32 v93, vcc, 0, v147, vcc
	global_store_dwordx4 v[92:93], v[88:91], off
	v_pk_fma_f32 v[84:85], v[84:85], v[68:69], v[138:139]
	s_mov_b32 s2, 0x100000
	s_waitcnt vmcnt(3)
	v_pk_fma_f32 v[88:89], v[82:83], v[66:67], v[144:145]
	v_pk_fma_f32 v[82:83], v[80:81], v[64:65], v[142:143]
	v_cvt_pk_bf16_f32 v80, v84, v85
	v_cvt_pk_bf16_f32 v81, v86, v87
	v_cvt_pk_bf16_f32 v82, v82, v83
	v_cvt_pk_bf16_f32 v83, v88, v89
	v_add_co_u32_e32 v88, vcc, s2, v148
	global_store_dwordx4 v[92:93], v[80:83], off offset:256
	s_nop 0
	v_addc_co_u32_e32 v89, vcc, 0, v149, vcc
	v_lshl_add_u64 v[80:81], v[148:149], 0, s[10:11]
	global_load_dwordx4 v[84:87], v[88:89], off
	s_nop 0
	global_load_dwordx4 v[80:83], v[80:81], off offset:16
	s_mov_b64 s[10:11], 0x100200
	v_lshl_add_u64 v[92:93], v[148:149], 0, s[10:11]
	s_mov_b32 s2, 0x120000
	global_load_dwordx4 v[88:91], v[88:89], off offset:512
	s_nop 0
	global_load_dwordx4 v[92:95], v[92:93], off offset:16
	s_mov_b64 s[10:11], 0x120000
	v_add_co_u32_e32 v106, vcc, s2, v148
	v_lshl_add_u64 v[102:103], v[148:149], 0, s[10:11]
	s_nop 0
	v_addc_co_u32_e32 v107, vcc, 0, v149, vcc
	global_load_dwordx4 v[98:101], v[106:107], off
	s_nop 0
	global_load_dwordx4 v[102:105], v[102:103], off offset:16
	s_mov_b64 s[10:11], 0x120200
	v_lshl_add_u64 v[110:111], v[148:149], 0, s[10:11]
	global_load_dwordx4 v[106:109], v[106:107], off offset:512
	s_nop 0
	global_load_dwordx4 v[110:113], v[110:111], off offset:16
	s_mov_b32 s2, 0x80000
	s_mov_b64 s[10:11], 0x140000
	s_waitcnt vmcnt(7)
	v_pk_fma_f32 v[60:61], v[60:61], v[76:77], v[84:85]
	v_pk_fma_f32 v[62:63], v[62:63], v[78:79], v[86:87]
	s_waitcnt vmcnt(6)
	v_pk_fma_f32 v[82:83], v[58:59], v[74:75], v[82:83]
	v_pk_fma_f32 v[58:59], v[56:57], v[72:73], v[80:81]
	v_cvt_pk_bf16_f32 v56, v60, v61
	v_add_co_u32_e32 v60, vcc, s2, v146
	v_cvt_pk_bf16_f32 v57, v62, v63
	v_cvt_pk_bf16_f32 v58, v58, v59
	v_cvt_pk_bf16_f32 v59, v82, v83
	v_addc_co_u32_e32 v61, vcc, 0, v147, vcc
	global_store_dwordx4 v[60:61], v[56:59], off
	s_waitcnt vmcnt(6)
	v_pk_fma_f32 v[46:47], v[46:47], v[70:71], v[90:91]
	v_pk_fma_f32 v[44:45], v[44:45], v[68:69], v[88:89]
	s_waitcnt vmcnt(5)
	v_pk_fma_f32 v[56:57], v[42:43], v[66:67], v[94:95]
	v_pk_fma_f32 v[42:43], v[40:41], v[64:65], v[92:93]
	v_cvt_pk_bf16_f32 v40, v44, v45
	v_cvt_pk_bf16_f32 v41, v46, v47
	v_cvt_pk_bf16_f32 v42, v42, v43
	v_cvt_pk_bf16_f32 v43, v56, v57
	global_store_dwordx4 v[60:61], v[40:43], off offset:256
	s_waitcnt vmcnt(4)
	v_pk_fma_f32 v[44:45], v[50:51], v[74:75], v[104:105]
	s_mov_b32 s2, 0x90000
	v_pk_fma_f32 v[42:43], v[54:55], v[78:79], v[100:101]
	v_pk_fma_f32 v[40:41], v[52:53], v[76:77], v[98:99]
	v_pk_fma_f32 v[46:47], v[48:49], v[72:73], v[102:103]
	v_cvt_pk_bf16_f32 v40, v40, v41
	v_cvt_pk_bf16_f32 v41, v42, v43
	v_cvt_pk_bf16_f32 v43, v44, v45
	v_add_co_u32_e32 v44, vcc, s2, v146
	v_cvt_pk_bf16_f32 v42, v46, v47
	s_nop 0
	v_addc_co_u32_e32 v45, vcc, 0, v147, vcc
	global_store_dwordx4 v[44:45], v[40:43], off
	s_waitcnt vmcnt(4)
	v_pk_fma_f32 v[38:39], v[38:39], v[70:71], v[108:109]
	v_pk_fma_f32 v[36:37], v[36:37], v[68:69], v[106:107]
	s_waitcnt vmcnt(3)
	v_pk_fma_f32 v[40:41], v[34:35], v[66:67], v[112:113]
	v_pk_fma_f32 v[34:35], v[32:33], v[64:65], v[110:111]
	s_mov_b32 s2, 0x140000
	v_cvt_pk_bf16_f32 v32, v36, v37
	v_cvt_pk_bf16_f32 v33, v38, v39
	v_cvt_pk_bf16_f32 v34, v34, v35
	v_cvt_pk_bf16_f32 v35, v40, v41
	v_add_co_u32_e32 v40, vcc, s2, v148
	global_store_dwordx4 v[44:45], v[32:35], off offset:256
	v_lshl_add_u64 v[36:37], v[148:149], 0, s[10:11]
	v_addc_co_u32_e32 v41, vcc, 0, v149, vcc
	global_load_dwordx4 v[32:35], v[40:41], off
	s_nop 0
	global_load_dwordx4 v[36:39], v[36:37], off offset:16
	s_mov_b64 s[10:11], 0x140200
	v_lshl_add_u64 v[44:45], v[148:149], 0, s[10:11]
	s_mov_b32 s2, 0x160000
	global_load_dwordx4 v[40:43], v[40:41], off offset:512
	s_nop 0
	global_load_dwordx4 v[44:47], v[44:45], off offset:16
	s_mov_b64 s[10:11], 0x160000
	v_add_co_u32_e32 v56, vcc, s2, v148
	v_lshl_add_u64 v[52:53], v[148:149], 0, s[10:11]
	s_nop 0
	v_addc_co_u32_e32 v57, vcc, 0, v149, vcc
	global_load_dwordx4 v[48:51], v[56:57], off
	s_nop 0
	global_load_dwordx4 v[52:55], v[52:53], off offset:16
	s_mov_b64 s[10:11], 0x160200
	v_lshl_add_u64 v[60:61], v[148:149], 0, s[10:11]
	global_load_dwordx4 v[56:59], v[56:57], off offset:512
	s_nop 0
	global_load_dwordx4 v[60:63], v[60:61], off offset:16
	s_mov_b32 s2, 0xa0000
	s_waitcnt vmcnt(7)
	v_pk_fma_f32 v[28:29], v[28:29], v[76:77], v[32:33]
	v_pk_fma_f32 v[30:31], v[30:31], v[78:79], v[34:35]
	s_waitcnt vmcnt(6)
	v_pk_fma_f32 v[32:33], v[26:27], v[74:75], v[38:39]
	v_pk_fma_f32 v[26:27], v[24:25], v[72:73], v[36:37]
	v_cvt_pk_bf16_f32 v24, v28, v29
	v_add_co_u32_e32 v28, vcc, s2, v146
	v_cvt_pk_bf16_f32 v25, v30, v31
	v_cvt_pk_bf16_f32 v26, v26, v27
	v_cvt_pk_bf16_f32 v27, v32, v33
	v_addc_co_u32_e32 v29, vcc, 0, v147, vcc
	global_store_dwordx4 v[28:29], v[24:27], off
	s_waitcnt vmcnt(6)
	v_pk_fma_f32 v[14:15], v[14:15], v[70:71], v[42:43]
	v_pk_fma_f32 v[12:13], v[12:13], v[68:69], v[40:41]
	s_waitcnt vmcnt(5)
	v_pk_fma_f32 v[24:25], v[10:11], v[66:67], v[46:47]
	v_pk_fma_f32 v[10:11], v[8:9], v[64:65], v[44:45]
	v_cvt_pk_bf16_f32 v8, v12, v13
	v_cvt_pk_bf16_f32 v9, v14, v15
	v_cvt_pk_bf16_f32 v10, v10, v11
	v_cvt_pk_bf16_f32 v11, v24, v25
	global_store_dwordx4 v[28:29], v[8:11], off offset:256
	s_waitcnt vmcnt(4)
	v_pk_fma_f32 v[12:13], v[18:19], v[74:75], v[54:55]
	s_mov_b32 s2, 0xb0000
	v_pk_fma_f32 v[10:11], v[22:23], v[78:79], v[50:51]
	v_pk_fma_f32 v[8:9], v[20:21], v[76:77], v[48:49]
	v_pk_fma_f32 v[14:15], v[16:17], v[72:73], v[52:53]
	v_cvt_pk_bf16_f32 v8, v8, v9
	v_cvt_pk_bf16_f32 v9, v10, v11
	v_cvt_pk_bf16_f32 v11, v12, v13
	v_add_co_u32_e32 v12, vcc, s2, v146
	v_cvt_pk_bf16_f32 v10, v14, v15
	s_nop 0
	v_addc_co_u32_e32 v13, vcc, 0, v147, vcc
	global_store_dwordx4 v[12:13], v[8:11], off
	s_waitcnt vmcnt(4)
	v_pk_fma_f32 v[6:7], v[6:7], v[70:71], v[58:59]
	v_pk_fma_f32 v[4:5], v[4:5], v[68:69], v[56:57]
	s_waitcnt vmcnt(3)
	v_pk_fma_f32 v[8:9], v[2:3], v[66:67], v[62:63]
	v_pk_fma_f32 v[2:3], v[0:1], v[64:65], v[60:61]
	v_cvt_pk_bf16_f32 v0, v4, v5
	v_cvt_pk_bf16_f32 v1, v6, v7
	v_cvt_pk_bf16_f32 v2, v2, v3
	v_cvt_pk_bf16_f32 v3, v8, v9
	s_and_b64 vcc, exec, s[4:5]
	s_mov_b32 s2, s14
	global_store_dwordx4 v[12:13], v[0:3], off offset:256
	s_cbranch_vccz .LBB0_1508
	s_branch .LBB0_1517

.LBB0_1639:
	ds_read_b128 v[134:137], v132
	ds_read_b128 v[138:141], v132 offset:1024
	ds_read_b128 v[142:145], v132 offset:2048
	ds_read_b128 v[146:149], v132 offset:3072
	s_add_i32 s10, s41, 0xfff80080
	s_cmp_eq_u32 s43, 28
	s_cselect_b32 s46, s39, s10
	s_cselect_b32 s44, s40, s42
	s_or_b32 s45, s46, 0x80
	s_mov_b32 m0, s35
	ds_read_b128 v[150:153], v133
	ds_read_b128 v[154:157], v133 offset:1024
	ds_read_b128 v[158:161], v133 offset:2048
	ds_read_b128 v[162:165], v133 offset:3072
	ds_read_b128 v[166:169], v133 offset:4096
	ds_read_b128 v[170:173], v133 offset:5120
	ds_read_b128 v[174:177], v133 offset:6144
	ds_read_b128 v[178:181], v133 offset:7168
	buffer_load_dwordx4 v130, s[72:75], s41 offen lds
	s_mov_b32 m0, s36
	s_nop 0
	buffer_load_dwordx4 v131, s[72:75], s41 offen lds
	s_waitcnt lgkmcnt(8)
	s_barrier
	s_setprio 1
	s_waitcnt lgkmcnt(7)
	v_mfma_f32_16x16x32_bf16 v[126:129], v[150:153], v[134:137], v[126:129]
	v_mfma_f32_16x16x32_bf16 v[114:117], v[150:153], v[142:145], v[114:117]
	s_waitcnt lgkmcnt(5)
	v_mfma_f32_16x16x32_bf16 v[122:125], v[158:161], v[134:137], v[122:125]
	v_mfma_f32_16x16x32_bf16 v[106:109], v[158:161], v[142:145], v[106:109]
	s_waitcnt lgkmcnt(3)
	v_mfma_f32_16x16x32_bf16 v[118:121], v[166:169], v[134:137], v[118:121]
	v_mfma_f32_16x16x32_bf16 v[102:105], v[166:169], v[142:145], v[102:105]
	s_waitcnt lgkmcnt(1)
	v_mfma_f32_16x16x32_bf16 v[110:113], v[174:177], v[134:137], v[110:113]
	v_mfma_f32_16x16x32_bf16 v[98:101], v[174:177], v[142:145], v[98:101]
	v_mfma_f32_16x16x32_bf16 v[126:129], v[154:157], v[138:141], v[126:129]
	v_mfma_f32_16x16x32_bf16 v[114:117], v[154:157], v[146:149], v[114:117]
	v_mfma_f32_16x16x32_bf16 v[122:125], v[162:165], v[138:141], v[122:125]
	v_mfma_f32_16x16x32_bf16 v[106:109], v[162:165], v[146:149], v[106:109]
	v_mfma_f32_16x16x32_bf16 v[118:121], v[170:173], v[138:141], v[118:121]
	v_mfma_f32_16x16x32_bf16 v[102:105], v[170:173], v[146:149], v[102:105]
	s_waitcnt lgkmcnt(0)
	v_mfma_f32_16x16x32_bf16 v[110:113], v[178:181], v[138:141], v[110:113]
	v_mfma_f32_16x16x32_bf16 v[98:101], v[178:181], v[146:149], v[98:101]
	s_setprio 0
	s_barrier
	s_mov_b32 s10, s74
	s_mov_b32 s11, s75
	s_mov_b32 m0, s19
	ds_read_b128 v[182:185], v132 offset:16384
	ds_read_b128 v[186:189], v132 offset:17408
	ds_read_b128 v[190:193], v132 offset:18432
	ds_read_b128 v[194:197], v132 offset:19456
	buffer_load_dwordx4 v130, s[8:11], s44 offen lds
	s_mov_b32 m0, s20
	s_nop 0
	buffer_load_dwordx4 v131, s[8:11], s44 offen lds
	s_barrier
	s_setprio 1
	s_waitcnt lgkmcnt(3)
	v_mfma_f32_16x16x32_bf16 v[92:95], v[150:153], v[182:185], v[92:95]
	s_waitcnt lgkmcnt(1)
	v_mfma_f32_16x16x32_bf16 v[64:67], v[150:153], v[190:193], v[64:67]
	v_mfma_f32_16x16x32_bf16 v[84:87], v[158:161], v[182:185], v[84:87]
	v_mfma_f32_16x16x32_bf16 v[48:51], v[158:161], v[190:193], v[48:51]
	v_mfma_f32_16x16x32_bf16 v[76:79], v[166:169], v[182:185], v[76:79]
	v_mfma_f32_16x16x32_bf16 v[40:43], v[166:169], v[190:193], v[40:43]
	v_mfma_f32_16x16x32_bf16 v[60:63], v[174:177], v[182:185], v[60:63]
	v_mfma_f32_16x16x32_bf16 v[32:35], v[174:177], v[190:193], v[32:35]
	v_mfma_f32_16x16x32_bf16 v[92:95], v[154:157], v[186:189], v[92:95]
	s_waitcnt lgkmcnt(0)
	v_mfma_f32_16x16x32_bf16 v[64:67], v[154:157], v[194:197], v[64:67]
	v_mfma_f32_16x16x32_bf16 v[84:87], v[162:165], v[186:189], v[84:87]
	v_mfma_f32_16x16x32_bf16 v[48:51], v[162:165], v[194:197], v[48:51]
	v_mfma_f32_16x16x32_bf16 v[76:79], v[170:173], v[186:189], v[76:79]
	v_mfma_f32_16x16x32_bf16 v[40:43], v[170:173], v[194:197], v[40:43]
	v_mfma_f32_16x16x32_bf16 v[60:63], v[178:181], v[186:189], v[60:63]
	v_mfma_f32_16x16x32_bf16 v[32:35], v[178:181], v[194:197], v[32:35]
	s_setprio 0
	s_mov_b32 m0, s2
	s_barrier
	ds_read_b128 v[150:153], v133 offset:16384
	ds_read_b128 v[154:157], v133 offset:17408
	ds_read_b128 v[158:161], v133 offset:18432
	ds_read_b128 v[162:165], v133 offset:19456
	ds_read_b128 v[166:169], v133 offset:20480
	ds_read_b128 v[170:173], v133 offset:21504
	ds_read_b128 v[174:177], v133 offset:22528
	ds_read_b128 v[178:181], v133 offset:23552
	buffer_load_dwordx4 v130, s[72:75], s46 offen lds
	s_mov_b32 m0, s21
	s_nop 0
	buffer_load_dwordx4 v131, s[72:75], s46 offen lds
	s_barrier
	s_setprio 1
	s_waitcnt lgkmcnt(7)
	v_mfma_f32_16x16x32_bf16 v[88:91], v[150:153], v[134:137], v[88:91]
	v_mfma_f32_16x16x32_bf16 v[72:75], v[150:153], v[142:145], v[72:75]
	s_waitcnt lgkmcnt(5)
	v_mfma_f32_16x16x32_bf16 v[80:83], v[158:161], v[134:137], v[80:83]
	v_mfma_f32_16x16x32_bf16 v[56:59], v[158:161], v[142:145], v[56:59]
	s_waitcnt lgkmcnt(3)
	v_mfma_f32_16x16x32_bf16 v[68:71], v[166:169], v[134:137], v[68:71]
	v_mfma_f32_16x16x32_bf16 v[44:47], v[166:169], v[142:145], v[44:47]
	s_waitcnt lgkmcnt(1)
	v_mfma_f32_16x16x32_bf16 v[52:55], v[174:177], v[134:137], v[52:55]
	v_mfma_f32_16x16x32_bf16 v[36:39], v[174:177], v[142:145], v[36:39]
	v_mfma_f32_16x16x32_bf16 v[88:91], v[154:157], v[138:141], v[88:91]
	v_mfma_f32_16x16x32_bf16 v[72:75], v[154:157], v[146:149], v[72:75]
	v_mfma_f32_16x16x32_bf16 v[80:83], v[162:165], v[138:141], v[80:83]
	v_mfma_f32_16x16x32_bf16 v[56:59], v[162:165], v[146:149], v[56:59]
	v_mfma_f32_16x16x32_bf16 v[68:71], v[170:173], v[138:141], v[68:71]
	v_mfma_f32_16x16x32_bf16 v[44:47], v[170:173], v[146:149], v[44:47]
	s_waitcnt lgkmcnt(0)
	v_mfma_f32_16x16x32_bf16 v[52:55], v[178:181], v[138:141], v[52:55]
	v_mfma_f32_16x16x32_bf16 v[36:39], v[178:181], v[146:149], v[36:39]
	s_setprio 0
	s_barrier
	s_add_i32 s47, s44, 0x80000
	s_mov_b32 m0, s22
	s_nop 0
	buffer_load_dwordx4 v130, s[8:11], s47 offen lds
	s_mov_b32 m0, s23
	s_nop 0
	buffer_load_dwordx4 v131, s[8:11], s47 offen lds
	s_waitcnt vmcnt(6)
	s_barrier
	s_setprio 1
	v_mfma_f32_16x16x32_bf16 v[28:31], v[150:153], v[182:185], v[28:31]
	v_mfma_f32_16x16x32_bf16 v[16:19], v[150:153], v[190:193], v[16:19]
	v_mfma_f32_16x16x32_bf16 v[24:27], v[158:161], v[182:185], v[24:27]
	v_mfma_f32_16x16x32_bf16 v[8:11], v[158:161], v[190:193], v[8:11]
	v_mfma_f32_16x16x32_bf16 v[20:23], v[166:169], v[182:185], v[20:23]
	v_mfma_f32_16x16x32_bf16 v[4:7], v[166:169], v[190:193], v[4:7]
	v_mfma_f32_16x16x32_bf16 v[12:15], v[174:177], v[182:185], v[12:15]
	v_mfma_f32_16x16x32_bf16 v[0:3], v[174:177], v[190:193], v[0:3]
	v_mfma_f32_16x16x32_bf16 v[28:31], v[154:157], v[186:189], v[28:31]
	v_mfma_f32_16x16x32_bf16 v[16:19], v[154:157], v[194:197], v[16:19]
	v_mfma_f32_16x16x32_bf16 v[24:27], v[162:165], v[186:189], v[24:27]
	v_mfma_f32_16x16x32_bf16 v[8:11], v[162:165], v[194:197], v[8:11]
	v_mfma_f32_16x16x32_bf16 v[20:23], v[170:173], v[186:189], v[20:23]
	v_mfma_f32_16x16x32_bf16 v[4:7], v[170:173], v[194:197], v[4:7]
	v_mfma_f32_16x16x32_bf16 v[12:15], v[178:181], v[186:189], v[12:15]
	v_mfma_f32_16x16x32_bf16 v[0:3], v[178:181], v[194:197], v[0:3]
	s_setprio 0
	s_barrier
	ds_read_b128 v[134:137], v132 offset:32768
	ds_read_b128 v[138:141], v132 offset:33792
	ds_read_b128 v[142:145], v132 offset:34816
	ds_read_b128 v[146:149], v132 offset:35840
	s_add_i32 s46, s46, 0x80000
	s_mov_b32 m0, s24
	ds_read_b128 v[150:153], v133 offset:32768
	ds_read_b128 v[154:157], v133 offset:33792
	ds_read_b128 v[158:161], v133 offset:34816
	ds_read_b128 v[162:165], v133 offset:35840
	ds_read_b128 v[166:169], v133 offset:36864
	ds_read_b128 v[170:173], v133 offset:37888
	ds_read_b128 v[174:177], v133 offset:38912
	ds_read_b128 v[178:181], v133 offset:39936
	buffer_load_dwordx4 v130, s[72:75], s46 offen lds
	s_mov_b32 m0, s25
	s_nop 0
	buffer_load_dwordx4 v131, s[72:75], s46 offen lds
	s_waitcnt lgkmcnt(8)
	s_barrier
	s_setprio 1
	s_waitcnt lgkmcnt(7)
	v_mfma_f32_16x16x32_bf16 v[126:129], v[150:153], v[134:137], v[126:129]
	v_mfma_f32_16x16x32_bf16 v[114:117], v[150:153], v[142:145], v[114:117]
	s_waitcnt lgkmcnt(5)
	v_mfma_f32_16x16x32_bf16 v[122:125], v[158:161], v[134:137], v[122:125]
	v_mfma_f32_16x16x32_bf16 v[106:109], v[158:161], v[142:145], v[106:109]
	s_waitcnt lgkmcnt(3)
	v_mfma_f32_16x16x32_bf16 v[118:121], v[166:169], v[134:137], v[118:121]
	v_mfma_f32_16x16x32_bf16 v[102:105], v[166:169], v[142:145], v[102:105]
	s_waitcnt lgkmcnt(1)
	v_mfma_f32_16x16x32_bf16 v[110:113], v[174:177], v[134:137], v[110:113]
	v_mfma_f32_16x16x32_bf16 v[98:101], v[174:177], v[142:145], v[98:101]
	v_mfma_f32_16x16x32_bf16 v[126:129], v[154:157], v[138:141], v[126:129]
	v_mfma_f32_16x16x32_bf16 v[114:117], v[154:157], v[146:149], v[114:117]
	v_mfma_f32_16x16x32_bf16 v[122:125], v[162:165], v[138:141], v[122:125]
	v_mfma_f32_16x16x32_bf16 v[106:109], v[162:165], v[146:149], v[106:109]
	v_mfma_f32_16x16x32_bf16 v[118:121], v[170:173], v[138:141], v[118:121]
	v_mfma_f32_16x16x32_bf16 v[102:105], v[170:173], v[146:149], v[102:105]
	s_waitcnt lgkmcnt(0)
	v_mfma_f32_16x16x32_bf16 v[110:113], v[178:181], v[138:141], v[110:113]
	v_mfma_f32_16x16x32_bf16 v[98:101], v[178:181], v[146:149], v[98:101]
	s_setprio 0
	s_barrier
	s_or_b32 s46, s44, 0x80
	s_mov_b32 m0, s26
	ds_read_b128 v[182:185], v132 offset:49152
	ds_read_b128 v[186:189], v132 offset:50176
	ds_read_b128 v[190:193], v132 offset:51200
	ds_read_b128 v[194:197], v132 offset:52224
	buffer_load_dwordx4 v130, s[8:11], s46 offen lds
	s_mov_b32 m0, s27
	s_nop 0
	buffer_load_dwordx4 v131, s[8:11], s46 offen lds
	s_barrier
	s_setprio 1
	s_waitcnt lgkmcnt(3)
	v_mfma_f32_16x16x32_bf16 v[92:95], v[150:153], v[182:185], v[92:95]
	s_waitcnt lgkmcnt(1)
	v_mfma_f32_16x16x32_bf16 v[64:67], v[150:153], v[190:193], v[64:67]
	v_mfma_f32_16x16x32_bf16 v[84:87], v[158:161], v[182:185], v[84:87]
	v_mfma_f32_16x16x32_bf16 v[48:51], v[158:161], v[190:193], v[48:51]
	v_mfma_f32_16x16x32_bf16 v[76:79], v[166:169], v[182:185], v[76:79]
	v_mfma_f32_16x16x32_bf16 v[40:43], v[166:169], v[190:193], v[40:43]
	v_mfma_f32_16x16x32_bf16 v[60:63], v[174:177], v[182:185], v[60:63]
	v_mfma_f32_16x16x32_bf16 v[32:35], v[174:177], v[190:193], v[32:35]
	v_mfma_f32_16x16x32_bf16 v[92:95], v[154:157], v[186:189], v[92:95]
	s_waitcnt lgkmcnt(0)
	v_mfma_f32_16x16x32_bf16 v[64:67], v[154:157], v[194:197], v[64:67]
	v_mfma_f32_16x16x32_bf16 v[84:87], v[162:165], v[186:189], v[84:87]
	v_mfma_f32_16x16x32_bf16 v[48:51], v[162:165], v[194:197], v[48:51]
	v_mfma_f32_16x16x32_bf16 v[76:79], v[170:173], v[186:189], v[76:79]
	v_mfma_f32_16x16x32_bf16 v[40:43], v[170:173], v[194:197], v[40:43]
	v_mfma_f32_16x16x32_bf16 v[60:63], v[178:181], v[186:189], v[60:63]
	v_mfma_f32_16x16x32_bf16 v[32:35], v[178:181], v[194:197], v[32:35]
	s_setprio 0
	s_mov_b32 m0, s28
	s_barrier
	ds_read_b128 v[150:153], v133 offset:49152
	ds_read_b128 v[154:157], v133 offset:50176
	ds_read_b128 v[158:161], v133 offset:51200
	ds_read_b128 v[162:165], v133 offset:52224
	ds_read_b128 v[166:169], v133 offset:53248
	ds_read_b128 v[170:173], v133 offset:54272
	ds_read_b128 v[174:177], v133 offset:55296
	ds_read_b128 v[178:181], v133 offset:56320
	buffer_load_dwordx4 v130, s[72:75], s45 offen lds
	s_mov_b32 m0, s29
	s_nop 0
	buffer_load_dwordx4 v131, s[72:75], s45 offen lds
	s_barrier
	s_setprio 1
	s_waitcnt lgkmcnt(7)
	v_mfma_f32_16x16x32_bf16 v[88:91], v[150:153], v[134:137], v[88:91]
	v_mfma_f32_16x16x32_bf16 v[72:75], v[150:153], v[142:145], v[72:75]
	s_waitcnt lgkmcnt(5)
	v_mfma_f32_16x16x32_bf16 v[80:83], v[158:161], v[134:137], v[80:83]
	v_mfma_f32_16x16x32_bf16 v[56:59], v[158:161], v[142:145], v[56:59]
	s_waitcnt lgkmcnt(3)
	v_mfma_f32_16x16x32_bf16 v[68:71], v[166:169], v[134:137], v[68:71]
	v_mfma_f32_16x16x32_bf16 v[44:47], v[166:169], v[142:145], v[44:47]
	s_waitcnt lgkmcnt(1)
	v_mfma_f32_16x16x32_bf16 v[52:55], v[174:177], v[134:137], v[52:55]
	v_mfma_f32_16x16x32_bf16 v[36:39], v[174:177], v[142:145], v[36:39]
	v_mfma_f32_16x16x32_bf16 v[88:91], v[154:157], v[138:141], v[88:91]
	v_mfma_f32_16x16x32_bf16 v[72:75], v[154:157], v[146:149], v[72:75]
	v_mfma_f32_16x16x32_bf16 v[80:83], v[162:165], v[138:141], v[80:83]
	v_mfma_f32_16x16x32_bf16 v[56:59], v[162:165], v[146:149], v[56:59]
	v_mfma_f32_16x16x32_bf16 v[68:71], v[170:173], v[138:141], v[68:71]
	v_mfma_f32_16x16x32_bf16 v[44:47], v[170:173], v[146:149], v[44:47]
	s_waitcnt lgkmcnt(0)
	v_mfma_f32_16x16x32_bf16 v[52:55], v[178:181], v[138:141], v[52:55]
	v_mfma_f32_16x16x32_bf16 v[36:39], v[178:181], v[146:149], v[36:39]
	s_setprio 0
	s_barrier
	s_add_i32 s44, s44, 0x80080
	s_mov_b32 m0, s30
	s_nop 0
	buffer_load_dwordx4 v130, s[8:11], s44 offen lds
	s_mov_b32 m0, s31
	s_nop 0
	buffer_load_dwordx4 v131, s[8:11], s44 offen lds
	s_waitcnt vmcnt(6)
	s_barrier
	s_setprio 1
	v_mfma_f32_16x16x32_bf16 v[28:31], v[150:153], v[182:185], v[28:31]
	v_mfma_f32_16x16x32_bf16 v[16:19], v[150:153], v[190:193], v[16:19]
	v_mfma_f32_16x16x32_bf16 v[24:27], v[158:161], v[182:185], v[24:27]
	v_mfma_f32_16x16x32_bf16 v[8:11], v[158:161], v[190:193], v[8:11]
	v_mfma_f32_16x16x32_bf16 v[20:23], v[166:169], v[182:185], v[20:23]
	v_mfma_f32_16x16x32_bf16 v[4:7], v[166:169], v[190:193], v[4:7]
	v_mfma_f32_16x16x32_bf16 v[12:15], v[174:177], v[182:185], v[12:15]
	v_mfma_f32_16x16x32_bf16 v[0:3], v[174:177], v[190:193], v[0:3]
	v_mfma_f32_16x16x32_bf16 v[28:31], v[154:157], v[186:189], v[28:31]
	v_mfma_f32_16x16x32_bf16 v[16:19], v[154:157], v[194:197], v[16:19]
	v_mfma_f32_16x16x32_bf16 v[24:27], v[162:165], v[186:189], v[24:27]
	v_mfma_f32_16x16x32_bf16 v[8:11], v[162:165], v[194:197], v[8:11]
	v_mfma_f32_16x16x32_bf16 v[20:23], v[170:173], v[186:189], v[20:23]
	v_mfma_f32_16x16x32_bf16 v[4:7], v[170:173], v[194:197], v[4:7]
	v_mfma_f32_16x16x32_bf16 v[12:15], v[178:181], v[186:189], v[12:15]
	v_mfma_f32_16x16x32_bf16 v[0:3], v[178:181], v[194:197], v[0:3]
	s_setprio 0
	s_add_i32 s43, s43, 2
	s_addk_i32 s41, 0x100
	s_addk_i32 s42, 0x100
	s_cmp_gt_u32 s43, 29
	s_barrier
	s_cbranch_scc0 .LBB0_1639
	s_getreg_b32 s10, hwreg(HW_REG_HW_ID, 0, 6)
	s_and_b32 s10, s10, 63
	s_lshl_b32 s10, s10, 2
	s_add_i32 s10, s10, 0
	s_add_i32 s10, s10, 0x20010
	v_mov_b32_e32 v96, s10
	ds_read_b32 v96, v96
	s_mul_i32 s10, s34, 0x120
	s_lshl_b32 s11, s37, 2
	v_mbcnt_lo_u32_b32 v136, -1, 0
	v_mbcnt_hi_u32_b32 v136, -1, v136
	s_add_i32 s11, s11, s10
	s_waitcnt lgkmcnt(0)
	v_readfirstlane_b32 s34, v96
	v_and_b32_e32 v137, 15, v136
	s_mov_b32 s10, 0x21000
	v_lshl_or_b32 v96, s34, 6, v136
	v_ashrrev_i32_e32 v134, 8, v96
	v_add_u32_e32 v134, s11, v134
	v_ashrrev_i32_e32 v135, 31, v134
	v_lshrrev_b32_e32 v96, 1, v96
	v_lshlrev_b64 v[134:135], 8, v[134:135]
	v_and_b32_e32 v96, 0x60, v96
	v_or3_b32 v134, v134, v96, v137
	v_lshlrev_b64 v[134:135], 8, v[134:135]
	v_lshl_add_u64 v[134:135], s[12:13], 0, v[134:135]
	v_and_b32_e32 v96, 48, v136
	v_lshl_add_u64 v[134:135], v[134:135], 0, v[96:97]
	global_store_dwordx4 v[134:135], v[126:129], off
	global_store_dwordx4 v[134:135], v[122:125], off offset:64
	global_store_dwordx4 v[134:135], v[118:121], off offset:128
	global_store_dwordx4 v[134:135], v[110:113], off offset:192
	s_mov_b32 s34, s14
	s_mov_b32 s37, s15
	v_add_co_u32_e32 v110, vcc, s75, v134
	s_mov_b32 s42, s17
	s_nop 0
	v_addc_co_u32_e32 v111, vcc, 0, v135, vcc
	v_add_co_u32_e32 v112, vcc, s10, v134
	s_mov_b64 s[10:11], 0x1000
	s_nop 0
	v_addc_co_u32_e32 v113, vcc, 0, v135, vcc
	global_store_dwordx4 v[112:113], v[88:91], off offset:-4096
	global_store_dwordx4 v[110:111], v[80:83], off offset:64
	global_store_dwordx4 v[110:111], v[68:71], off offset:128
	global_store_dwordx4 v[110:111], v[52:55], off offset:192
	s_mov_b32 s41, s16
	s_nop 0
	v_add_co_u32_e32 v54, vcc, s63, v134
	v_lshl_add_u64 v[52:53], v[134:135], 0, s[10:11]
	s_nop 0
	v_addc_co_u32_e32 v55, vcc, 0, v135, vcc
	s_mov_b64 s[10:11], 0x8000
	global_store_dwordx4 v[54:55], v[114:117], off
	global_store_dwordx4 v[52:53], v[106:109], off offset:64
	global_store_dwordx4 v[52:53], v[102:105], off offset:128
	global_store_dwordx4 v[52:53], v[98:101], off offset:192
	global_store_dwordx4 v[112:113], v[72:75], off
	global_store_dwordx4 v[112:113], v[56:59], off offset:64
	global_store_dwordx4 v[112:113], v[44:47], off offset:128
	global_store_dwordx4 v[112:113], v[36:39], off offset:192
	s_nop 1
	v_lshl_add_u64 v[36:37], v[134:135], 0, s[10:11]
	s_mov_b32 s10, 0x8000
	v_add_co_u32_e32 v38, vcc, s10, v134
	s_mov_b32 s10, 0x28000
	s_nop 0
	v_addc_co_u32_e32 v39, vcc, 0, v135, vcc
	global_store_dwordx4 v[38:39], v[92:95], off
	global_store_dwordx4 v[36:37], v[84:87], off offset:64
	global_store_dwordx4 v[36:37], v[76:79], off offset:128
	global_store_dwordx4 v[36:37], v[60:63], off offset:192
	v_add_co_u32_e32 v36, vcc, s10, v134
	s_mov_b64 s[10:11], 0x9000
	s_nop 0
	v_addc_co_u32_e32 v37, vcc, 0, v135, vcc
	global_store_dwordx4 v[36:37], v[28:31], off
	global_store_dwordx4 v[36:37], v[24:27], off offset:64
	global_store_dwordx4 v[36:37], v[20:23], off offset:128
	global_store_dwordx4 v[36:37], v[12:15], off offset:192
	s_nop 1
	v_add_co_u32_e32 v14, vcc, 0x9000, v134
	v_lshl_add_u64 v[12:13], v[134:135], 0, s[10:11]
	s_nop 0
	v_addc_co_u32_e32 v15, vcc, 0, v135, vcc
	global_store_dwordx4 v[14:15], v[64:67], off
	global_store_dwordx4 v[12:13], v[48:51], off offset:64
	global_store_dwordx4 v[12:13], v[40:43], off offset:128
	global_store_dwordx4 v[12:13], v[32:35], off offset:192
	v_add_co_u32_e32 v12, vcc, 0x29000, v134
	s_nop 1
	v_addc_co_u32_e32 v13, vcc, 0, v135, vcc
	s_and_b64 vcc, exec, s[4:5]
	global_store_dwordx4 v[12:13], v[16:19], off
	global_store_dwordx4 v[12:13], v[8:11], off offset:64
	global_store_dwordx4 v[12:13], v[4:7], off offset:128
	global_store_dwordx4 v[12:13], v[0:3], off offset:192
	s_cbranch_vccz .LBB0_1633
	s_branch .LBB0_1642
